# P7/P17 epilogue gate and aux loads (last use) tagged nt
# baseline (speedup 1.0000x reference)
; __device__ __forceinline__ float sigmoidf_(float x) { return __builtin_amdgcn_rcpf(1.f + __builtin_amdgcn_exp2f(-1.4426950408889634f * x)); }
;     __device__ __forceinline__ void operator()(const f32x4 (&acc)[2][2][4][2], const Unit& u, int wr, int wc, int fr, int fq) const {
;     ...
;         if (QI8) {
; #pragma unroll
;             for (int ai = 0; ai < 2; ++ai)
; #pragma unroll
;                 for (int m = 0; m < 4; ++m) ra[ai][m] = sa[row0 + ai * HALF + m * 16];
; #pragma unroll
;             for (int bj = 0; bj < 2; ++bj) { cb[bj][0] = *(const f32x4*)(sb + col0 + bj * HALF) * tsc; cb[bj][1] = *(const f32x4*)(sb + col0 + bj * HALF + 4) * tsc; } }
;         else if (MODE == 1) {
; #pragma unroll
;             for (int bj = 0; bj < 2; ++bj) { cb[bj][0] = *(const f32x4*)(colscale + col0 + bj * HALF); cb[bj][1] = *(const f32x4*)(colscale + col0 + bj * HALF + 4); } }
;         const bool dual = (MODE == 0) && aux != nullptr && u.pn >= ZC_KV / 256 && u.pn < ZC_KV / 256 + 4;
;         u32x4 gq[2][2], aq[2][2]; f32x4 rs[2][2][2];
;     ...
;         EPB_LOAD(0);
; #pragma unroll
;         for (int kb = 0; kb < 8; ++kb) { const int ai = kb >> 2, m = kb & 3;
;             if (kb < 7) EPB_LOAD(kb + 1);
;             { const int row = row0 + ai * HALF + m * 16; float rmx = 0.f;
; #pragma unroll
;                 for (int bj = 0; bj < 2; ++bj) { const int col = col0 + bj * HALF; f32x4 v0 = acc[ai][bj][m][0], v1 = acc[ai][bj][m][1];
;                     if (QI8) { const f32x4 c0 = cb[bj][0] * ra[ai][m], c1 = cb[bj][1] * ra[ai][m]; const i32x4 i0 = __builtin_bit_cast(i32x4, v0), i1 = __builtin_bit_cast(i32x4, v1);
;                         v0 = (f32x4){(float)i0[0], (float)i0[1], (float)i0[2], (float)i0[3]} * c0; v1 = (f32x4){(float)i1[0], (float)i1[1], (float)i1[2], (float)i1[3]} * c1; }
;                     else if (MODE == 0) { v0 = v0 * tsc; v1 = v1 * tsc; }
;                     if (!QI8 && MODE == 1) { v0 = v0 * cb[bj][0]; v1 = v1 * cb[bj][1]; }
;                     if (MODE == 2 || MODE == 3) { const u32x4 g = gq[kb & 1][bj];
;                         f32x4 g0 = {sigmoidf_(bflo(g.x)), sigmoidf_(bfhi(g.x)), sigmoidf_(bflo(g.y)), sigmoidf_(bfhi(g.y))};
;                         f32x4 g1 = {sigmoidf_(bflo(g.z)), sigmoidf_(bfhi(g.z)), sigmoidf_(bflo(g.w)), sigmoidf_(bfhi(g.w))};
;                         v0 = v0 * g0; v1 = v1 * g1;
.LBB0_1003:
	v_lshl_or_b32 v70, s66, 8, v231
	v_lshl_add_u32 v152, s30, 8, v229
	v_ashrrev_i32_e32 v71, 31, v70
	v_mov_b64_e32 v[154:155], s[14:15]
	v_ashrrev_i32_e32 v153, 31, v152
	v_mad_i64_i32 v[144:145], s[34:35], v152, s64, v[154:155]
	v_lshlrev_b64 v[146:147], 1, v[70:71]
	v_lshl_add_u64 v[142:143], v[152:153], 2, s[10:11]
	v_lshl_add_u64 v[72:73], v[70:71], 2, s[12:13]
	v_lshl_add_u64 v[144:145], v[144:145], 0, v[146:147]
	global_load_dword v178, v[142:143], off
	global_load_dwordx4 v[78:81], v[72:73], off
	global_load_dwordx4 v[74:77], v[72:73], off offset:16
	global_load_dwordx4 v[170:173], v[144:145], off nt
	v_cvt_f32_i32_e32 v181, v69
	v_cvt_f32_i32_e32 v180, v68
	v_cvt_f32_i32_e32 v183, v67
	v_cvt_f32_i32_e32 v182, v66
	global_load_dwordx4 v[66:69], v[72:73], off offset:528
	s_nop 0
	global_load_dwordx4 v[70:73], v[72:73], off offset:512
	s_nop 0
	global_load_dwordx4 v[174:177], v[144:145], off offset:256 nt
	global_load_dword v166, v[142:143], off offset:64
	global_load_dword v164, v[142:143], off offset:128
	global_load_dword v162, v[142:143], off offset:192
	global_load_dword v158, v[142:143], off offset:512
	global_load_dword v156, v[142:143], off offset:576
	global_load_dword v150, v[142:143], off offset:640
	global_load_dword v148, v[142:143], off offset:704
	v_or_b32_e32 v168, 16, v152
	v_cvt_f32_i32_e32 v187, v139
	v_cvt_f32_i32_e32 v186, v138
	v_mad_i64_i32 v[138:139], s[34:35], v168, s64, v[154:155]
	v_lshl_add_u64 v[138:139], v[138:139], 0, v[146:147]
	v_cvt_f32_i32_e32 v185, v141
	v_cvt_f32_i32_e32 v184, v140
	global_load_dwordx4 v[142:145], v[138:139], off nt
	s_nop 0
	global_load_dwordx4 v[138:141], v[138:139], off offset:256 nt
	v_cvt_f32_i32_e32 v137, v137
	v_cvt_f32_i32_e32 v136, v136
	v_cvt_f32_i32_e32 v135, v135
	v_cvt_f32_i32_e32 v134, v134
	v_cvt_f32_i32_e32 v133, v133
	v_cvt_f32_i32_e32 v132, v132
	v_cvt_f32_i32_e32 v131, v131
	v_cvt_f32_i32_e32 v130, v130
	v_cvt_f32_i32_e32 v129, v129
	v_cvt_f32_i32_e32 v128, v128
	v_cvt_f32_i32_e32 v127, v127
	v_cvt_f32_i32_e32 v126, v126
	v_cvt_f32_i32_e32 v125, v125
	v_cvt_f32_i32_e32 v124, v124
	v_cvt_f32_i32_e32 v123, v123
	v_cvt_f32_i32_e32 v122, v122
	v_ashrrev_i32_e32 v169, 31, v168
	v_cvt_f32_i32_e32 v119, v119
	v_cvt_f32_i32_e32 v118, v118
	v_cvt_f32_i32_e32 v121, v121
	v_cvt_f32_i32_e32 v120, v120
	v_cvt_f32_i32_e32 v117, v117
	v_cvt_f32_i32_e32 v116, v116
	v_cvt_f32_i32_e32 v115, v115
	v_cvt_f32_i32_e32 v114, v114
	v_cvt_f32_i32_e32 v111, v111
	v_cvt_f32_i32_e32 v110, v110
	v_cvt_f32_i32_e32 v113, v113
	v_cvt_f32_i32_e32 v112, v112
	v_cvt_f32_i32_e32 v109, v109
	v_cvt_f32_i32_e32 v108, v108
	v_cvt_f32_i32_e32 v107, v107
	v_cvt_f32_i32_e32 v106, v106
	v_cvt_f32_i32_e32 v103, v103
	v_cvt_f32_i32_e32 v102, v102
	v_cvt_f32_i32_e32 v105, v105
	v_cvt_f32_i32_e32 v104, v104
	v_cvt_f32_i32_e32 v101, v101
	v_cvt_f32_i32_e32 v100, v100
	v_cvt_f32_i32_e32 v99, v99
	v_cvt_f32_i32_e32 v98, v98
	v_add_u32_e32 v160, 0x80, v152
	v_cvt_f32_i32_e32 v95, v95
	v_cvt_f32_i32_e32 v94, v94
	v_cvt_f32_i32_e32 v97, v97
	v_cvt_f32_i32_e32 v96, v96
	v_cvt_f32_i32_e32 v93, v93
	v_cvt_f32_i32_e32 v92, v92
	v_cvt_f32_i32_e32 v91, v91
	v_cvt_f32_i32_e32 v90, v90
	v_cvt_f32_i32_e32 v87, v87
	v_cvt_f32_i32_e32 v86, v86
	v_cvt_f32_i32_e32 v89, v89
	v_cvt_f32_i32_e32 v88, v88
	v_cvt_f32_i32_e32 v85, v85
	v_cvt_f32_i32_e32 v84, v84
	v_cvt_f32_i32_e32 v83, v83
	v_cvt_f32_i32_e32 v82, v82
	v_cvt_f32_i32_e32 v63, v63
	v_cvt_f32_i32_e32 v62, v62
	v_cvt_f32_i32_e32 v65, v65
	v_cvt_f32_i32_e32 v64, v64
	s_waitcnt vmcnt(0)
	v_pk_mul_f32 v[188:189], v[178:179], v[80:81] op_sel_hi:[0,1]
	v_pk_mul_f32 v[190:191], v[178:179], v[78:79] op_sel_hi:[0,1]
	v_lshlrev_b32_e32 v149, 16, v170
	v_and_b32_e32 v151, 0xffff0000, v170
	v_lshlrev_b32_e32 v157, 16, v171
	v_and_b32_e32 v159, 0xffff0000, v171
	v_lshlrev_b32_e32 v167, 16, v173
	v_and_b32_e32 v170, 0xffff0000, v173
	v_lshlrev_b32_e32 v163, 16, v172
	v_and_b32_e32 v165, 0xffff0000, v172
	v_mul_f32_e32 v149, 0xbfb8aa3b, v149
	v_mul_f32_e32 v151, 0xbfb8aa3b, v151
	v_mul_f32_e32 v157, 0xbfb8aa3b, v157
	v_mul_f32_e32 v159, 0xbfb8aa3b, v159
	v_mul_f32_e32 v167, 0xbfb8aa3b, v167
	v_mul_f32_e32 v170, 0xbfb8aa3b, v170
	v_mul_f32_e32 v163, 0xbfb8aa3b, v163
	v_mul_f32_e32 v165, 0xbfb8aa3b, v165
	v_exp_f32_e32 v149, v149
	v_exp_f32_e32 v151, v151
	v_exp_f32_e32 v157, v157
	v_exp_f32_e32 v159, v159
	v_exp_f32_e32 v167, v167
	v_exp_f32_e32 v170, v170
	v_exp_f32_e32 v163, v163
	v_exp_f32_e32 v165, v165
	v_pk_mul_f32 v[192:193], v[178:179], v[76:77] op_sel_hi:[0,1]
	v_pk_mul_f32 v[212:213], v[178:179], v[74:75] op_sel_hi:[0,1]
	v_add_f32_e32 v149, 1.0, v149
	v_add_f32_e32 v151, 1.0, v151
	v_add_f32_e32 v157, 1.0, v157
	v_add_f32_e32 v159, 1.0, v159
	v_add_f32_e32 v167, 1.0, v167
	v_add_f32_e32 v179, 1.0, v170
	v_pk_mul_f32 v[182:183], v[190:191], v[182:183]
	v_add_f32_e32 v163, 1.0, v163
	v_add_f32_e32 v165, 1.0, v165
	v_rcp_f32_e32 v170, v149
	v_rcp_f32_e32 v171, v151
	v_rcp_f32_e32 v172, v157
	v_rcp_f32_e32 v173, v159
	v_rcp_f32_e32 v190, v167
	v_rcp_f32_e32 v191, v179
	v_pk_mul_f32 v[180:181], v[188:189], v[180:181]
	v_rcp_f32_e32 v188, v163
	v_rcp_f32_e32 v189, v165
	v_pk_mul_f32 v[184:185], v[192:193], v[184:185]
	v_lshlrev_b32_e32 v149, 16, v174
	v_pk_mul_f32 v[186:187], v[212:213], v[186:187]
	v_pk_mul_f32 v[172:173], v[180:181], v[172:173]
	v_pk_mul_f32 v[170:171], v[182:183], v[170:171]
	v_pk_mul_f32 v[180:181], v[184:185], v[190:191]
	v_mul_f32_e32 v149, 0xbfb8aa3b, v149
	v_and_b32_e32 v151, 0xffff0000, v174
	v_pk_mul_f32 v[182:183], v[186:187], v[188:189]
	v_cvt_pk_bf16_f32 v170, v170, v171
	v_cvt_pk_bf16_f32 v171, v172, v173
	v_exp_f32_e32 v149, v149
;     __device__ __forceinline__ void operator()(const f32x4 (&acc)[2][2][4][2], const Unit& u, int wr, int wc, int fr, int fq) const {
;     ...
;         EPB_LOAD(0);
; #pragma unroll
;         for (int kb = 0; kb < 8; ++kb) { const int ai = kb >> 2, m = kb & 3;
;             if (kb < 7) EPB_LOAD(kb + 1);
;             { const int row = row0 + ai * HALF + m * 16; float rmx = 0.f;
; #pragma unroll
;                 for (int bj = 0; bj < 2; ++bj) { const int col = col0 + bj * HALF; f32x4 v0 = acc[ai][bj][m][0], v1 = acc[ai][bj][m][1];
;                     if (QI8) { const f32x4 c0 = cb[bj][0] * ra[ai][m], c1 = cb[bj][1] * ra[ai][m]; const i32x4 i0 = __builtin_bit_cast(i32x4, v0), i1 = __builtin_bit_cast(i32x4, v1);
;                         v0 = (f32x4){(float)i0[0], (float)i0[1], (float)i0[2], (float)i0[3]} * c0; v1 = (f32x4){(float)i1[0], (float)i1[1], (float)i1[2], (float)i1[3]} * c1; }
;                     else if (MODE == 0) { v0 = v0 * tsc; v1 = v1 * tsc; }
;                     if (!QI8 && MODE == 1) { v0 = v0 * cb[bj][0]; v1 = v1 * cb[bj][1]; }
;                     if (MODE == 2 || MODE == 3) { const u32x4 g = gq[kb & 1][bj];
;                         f32x4 g0 = {sigmoidf_(bflo(g.x)), sigmoidf_(bfhi(g.x)), sigmoidf_(bflo(g.y)), sigmoidf_(bfhi(g.y))};
;                         f32x4 g1 = {sigmoidf_(bflo(g.z)), sigmoidf_(bfhi(g.z)), sigmoidf_(bflo(g.w)), sigmoidf_(bfhi(g.w))};
;                         v0 = v0 * g0; v1 = v1 * g1;
;                         if (MODE == 3) { const u32x4 q = aq[kb & 1][bj];
;                             v0 = v0 + (f32x4){bflo(q.x), bfhi(q.x), bflo(q.y), bfhi(q.y)}; v1 = v1 + (f32x4){bflo(q.z), bfhi(q.z), bflo(q.w), bfhi(q.w)}; } }
;                     if (MODE == 4) { v0 = v0 + rs[kb & 1][bj][0]; v1 = v1 + rs[kb & 1][bj][1]; }
;                     if (MODE == 5) { const u32x4 c = gq[kb & 1][bj], q = aq[kb & 1][bj];
;                         v0 = (f32x4){bflo(c.x) + sigmoidf_(v0[0]) * bflo(q.x), bfhi(c.x) + sigmoidf_(v0[1]) * bfhi(q.x), bflo(c.y) + sigmoidf_(v0[2]) * bflo(q.y), bfhi(c.y) + sigmoidf_(v0[3]) * bfhi(q.y)};
;                         v1 = (f32x4){bflo(c.z) + sigmoidf_(v1[0]) * bflo(q.z), bfhi(c.z) + sigmoidf_(v1[1]) * bfhi(q.z), bflo(c.w) + sigmoidf_(v1[2]) * bflo(q.w), bfhi(c.w) + sigmoidf_(v1[3]) * bfhi(q.w)}; }
	v_cvt_pk_bf16_f32 v172, v182, v183
	v_cvt_pk_bf16_f32 v173, v180, v181
	v_lshlrev_b64 v[180:181], 13, v[152:153]
	v_mul_f32_e32 v151, 0xbfb8aa3b, v151
	v_lshlrev_b32_e32 v153, 16, v175
	v_exp_f32_e32 v151, v151
	v_mul_f32_e32 v153, 0xbfb8aa3b, v153
	v_lshl_add_u64 v[180:181], s[0:1], 0, v[180:181]
	v_exp_f32_e32 v153, v153
	v_lshl_add_u64 v[180:181], v[180:181], 0, v[146:147]
	global_store_dwordx4 v[180:181], v[170:173], off
	v_add_f32_e32 v149, 1.0, v149
	v_pk_mul_f32 v[182:183], v[178:179], v[68:69] op_sel_hi:[0,1]
	v_pk_mul_f32 v[170:171], v[178:179], v[72:73] op_sel_hi:[0,1]
	v_pk_mul_f32 v[136:137], v[170:171], v[136:137]
	v_rcp_f32_e32 v170, v149
	v_add_f32_e32 v149, 1.0, v151
	v_and_b32_e32 v151, 0xffff0000, v175
	v_rcp_f32_e32 v171, v149
	v_add_f32_e32 v149, 1.0, v153
	v_mul_f32_e32 v151, 0xbfb8aa3b, v151
	v_lshlrev_b32_e32 v153, 16, v176
	v_exp_f32_e32 v151, v151
	v_mul_f32_e32 v153, 0xbfb8aa3b, v153
	v_exp_f32_e32 v153, v153
	v_pk_mul_f32 v[172:173], v[178:179], v[70:71] op_sel_hi:[0,1]
	v_pk_mul_f32 v[134:135], v[172:173], v[134:135]
	v_rcp_f32_e32 v172, v149
	v_add_f32_e32 v149, 1.0, v151
	v_rcp_f32_e32 v173, v149
	v_add_f32_e32 v149, 1.0, v153
	v_lshlrev_b32_e32 v151, 16, v177
	v_rcp_f32_e32 v174, v149
	v_and_b32_e32 v149, 0xffff0000, v176
	v_mul_f32_e32 v151, 0xbfb8aa3b, v151
	v_and_b32_e32 v153, 0xffff0000, v177
	v_mul_f32_e32 v149, 0xbfb8aa3b, v149
	v_exp_f32_e32 v151, v151
	v_mul_f32_e32 v153, 0xbfb8aa3b, v153
	v_exp_f32_e32 v149, v149
	v_exp_f32_e32 v153, v153
	v_add_f32_e32 v151, 1.0, v151
	v_rcp_f32_e32 v176, v151
	v_add_f32_e32 v149, 1.0, v149
	v_add_f32_e32 v151, 1.0, v153
	v_rcp_f32_e32 v177, v151
	v_rcp_f32_e32 v175, v149
	v_lshlrev_b32_e32 v149, 16, v142
	v_mul_f32_e32 v149, 0xbfb8aa3b, v149
	v_pk_mul_f32 v[178:179], v[178:179], v[66:67] op_sel_hi:[0,1]
	v_exp_f32_e32 v149, v149
	v_pk_mul_f32 v[130:131], v[178:179], v[130:131]
	v_pk_mul_f32 v[132:133], v[182:183], v[132:133]
	v_pk_mul_f32 v[134:135], v[134:135], v[170:171]
	v_pk_mul_f32 v[170:171], v[132:133], v[176:177]
	v_pk_mul_f32 v[132:133], v[130:131], v[174:175]
	v_pk_mul_f32 v[136:137], v[136:137], v[172:173]
	v_cvt_pk_bf16_f32 v130, v134, v135
	v_pk_mul_f32 v[172:173], v[166:167], v[80:81] op_sel_hi:[0,1]
	v_cvt_pk_bf16_f32 v131, v136, v137
	v_cvt_pk_bf16_f32 v132, v132, v133
	v_cvt_pk_bf16_f32 v133, v170, v171
	v_or_b32_e32 v170, 32, v152
	global_store_dwordx4 v[180:181], v[130:133], off offset:256
	v_add_f32_e32 v149, 1.0, v149
	v_pk_mul_f32 v[128:129], v[172:173], v[128:129]
	v_mad_i64_i32 v[130:131], s[34:35], v170, s64, v[154:155]
	v_lshl_add_u64 v[130:131], v[130:131], 0, v[146:147]
	v_rcp_f32_e32 v172, v149
	v_lshlrev_b32_e32 v149, 16, v144
	global_load_dwordx4 v[134:137], v[130:131], off nt
	s_nop 0
	global_load_dwordx4 v[130:133], v[130:131], off offset:256 nt
	v_mul_f32_e32 v149, 0xbfb8aa3b, v149
	v_exp_f32_e32 v149, v149
	v_pk_mul_f32 v[174:175], v[166:167], v[78:79] op_sel_hi:[0,1]
	v_and_b32_e32 v142, 0xffff0000, v142
	v_pk_mul_f32 v[126:127], v[174:175], v[126:127]
	v_add_f32_e32 v149, 1.0, v149
	v_mul_f32_e32 v142, 0xbfb8aa3b, v142
	v_lshlrev_b32_e32 v151, 16, v143
	v_and_b32_e32 v143, 0xffff0000, v143
	v_rcp_f32_e32 v174, v149
	v_and_b32_e32 v144, 0xffff0000, v144
	v_lshlrev_b32_e32 v149, 16, v145
	v_and_b32_e32 v145, 0xffff0000, v145
	v_exp_f32_e32 v142, v142
	v_mul_f32_e32 v151, 0xbfb8aa3b, v151
	v_mul_f32_e32 v143, 0xbfb8aa3b, v143
	v_mul_f32_e32 v144, 0xbfb8aa3b, v144
	v_mul_f32_e32 v149, 0xbfb8aa3b, v149
	v_mul_f32_e32 v145, 0xbfb8aa3b, v145
	v_exp_f32_e32 v151, v151
	v_exp_f32_e32 v143, v143
	v_exp_f32_e32 v144, v144
	v_exp_f32_e32 v149, v149
	v_exp_f32_e32 v145, v145
	v_add_f32_e32 v142, 1.0, v142
	v_rcp_f32_e32 v173, v142
	v_add_f32_e32 v142, 1.0, v151
	v_add_f32_e32 v143, 1.0, v143
	v_add_f32_e32 v151, 1.0, v144
	v_add_f32_e32 v144, 1.0, v149
	v_add_f32_e32 v145, 1.0, v145
	v_rcp_f32_e32 v142, v142
	v_rcp_f32_e32 v143, v143
	v_rcp_f32_e32 v144, v144
	v_rcp_f32_e32 v145, v145
	v_rcp_f32_e32 v175, v151
	v_pk_mul_f32 v[176:177], v[166:167], v[76:77] op_sel_hi:[0,1]
	v_pk_mul_f32 v[178:179], v[166:167], v[74:75] op_sel_hi:[0,1]
	v_pk_mul_f32 v[122:123], v[178:179], v[122:123]
	v_pk_mul_f32 v[124:125], v[176:177], v[124:125]
	v_pk_mul_f32 v[126:127], v[126:127], v[172:173]
	v_pk_mul_f32 v[128:129], v[128:129], v[142:143]
	v_pk_mul_f32 v[142:143], v[124:125], v[144:145]
	v_pk_mul_f32 v[124:125], v[122:123], v[174:175]
	v_cvt_pk_bf16_f32 v122, v126, v127
	v_lshlrev_b64 v[126:127], 13, v[168:169]
	v_lshl_add_u64 v[126:127], s[0:1], 0, v[126:127]
	v_cvt_pk_bf16_f32 v123, v128, v129
	v_cvt_pk_bf16_f32 v124, v124, v125
	v_cvt_pk_bf16_f32 v125, v142, v143
	v_lshl_add_u64 v[126:127], v[126:127], 0, v[146:147]
	global_store_dwordx4 v[126:127], v[122:125], off
	v_pk_mul_f32 v[128:129], v[166:167], v[68:69] op_sel_hi:[0,1]
	v_pk_mul_f32 v[116:117], v[128:129], v[116:117]
	v_pk_mul_f32 v[124:125], v[166:167], v[70:71] op_sel_hi:[0,1]
	v_pk_mul_f32 v[118:119], v[124:125], v[118:119]
	v_lshlrev_b32_e32 v124, 16, v138
	v_mul_f32_e32 v124, 0xbfb8aa3b, v124
	v_exp_f32_e32 v124, v124
	v_pk_mul_f32 v[122:123], v[166:167], v[72:73] op_sel_hi:[0,1]
	v_pk_mul_f32 v[120:121], v[122:123], v[120:121]
	v_and_b32_e32 v123, 0xffff0000, v138
	v_add_f32_e32 v122, 1.0, v124
	v_lshlrev_b32_e32 v124, 16, v139
	v_and_b32_e32 v125, 0xffff0000, v139
	v_lshlrev_b32_e32 v128, 16, v140
	v_and_b32_e32 v129, 0xffff0000, v140
	v_lshlrev_b32_e32 v138, 16, v141
	v_and_b32_e32 v139, 0xffff0000, v141
	v_mul_f32_e32 v123, 0xbfb8aa3b, v123
	v_mul_f32_e32 v128, 0xbfb8aa3b, v128
	v_mul_f32_e32 v129, 0xbfb8aa3b, v129
	v_mul_f32_e32 v138, 0xbfb8aa3b, v138
	v_mul_f32_e32 v139, 0xbfb8aa3b, v139
;     __device__ __forceinline__ void operator()(const f32x4 (&acc)[2][2][4][2], const Unit& u, int wr, int wc, int fr, int fq) const {
;     ...
;         EPB_LOAD(0);
; #pragma unroll
;         for (int kb = 0; kb < 8; ++kb) { const int ai = kb >> 2, m = kb & 3;
;             if (kb < 7) EPB_LOAD(kb + 1);
;             { const int row = row0 + ai * HALF + m * 16; float rmx = 0.f;
; #pragma unroll
;                 for (int bj = 0; bj < 2; ++bj) { const int col = col0 + bj * HALF; f32x4 v0 = acc[ai][bj][m][0], v1 = acc[ai][bj][m][1];
;                     if (QI8) { const f32x4 c0 = cb[bj][0] * ra[ai][m], c1 = cb[bj][1] * ra[ai][m]; const i32x4 i0 = __builtin_bit_cast(i32x4, v0), i1 = __builtin_bit_cast(i32x4, v1);
;                         v0 = (f32x4){(float)i0[0], (float)i0[1], (float)i0[2], (float)i0[3]} * c0; v1 = (f32x4){(float)i1[0], (float)i1[1], (float)i1[2], (float)i1[3]} * c1; }
;                     else if (MODE == 0) { v0 = v0 * tsc; v1 = v1 * tsc; }
;                     if (!QI8 && MODE == 1) { v0 = v0 * cb[bj][0]; v1 = v1 * cb[bj][1]; }
;                     if (MODE == 2 || MODE == 3) { const u32x4 g = gq[kb & 1][bj];
;                         f32x4 g0 = {sigmoidf_(bflo(g.x)), sigmoidf_(bfhi(g.x)), sigmoidf_(bflo(g.y)), sigmoidf_(bfhi(g.y))};
;                         f32x4 g1 = {sigmoidf_(bflo(g.z)), sigmoidf_(bfhi(g.z)), sigmoidf_(bflo(g.w)), sigmoidf_(bfhi(g.w))};
;                         v0 = v0 * g0; v1 = v1 * g1;
;                         if (MODE == 3) { const u32x4 q = aq[kb & 1][bj];
;                             v0 = v0 + (f32x4){bflo(q.x), bfhi(q.x), bflo(q.y), bfhi(q.y)}; v1 = v1 + (f32x4){bflo(q.z), bfhi(q.z), bflo(q.w), bfhi(q.w)}; } }
;                     if (MODE == 4) { v0 = v0 + rs[kb & 1][bj][0]; v1 = v1 + rs[kb & 1][bj][1]; }
;                     if (MODE == 5) { const u32x4 c = gq[kb & 1][bj], q = aq[kb & 1][bj];
;                         v0 = (f32x4){bflo(c.x) + sigmoidf_(v0[0]) * bflo(q.x), bfhi(c.x) + sigmoidf_(v0[1]) * bfhi(q.x), bflo(c.y) + sigmoidf_(v0[2]) * bflo(q.y), bfhi(c.y) + sigmoidf_(v0[3]) * bfhi(q.y)};
;                         v1 = (f32x4){bflo(c.z) + sigmoidf_(v1[0]) * bflo(q.z), bfhi(c.z) + sigmoidf_(v1[1]) * bfhi(q.z), bflo(c.w) + sigmoidf_(v1[2]) * bflo(q.w), bfhi(c.w) + sigmoidf_(v1[3]) * bfhi(q.w)}; }
	v_exp_f32_e32 v123, v123
	v_mul_f32_e32 v124, 0xbfb8aa3b, v124
	v_mul_f32_e32 v125, 0xbfb8aa3b, v125
	v_exp_f32_e32 v128, v128
	v_exp_f32_e32 v129, v129
	v_exp_f32_e32 v138, v138
	v_exp_f32_e32 v139, v139
	v_exp_f32_e32 v124, v124
	v_exp_f32_e32 v125, v125
	v_add_f32_e32 v123, 1.0, v123
	v_add_f32_e32 v128, 1.0, v128
	v_add_f32_e32 v129, 1.0, v129
	v_add_f32_e32 v138, 1.0, v138
	v_add_f32_e32 v139, 1.0, v139
	v_rcp_f32_e32 v122, v122
	v_rcp_f32_e32 v123, v123
	v_add_f32_e32 v124, 1.0, v124
	v_add_f32_e32 v125, 1.0, v125
	v_rcp_f32_e32 v128, v128
	v_rcp_f32_e32 v138, v138
	v_rcp_f32_e32 v139, v139
	v_rcp_f32_e32 v129, v129
	v_rcp_f32_e32 v124, v124
	v_rcp_f32_e32 v125, v125
	v_pk_mul_f32 v[142:143], v[166:167], v[66:67] op_sel_hi:[0,1]
	v_pk_mul_f32 v[114:115], v[142:143], v[114:115]
	v_pk_mul_f32 v[118:119], v[118:119], v[122:123]
	v_pk_mul_f32 v[122:123], v[116:117], v[138:139]
	v_pk_mul_f32 v[116:117], v[114:115], v[128:129]
	v_pk_mul_f32 v[120:121], v[120:121], v[124:125]
	v_cvt_pk_bf16_f32 v114, v118, v119
	v_pk_mul_f32 v[124:125], v[164:165], v[80:81] op_sel_hi:[0,1]
	v_cvt_pk_bf16_f32 v115, v120, v121
	v_cvt_pk_bf16_f32 v116, v116, v117
	v_cvt_pk_bf16_f32 v117, v122, v123
	v_or_b32_e32 v122, 48, v152
	global_store_dwordx4 v[126:127], v[114:117], off offset:256
	v_pk_mul_f32 v[126:127], v[164:165], v[78:79] op_sel_hi:[0,1]
	v_pk_mul_f32 v[110:111], v[126:127], v[110:111]
	v_mad_i64_i32 v[114:115], s[34:35], v122, s64, v[154:155]
	v_lshl_add_u64 v[114:115], v[114:115], 0, v[146:147]
	global_load_dwordx4 v[118:121], v[114:115], off nt
	s_nop 0
	global_load_dwordx4 v[114:117], v[114:115], off offset:256 nt
	s_waitcnt vmcnt(5)
	v_lshlrev_b32_e32 v126, 16, v134
	v_mul_f32_e32 v126, 0xbfb8aa3b, v126
	v_exp_f32_e32 v126, v126
	v_pk_mul_f32 v[128:129], v[164:165], v[76:77] op_sel_hi:[0,1]
	v_pk_mul_f32 v[112:113], v[124:125], v[112:113]
	v_and_b32_e32 v125, 0xffff0000, v134
	v_pk_mul_f32 v[108:109], v[128:129], v[108:109]
	v_add_f32_e32 v124, 1.0, v126
	v_mul_f32_e32 v125, 0xbfb8aa3b, v125
	v_lshlrev_b32_e32 v126, 16, v135
	v_and_b32_e32 v127, 0xffff0000, v135
	v_lshlrev_b32_e32 v128, 16, v136
	v_and_b32_e32 v129, 0xffff0000, v136
	v_lshlrev_b32_e32 v134, 16, v137
	v_and_b32_e32 v135, 0xffff0000, v137
	v_exp_f32_e32 v125, v125
	v_mul_f32_e32 v128, 0xbfb8aa3b, v128
	v_mul_f32_e32 v129, 0xbfb8aa3b, v129
	v_mul_f32_e32 v134, 0xbfb8aa3b, v134
	v_mul_f32_e32 v135, 0xbfb8aa3b, v135
	v_exp_f32_e32 v128, v128
	v_exp_f32_e32 v129, v129
	v_exp_f32_e32 v134, v134
	v_exp_f32_e32 v135, v135
	v_mul_f32_e32 v126, 0xbfb8aa3b, v126
	v_mul_f32_e32 v127, 0xbfb8aa3b, v127
	v_exp_f32_e32 v126, v126
	v_exp_f32_e32 v127, v127
	v_add_f32_e32 v125, 1.0, v125
	v_rcp_f32_e32 v124, v124
	v_rcp_f32_e32 v125, v125
	v_add_f32_e32 v128, 1.0, v128
	v_add_f32_e32 v129, 1.0, v129
	v_add_f32_e32 v134, 1.0, v134
	v_add_f32_e32 v135, 1.0, v135
	v_rcp_f32_e32 v128, v128
	v_rcp_f32_e32 v134, v134
	v_rcp_f32_e32 v135, v135
	v_rcp_f32_e32 v129, v129
	v_add_f32_e32 v126, 1.0, v126
	v_add_f32_e32 v127, 1.0, v127
	v_pk_mul_f32 v[138:139], v[164:165], v[74:75] op_sel_hi:[0,1]
	v_rcp_f32_e32 v126, v126
	v_rcp_f32_e32 v127, v127
	v_ashrrev_i32_e32 v171, 31, v170
	v_pk_mul_f32 v[106:107], v[138:139], v[106:107]
	v_pk_mul_f32 v[110:111], v[110:111], v[124:125]
	v_pk_mul_f32 v[124:125], v[108:109], v[134:135]
	v_pk_mul_f32 v[108:109], v[106:107], v[128:129]
	v_cvt_pk_bf16_f32 v106, v110, v111
	v_lshlrev_b64 v[110:111], 13, v[170:171]
	v_lshl_add_u64 v[110:111], s[0:1], 0, v[110:111]
	v_pk_mul_f32 v[112:113], v[112:113], v[126:127]
	v_lshl_add_u64 v[110:111], v[110:111], 0, v[146:147]
	v_cvt_pk_bf16_f32 v107, v112, v113
	v_cvt_pk_bf16_f32 v108, v108, v109
	v_cvt_pk_bf16_f32 v109, v124, v125
	global_store_dwordx4 v[110:111], v[106:109], off
	v_pk_mul_f32 v[112:113], v[164:165], v[68:69] op_sel_hi:[0,1]
	v_pk_mul_f32 v[124:125], v[164:165], v[66:67] op_sel_hi:[0,1]
	v_pk_mul_f32 v[108:109], v[164:165], v[70:71] op_sel_hi:[0,1]
	v_pk_mul_f32 v[102:103], v[108:109], v[102:103]
	s_waitcnt vmcnt(5)
	v_lshlrev_b32_e32 v108, 16, v130
	v_mul_f32_e32 v108, 0xbfb8aa3b, v108
	v_exp_f32_e32 v108, v108
	v_pk_mul_f32 v[106:107], v[164:165], v[72:73] op_sel_hi:[0,1]
	v_pk_mul_f32 v[104:105], v[106:107], v[104:105]
	v_pk_mul_f32 v[98:99], v[124:125], v[98:99]
	v_pk_mul_f32 v[100:101], v[112:113], v[100:101]
	v_add_f32_e32 v106, 1.0, v108
	v_and_b32_e32 v107, 0xffff0000, v130
	v_lshlrev_b32_e32 v108, 16, v131
	v_and_b32_e32 v109, 0xffff0000, v131
	v_lshlrev_b32_e32 v112, 16, v132
	v_and_b32_e32 v113, 0xffff0000, v132
	v_lshlrev_b32_e32 v124, 16, v133
	v_and_b32_e32 v125, 0xffff0000, v133
	v_mul_f32_e32 v107, 0xbfb8aa3b, v107
	v_mul_f32_e32 v108, 0xbfb8aa3b, v108
	v_mul_f32_e32 v109, 0xbfb8aa3b, v109
	v_mul_f32_e32 v112, 0xbfb8aa3b, v112
	v_mul_f32_e32 v113, 0xbfb8aa3b, v113
	v_mul_f32_e32 v124, 0xbfb8aa3b, v124
	v_mul_f32_e32 v125, 0xbfb8aa3b, v125
	v_exp_f32_e32 v107, v107
	v_exp_f32_e32 v108, v108
	v_exp_f32_e32 v109, v109
	v_exp_f32_e32 v112, v112
	v_exp_f32_e32 v113, v113
	v_exp_f32_e32 v124, v124
	v_exp_f32_e32 v125, v125
	v_add_f32_e32 v107, 1.0, v107
	v_add_f32_e32 v108, 1.0, v108
	v_add_f32_e32 v109, 1.0, v109
	v_add_f32_e32 v112, 1.0, v112
	v_add_f32_e32 v113, 1.0, v113
	v_add_f32_e32 v124, 1.0, v124
	v_add_f32_e32 v125, 1.0, v125
	v_rcp_f32_e32 v106, v106
	v_rcp_f32_e32 v107, v107
	v_rcp_f32_e32 v108, v108
	v_rcp_f32_e32 v109, v109
	v_rcp_f32_e32 v112, v112
	v_rcp_f32_e32 v124, v124
	v_rcp_f32_e32 v125, v125
	v_rcp_f32_e32 v113, v113
	v_pk_mul_f32 v[104:105], v[104:105], v[108:109]
	v_pk_mul_f32 v[102:103], v[102:103], v[106:107]
	v_pk_mul_f32 v[106:107], v[100:101], v[124:125]
	v_pk_mul_f32 v[100:101], v[98:99], v[112:113]
	v_cvt_pk_bf16_f32 v98, v102, v103
	v_cvt_pk_bf16_f32 v99, v104, v105
	v_pk_mul_f32 v[108:109], v[162:163], v[78:79] op_sel_hi:[0,1]
	v_cvt_pk_bf16_f32 v100, v100, v101
	v_cvt_pk_bf16_f32 v101, v106, v107
	global_store_dwordx4 v[110:111], v[98:101], off offset:256
	v_pk_mul_f32 v[94:95], v[108:109], v[94:95]
	s_waitcnt vmcnt(3)
;     __device__ __forceinline__ void operator()(const f32x4 (&acc)[2][2][4][2], const Unit& u, int wr, int wc, int fr, int fq) const {
;     ...
;         EPB_LOAD(0);
; #pragma unroll
;         for (int kb = 0; kb < 8; ++kb) { const int ai = kb >> 2, m = kb & 3;
;             if (kb < 7) EPB_LOAD(kb + 1);
;             { const int row = row0 + ai * HALF + m * 16; float rmx = 0.f;
; #pragma unroll
;                 for (int bj = 0; bj < 2; ++bj) { const int col = col0 + bj * HALF; f32x4 v0 = acc[ai][bj][m][0], v1 = acc[ai][bj][m][1];
;                     if (QI8) { const f32x4 c0 = cb[bj][0] * ra[ai][m], c1 = cb[bj][1] * ra[ai][m]; const i32x4 i0 = __builtin_bit_cast(i32x4, v0), i1 = __builtin_bit_cast(i32x4, v1);
;                         v0 = (f32x4){(float)i0[0], (float)i0[1], (float)i0[2], (float)i0[3]} * c0; v1 = (f32x4){(float)i1[0], (float)i1[1], (float)i1[2], (float)i1[3]} * c1; }
;                     else if (MODE == 0) { v0 = v0 * tsc; v1 = v1 * tsc; }
;                     if (!QI8 && MODE == 1) { v0 = v0 * cb[bj][0]; v1 = v1 * cb[bj][1]; }
;                     if (MODE == 2 || MODE == 3) { const u32x4 g = gq[kb & 1][bj];
;                         f32x4 g0 = {sigmoidf_(bflo(g.x)), sigmoidf_(bfhi(g.x)), sigmoidf_(bflo(g.y)), sigmoidf_(bfhi(g.y))};
;                         f32x4 g1 = {sigmoidf_(bflo(g.z)), sigmoidf_(bfhi(g.z)), sigmoidf_(bflo(g.w)), sigmoidf_(bfhi(g.w))};
;                         v0 = v0 * g0; v1 = v1 * g1;
;                         if (MODE == 3) { const u32x4 q = aq[kb & 1][bj];
;                             v0 = v0 + (f32x4){bflo(q.x), bfhi(q.x), bflo(q.y), bfhi(q.y)}; v1 = v1 + (f32x4){bflo(q.z), bfhi(q.z), bflo(q.w), bfhi(q.w)}; } }
;                     if (MODE == 4) { v0 = v0 + rs[kb & 1][bj][0]; v1 = v1 + rs[kb & 1][bj][1]; }
;                     if (MODE == 5) { const u32x4 c = gq[kb & 1][bj], q = aq[kb & 1][bj];
;                         v0 = (f32x4){bflo(c.x) + sigmoidf_(v0[0]) * bflo(q.x), bfhi(c.x) + sigmoidf_(v0[1]) * bfhi(q.x), bflo(c.y) + sigmoidf_(v0[2]) * bflo(q.y), bfhi(c.y) + sigmoidf_(v0[3]) * bfhi(q.y)};
;                         v1 = (f32x4){bflo(c.z) + sigmoidf_(v1[0]) * bflo(q.z), bfhi(c.z) + sigmoidf_(v1[1]) * bfhi(q.z), bflo(c.w) + sigmoidf_(v1[2]) * bflo(q.w), bfhi(c.w) + sigmoidf_(v1[3]) * bfhi(q.w)}; }
	v_lshlrev_b32_e32 v108, 16, v118
	v_mad_i64_i32 v[98:99], s[34:35], v160, s64, v[154:155]
	v_lshl_add_u64 v[98:99], v[98:99], 0, v[146:147]
	global_load_dwordx4 v[102:105], v[98:99], off nt
	s_nop 0
	global_load_dwordx4 v[98:101], v[98:99], off offset:256 nt
	v_mul_f32_e32 v108, 0xbfb8aa3b, v108
	v_pk_mul_f32 v[106:107], v[162:163], v[80:81] op_sel_hi:[0,1]
	v_exp_f32_e32 v108, v108
	v_pk_mul_f32 v[110:111], v[162:163], v[76:77] op_sel_hi:[0,1]
	v_pk_mul_f32 v[112:113], v[162:163], v[74:75] op_sel_hi:[0,1]
	v_pk_mul_f32 v[96:97], v[106:107], v[96:97]
	v_and_b32_e32 v107, 0xffff0000, v118
	v_pk_mul_f32 v[90:91], v[112:113], v[90:91]
	v_pk_mul_f32 v[92:93], v[110:111], v[92:93]
	v_mul_f32_e32 v107, 0xbfb8aa3b, v107
	v_lshlrev_b32_e32 v110, 16, v120
	v_and_b32_e32 v111, 0xffff0000, v120
	v_lshlrev_b32_e32 v112, 16, v121
	v_and_b32_e32 v113, 0xffff0000, v121
	v_exp_f32_e32 v107, v107
	v_mul_f32_e32 v110, 0xbfb8aa3b, v110
	v_mul_f32_e32 v111, 0xbfb8aa3b, v111
	v_mul_f32_e32 v112, 0xbfb8aa3b, v112
	v_mul_f32_e32 v113, 0xbfb8aa3b, v113
	v_add_f32_e32 v106, 1.0, v108
	v_lshlrev_b32_e32 v108, 16, v119
	v_and_b32_e32 v109, 0xffff0000, v119
	v_exp_f32_e32 v110, v110
	v_exp_f32_e32 v111, v111
	v_exp_f32_e32 v112, v112
	v_exp_f32_e32 v113, v113
	v_mul_f32_e32 v108, 0xbfb8aa3b, v108
	v_mul_f32_e32 v109, 0xbfb8aa3b, v109
	v_exp_f32_e32 v108, v108
	v_exp_f32_e32 v109, v109
	v_add_f32_e32 v107, 1.0, v107
	v_rcp_f32_e32 v106, v106
	v_rcp_f32_e32 v107, v107
	v_add_f32_e32 v110, 1.0, v110
	v_add_f32_e32 v111, 1.0, v111
	v_add_f32_e32 v112, 1.0, v112
	v_add_f32_e32 v113, 1.0, v113
	v_rcp_f32_e32 v110, v110
	v_rcp_f32_e32 v112, v112
	v_rcp_f32_e32 v113, v113
	v_rcp_f32_e32 v111, v111
	v_add_f32_e32 v108, 1.0, v108
	v_add_f32_e32 v109, 1.0, v109
	v_rcp_f32_e32 v108, v108
	v_rcp_f32_e32 v109, v109
	v_ashrrev_i32_e32 v123, 31, v122
	v_pk_mul_f32 v[94:95], v[94:95], v[106:107]
	v_pk_mul_f32 v[106:107], v[92:93], v[112:113]
	v_pk_mul_f32 v[92:93], v[90:91], v[110:111]
	v_cvt_pk_bf16_f32 v90, v94, v95
	v_lshlrev_b64 v[94:95], 13, v[122:123]
	v_lshl_add_u64 v[94:95], s[0:1], 0, v[94:95]
	v_pk_mul_f32 v[96:97], v[96:97], v[108:109]
	v_lshl_add_u64 v[94:95], v[94:95], 0, v[146:147]
	v_cvt_pk_bf16_f32 v91, v96, v97
	v_cvt_pk_bf16_f32 v92, v92, v93
	v_cvt_pk_bf16_f32 v93, v106, v107
	global_store_dwordx4 v[94:95], v[90:93], off
	v_pk_mul_f32 v[96:97], v[162:163], v[68:69] op_sel_hi:[0,1]
	v_pk_mul_f32 v[106:107], v[162:163], v[66:67] op_sel_hi:[0,1]
	v_pk_mul_f32 v[92:93], v[162:163], v[70:71] op_sel_hi:[0,1]
	v_pk_mul_f32 v[86:87], v[92:93], v[86:87]
	s_waitcnt vmcnt(5)
	v_lshlrev_b32_e32 v92, 16, v114
	v_mul_f32_e32 v92, 0xbfb8aa3b, v92
	v_exp_f32_e32 v92, v92
	v_pk_mul_f32 v[90:91], v[162:163], v[72:73] op_sel_hi:[0,1]
	v_pk_mul_f32 v[88:89], v[90:91], v[88:89]
	v_pk_mul_f32 v[82:83], v[106:107], v[82:83]
	v_pk_mul_f32 v[84:85], v[96:97], v[84:85]
	v_and_b32_e32 v91, 0xffff0000, v114
	v_lshlrev_b32_e32 v96, 16, v116
	v_and_b32_e32 v97, 0xffff0000, v116
	v_lshlrev_b32_e32 v106, 16, v117
	v_and_b32_e32 v107, 0xffff0000, v117
	v_add_f32_e32 v90, 1.0, v92
	v_mul_f32_e32 v91, 0xbfb8aa3b, v91
	v_lshlrev_b32_e32 v92, 16, v115
	v_and_b32_e32 v93, 0xffff0000, v115
	v_mul_f32_e32 v96, 0xbfb8aa3b, v96
	v_mul_f32_e32 v97, 0xbfb8aa3b, v97
	v_mul_f32_e32 v106, 0xbfb8aa3b, v106
	v_mul_f32_e32 v107, 0xbfb8aa3b, v107
	v_exp_f32_e32 v91, v91
	v_mul_f32_e32 v92, 0xbfb8aa3b, v92
	v_mul_f32_e32 v93, 0xbfb8aa3b, v93
	v_exp_f32_e32 v96, v96
	v_exp_f32_e32 v97, v97
	v_exp_f32_e32 v106, v106
	v_exp_f32_e32 v107, v107
	v_exp_f32_e32 v92, v92
	v_exp_f32_e32 v93, v93
	v_add_f32_e32 v91, 1.0, v91
	v_add_f32_e32 v96, 1.0, v96
	v_add_f32_e32 v97, 1.0, v97
	v_add_f32_e32 v106, 1.0, v106
	v_add_f32_e32 v107, 1.0, v107
	v_rcp_f32_e32 v90, v90
	v_rcp_f32_e32 v91, v91
	v_add_f32_e32 v92, 1.0, v92
	v_add_f32_e32 v93, 1.0, v93
	v_rcp_f32_e32 v96, v96
	v_rcp_f32_e32 v106, v106
	v_rcp_f32_e32 v107, v107
	v_rcp_f32_e32 v97, v97
	v_rcp_f32_e32 v92, v92
	v_rcp_f32_e32 v93, v93
	v_pk_mul_f32 v[86:87], v[86:87], v[90:91]
	v_pk_mul_f32 v[90:91], v[84:85], v[106:107]
	v_pk_mul_f32 v[84:85], v[82:83], v[96:97]
	v_pk_mul_f32 v[88:89], v[88:89], v[92:93]
	v_cvt_pk_bf16_f32 v82, v86, v87
	v_cvt_f32_i32_e32 v61, v61
	v_cvt_pk_bf16_f32 v83, v88, v89
	v_cvt_pk_bf16_f32 v84, v84, v85
	v_cvt_pk_bf16_f32 v85, v90, v91
	v_add_u32_e32 v90, 0x90, v152
	global_store_dwordx4 v[94:95], v[82:85], off offset:256
	v_pk_mul_f32 v[94:95], v[158:159], v[78:79] op_sel_hi:[0,1]
	v_pk_mul_f32 v[62:63], v[94:95], v[62:63]
	v_mad_i64_i32 v[82:83], s[34:35], v90, s64, v[154:155]
	v_lshl_add_u64 v[82:83], v[82:83], 0, v[146:147]
	global_load_dwordx4 v[86:89], v[82:83], off nt
	s_nop 0
	global_load_dwordx4 v[82:85], v[82:83], off offset:256 nt
	s_waitcnt vmcnt(5)
; __device__ __forceinline__ float sigmoidf_(float x) { return __builtin_amdgcn_rcpf(1.f + __builtin_amdgcn_exp2f(-1.4426950408889634f * x)); }
;     __device__ __forceinline__ void operator()(const f32x4 (&acc)[2][2][4][2], const Unit& u, int wr, int wc, int fr, int fq) const {
;     ...
;                 for (int bj = 0; bj < 2; ++bj) { const int col = col0 + bj * HALF; f32x4 v0 = acc[ai][bj][m][0], v1 = acc[ai][bj][m][1];
;                     if (QI8) { const f32x4 c0 = cb[bj][0] * ra[ai][m], c1 = cb[bj][1] * ra[ai][m]; const i32x4 i0 = __builtin_bit_cast(i32x4, v0), i1 = __builtin_bit_cast(i32x4, v1);
;                         v0 = (f32x4){(float)i0[0], (float)i0[1], (float)i0[2], (float)i0[3]} * c0; v1 = (f32x4){(float)i1[0], (float)i1[1], (float)i1[2], (float)i1[3]} * c1; }
;                     else if (MODE == 0) { v0 = v0 * tsc; v1 = v1 * tsc; }
;                     if (!QI8 && MODE == 1) { v0 = v0 * cb[bj][0]; v1 = v1 * cb[bj][1]; }
;                     if (MODE == 2 || MODE == 3) { const u32x4 g = gq[kb & 1][bj];
;                         f32x4 g0 = {sigmoidf_(bflo(g.x)), sigmoidf_(bfhi(g.x)), sigmoidf_(bflo(g.y)), sigmoidf_(bfhi(g.y))};
;                         f32x4 g1 = {sigmoidf_(bflo(g.z)), sigmoidf_(bfhi(g.z)), sigmoidf_(bflo(g.w)), sigmoidf_(bfhi(g.w))};
;                         v0 = v0 * g0; v1 = v1 * g1;
;                         if (MODE == 3) { const u32x4 q = aq[kb & 1][bj];
;                             v0 = v0 + (f32x4){bflo(q.x), bfhi(q.x), bflo(q.y), bfhi(q.y)}; v1 = v1 + (f32x4){bflo(q.z), bfhi(q.z), bflo(q.w), bfhi(q.w)}; } }
;                     if (MODE == 4) { v0 = v0 + rs[kb & 1][bj][0]; v1 = v1 + rs[kb & 1][bj][1]; }
;                     if (MODE == 5) { const u32x4 c = gq[kb & 1][bj], q = aq[kb & 1][bj];
;                         v0 = (f32x4){bflo(c.x) + sigmoidf_(v0[0]) * bflo(q.x), bfhi(c.x) + sigmoidf_(v0[1]) * bfhi(q.x), bflo(c.y) + sigmoidf_(v0[2]) * bflo(q.y), bfhi(c.y) + sigmoidf_(v0[3]) * bfhi(q.y)};
;                         v1 = (f32x4){bflo(c.z) + sigmoidf_(v1[0]) * bflo(q.z), bfhi(c.z) + sigmoidf_(v1[1]) * bfhi(q.z), bflo(c.w) + sigmoidf_(v1[2]) * bflo(q.w), bfhi(c.w) + sigmoidf_(v1[3]) * bfhi(q.w)}; }
;                     u32x4 w; w.x = cvtpk(v0[0], v0[1]); w.y = cvtpk(v0[2], v0[3]); w.z = cvtpk(v1[0], v1[1]); w.w = cvtpk(v1[2], v1[3]);
;                     *(u32x4*)(O + (size_t)row * ldo + col) = w;
	v_lshlrev_b32_e32 v94, 16, v102
	v_mul_f32_e32 v94, 0xbfb8aa3b, v94
	v_cvt_f32_i32_e32 v60, v60
	v_exp_f32_e32 v94, v94
	v_pk_mul_f32 v[92:93], v[158:159], v[80:81] op_sel_hi:[0,1]
	v_pk_mul_f32 v[96:97], v[158:159], v[76:77] op_sel_hi:[0,1]
	v_pk_mul_f32 v[64:65], v[92:93], v[64:65]
	v_and_b32_e32 v93, 0xffff0000, v102
	v_pk_mul_f32 v[60:61], v[96:97], v[60:61]
	v_add_f32_e32 v92, 1.0, v94
	v_mul_f32_e32 v93, 0xbfb8aa3b, v93
	v_lshlrev_b32_e32 v94, 16, v103
	v_and_b32_e32 v95, 0xffff0000, v103
	v_lshlrev_b32_e32 v96, 16, v104
	v_and_b32_e32 v97, 0xffff0000, v104
	v_lshlrev_b32_e32 v102, 16, v105
	v_and_b32_e32 v103, 0xffff0000, v105
	v_exp_f32_e32 v93, v93
	v_mul_f32_e32 v96, 0xbfb8aa3b, v96
	v_mul_f32_e32 v97, 0xbfb8aa3b, v97
	v_mul_f32_e32 v102, 0xbfb8aa3b, v102
	v_mul_f32_e32 v103, 0xbfb8aa3b, v103
	v_exp_f32_e32 v96, v96
	v_exp_f32_e32 v97, v97
	v_exp_f32_e32 v102, v102
	v_exp_f32_e32 v103, v103
	v_mul_f32_e32 v94, 0xbfb8aa3b, v94
	v_mul_f32_e32 v95, 0xbfb8aa3b, v95
	v_exp_f32_e32 v94, v94
	v_exp_f32_e32 v95, v95
	v_add_f32_e32 v93, 1.0, v93
	v_cvt_f32_i32_e32 v59, v59
	v_cvt_f32_i32_e32 v58, v58
	v_rcp_f32_e32 v92, v92
	v_rcp_f32_e32 v93, v93
	v_add_f32_e32 v96, 1.0, v96
	v_add_f32_e32 v97, 1.0, v97
	v_add_f32_e32 v102, 1.0, v102
	v_add_f32_e32 v103, 1.0, v103
	v_rcp_f32_e32 v96, v96
	v_rcp_f32_e32 v102, v102
	v_rcp_f32_e32 v103, v103
	v_rcp_f32_e32 v97, v97
	v_add_f32_e32 v94, 1.0, v94
	v_add_f32_e32 v95, 1.0, v95
	v_pk_mul_f32 v[106:107], v[158:159], v[74:75] op_sel_hi:[0,1]
	v_rcp_f32_e32 v94, v94
	v_rcp_f32_e32 v95, v95
	v_ashrrev_i32_e32 v161, 31, v160
	v_pk_mul_f32 v[58:59], v[106:107], v[58:59]
	v_pk_mul_f32 v[62:63], v[62:63], v[92:93]
	v_pk_mul_f32 v[92:93], v[60:61], v[102:103]
	v_pk_mul_f32 v[60:61], v[58:59], v[96:97]
	v_cvt_pk_bf16_f32 v58, v62, v63
	v_lshlrev_b64 v[62:63], 13, v[160:161]
	v_cvt_f32_i32_e32 v55, v55
	v_cvt_f32_i32_e32 v54, v54
	v_lshl_add_u64 v[62:63], s[0:1], 0, v[62:63]
	v_pk_mul_f32 v[64:65], v[64:65], v[94:95]
	v_lshl_add_u64 v[62:63], v[62:63], 0, v[146:147]
	v_cvt_pk_bf16_f32 v59, v64, v65
	v_cvt_pk_bf16_f32 v60, v60, v61
	v_cvt_pk_bf16_f32 v61, v92, v93
	global_store_dwordx4 v[62:63], v[58:61], off
	v_cvt_f32_i32_e32 v57, v57
	v_cvt_f32_i32_e32 v56, v56
	v_pk_mul_f32 v[60:61], v[158:159], v[70:71] op_sel_hi:[0,1]
	v_pk_mul_f32 v[54:55], v[60:61], v[54:55]
	s_waitcnt vmcnt(5)
	v_lshlrev_b32_e32 v60, 16, v98
	v_cvt_f32_i32_e32 v53, v53
	v_cvt_f32_i32_e32 v52, v52
	v_cvt_f32_i32_e32 v51, v51
	v_cvt_f32_i32_e32 v50, v50
	v_mul_f32_e32 v60, 0xbfb8aa3b, v60
	v_exp_f32_e32 v60, v60
	v_pk_mul_f32 v[58:59], v[158:159], v[72:73] op_sel_hi:[0,1]
	v_pk_mul_f32 v[64:65], v[158:159], v[68:69] op_sel_hi:[0,1]
	v_pk_mul_f32 v[92:93], v[158:159], v[66:67] op_sel_hi:[0,1]
	v_pk_mul_f32 v[56:57], v[58:59], v[56:57]
	v_pk_mul_f32 v[50:51], v[92:93], v[50:51]
	v_pk_mul_f32 v[52:53], v[64:65], v[52:53]
	v_and_b32_e32 v59, 0xffff0000, v98
	v_lshlrev_b32_e32 v64, 16, v100
	v_and_b32_e32 v65, 0xffff0000, v100
	v_lshlrev_b32_e32 v92, 16, v101
	v_and_b32_e32 v93, 0xffff0000, v101
	v_add_f32_e32 v58, 1.0, v60
	v_mul_f32_e32 v59, 0xbfb8aa3b, v59
	v_lshlrev_b32_e32 v60, 16, v99
	v_and_b32_e32 v61, 0xffff0000, v99
	v_mul_f32_e32 v64, 0xbfb8aa3b, v64
	v_mul_f32_e32 v65, 0xbfb8aa3b, v65
	v_mul_f32_e32 v92, 0xbfb8aa3b, v92
	v_mul_f32_e32 v93, 0xbfb8aa3b, v93
	v_exp_f32_e32 v59, v59
	v_mul_f32_e32 v60, 0xbfb8aa3b, v60
	v_mul_f32_e32 v61, 0xbfb8aa3b, v61
	v_exp_f32_e32 v64, v64
	v_exp_f32_e32 v65, v65
	v_exp_f32_e32 v92, v92
	v_exp_f32_e32 v93, v93
	v_exp_f32_e32 v60, v60
	v_exp_f32_e32 v61, v61
	v_add_f32_e32 v59, 1.0, v59
	v_add_f32_e32 v64, 1.0, v64
	v_add_f32_e32 v65, 1.0, v65
	v_add_f32_e32 v92, 1.0, v92
	v_add_f32_e32 v93, 1.0, v93
	v_rcp_f32_e32 v58, v58
	v_rcp_f32_e32 v59, v59
	v_add_f32_e32 v60, 1.0, v60
	v_add_f32_e32 v61, 1.0, v61
	v_rcp_f32_e32 v64, v64
	v_rcp_f32_e32 v92, v92
	v_rcp_f32_e32 v93, v93
	v_rcp_f32_e32 v65, v65
	v_rcp_f32_e32 v60, v60
	v_rcp_f32_e32 v61, v61
	v_cvt_f32_i32_e32 v47, v47
	v_cvt_f32_i32_e32 v46, v46
	v_pk_mul_f32 v[54:55], v[54:55], v[58:59]
	v_pk_mul_f32 v[58:59], v[52:53], v[92:93]
	v_pk_mul_f32 v[52:53], v[50:51], v[64:65]
	v_pk_mul_f32 v[56:57], v[56:57], v[60:61]
	v_cvt_pk_bf16_f32 v50, v54, v55
	v_cvt_f32_i32_e32 v49, v49
	v_cvt_pk_bf16_f32 v51, v56, v57
	v_cvt_pk_bf16_f32 v52, v52, v53
	v_cvt_pk_bf16_f32 v53, v58, v59
	v_add_u32_e32 v58, 0xa0, v152
	global_store_dwordx4 v[62:63], v[50:53], off offset:256
	v_pk_mul_f32 v[62:63], v[156:157], v[78:79] op_sel_hi:[0,1]
	v_pk_mul_f32 v[46:47], v[62:63], v[46:47]
	v_mad_i64_i32 v[50:51], s[34:35], v58, s64, v[154:155]
	v_lshl_add_u64 v[50:51], v[50:51], 0, v[146:147]
	s_waitcnt vmcnt(3)
;     __device__ __forceinline__ void operator()(const f32x4 (&acc)[2][2][4][2], const Unit& u, int wr, int wc, int fr, int fq) const {
;     ...
;         EPB_LOAD(0);
; #pragma unroll
;         for (int kb = 0; kb < 8; ++kb) { const int ai = kb >> 2, m = kb & 3;
;             if (kb < 7) EPB_LOAD(kb + 1);
;             { const int row = row0 + ai * HALF + m * 16; float rmx = 0.f;
; #pragma unroll
;                 for (int bj = 0; bj < 2; ++bj) { const int col = col0 + bj * HALF; f32x4 v0 = acc[ai][bj][m][0], v1 = acc[ai][bj][m][1];
;                     if (QI8) { const f32x4 c0 = cb[bj][0] * ra[ai][m], c1 = cb[bj][1] * ra[ai][m]; const i32x4 i0 = __builtin_bit_cast(i32x4, v0), i1 = __builtin_bit_cast(i32x4, v1);
;                         v0 = (f32x4){(float)i0[0], (float)i0[1], (float)i0[2], (float)i0[3]} * c0; v1 = (f32x4){(float)i1[0], (float)i1[1], (float)i1[2], (float)i1[3]} * c1; }
;                     else if (MODE == 0) { v0 = v0 * tsc; v1 = v1 * tsc; }
;                     if (!QI8 && MODE == 1) { v0 = v0 * cb[bj][0]; v1 = v1 * cb[bj][1]; }
;                     if (MODE == 2 || MODE == 3) { const u32x4 g = gq[kb & 1][bj];
;                         f32x4 g0 = {sigmoidf_(bflo(g.x)), sigmoidf_(bfhi(g.x)), sigmoidf_(bflo(g.y)), sigmoidf_(bfhi(g.y))};
;                         f32x4 g1 = {sigmoidf_(bflo(g.z)), sigmoidf_(bfhi(g.z)), sigmoidf_(bflo(g.w)), sigmoidf_(bfhi(g.w))};
;                         v0 = v0 * g0; v1 = v1 * g1;
;                         if (MODE == 3) { const u32x4 q = aq[kb & 1][bj];
;                             v0 = v0 + (f32x4){bflo(q.x), bfhi(q.x), bflo(q.y), bfhi(q.y)}; v1 = v1 + (f32x4){bflo(q.z), bfhi(q.z), bflo(q.w), bfhi(q.w)}; } }
;                     if (MODE == 4) { v0 = v0 + rs[kb & 1][bj][0]; v1 = v1 + rs[kb & 1][bj][1]; }
;                     if (MODE == 5) { const u32x4 c = gq[kb & 1][bj], q = aq[kb & 1][bj];
;                         v0 = (f32x4){bflo(c.x) + sigmoidf_(v0[0]) * bflo(q.x), bfhi(c.x) + sigmoidf_(v0[1]) * bfhi(q.x), bflo(c.y) + sigmoidf_(v0[2]) * bflo(q.y), bfhi(c.y) + sigmoidf_(v0[3]) * bfhi(q.y)};
;                         v1 = (f32x4){bflo(c.z) + sigmoidf_(v1[0]) * bflo(q.z), bfhi(c.z) + sigmoidf_(v1[1]) * bfhi(q.z), bflo(c.w) + sigmoidf_(v1[2]) * bflo(q.w), bfhi(c.w) + sigmoidf_(v1[3]) * bfhi(q.w)}; }
	v_lshlrev_b32_e32 v62, 16, v86
	global_load_dwordx4 v[54:57], v[50:51], off nt
	s_nop 0
	global_load_dwordx4 v[50:53], v[50:51], off offset:256 nt
	v_cvt_f32_i32_e32 v48, v48
	v_mul_f32_e32 v62, 0xbfb8aa3b, v62
	v_cvt_f32_i32_e32 v45, v45
	v_cvt_f32_i32_e32 v44, v44
	v_exp_f32_e32 v62, v62
	v_pk_mul_f32 v[60:61], v[156:157], v[80:81] op_sel_hi:[0,1]
	v_pk_mul_f32 v[64:65], v[156:157], v[76:77] op_sel_hi:[0,1]
	v_pk_mul_f32 v[48:49], v[60:61], v[48:49]
	v_and_b32_e32 v61, 0xffff0000, v86
	v_pk_mul_f32 v[44:45], v[64:65], v[44:45]
	v_add_f32_e32 v60, 1.0, v62
	v_mul_f32_e32 v61, 0xbfb8aa3b, v61
	v_lshlrev_b32_e32 v62, 16, v87
	v_and_b32_e32 v63, 0xffff0000, v87
	v_lshlrev_b32_e32 v64, 16, v88
	v_and_b32_e32 v65, 0xffff0000, v88
	v_lshlrev_b32_e32 v86, 16, v89
	v_and_b32_e32 v87, 0xffff0000, v89
	v_exp_f32_e32 v61, v61
	v_mul_f32_e32 v64, 0xbfb8aa3b, v64
	v_mul_f32_e32 v65, 0xbfb8aa3b, v65
	v_mul_f32_e32 v86, 0xbfb8aa3b, v86
	v_mul_f32_e32 v87, 0xbfb8aa3b, v87
	v_exp_f32_e32 v64, v64
	v_exp_f32_e32 v65, v65
	v_exp_f32_e32 v86, v86
	v_exp_f32_e32 v87, v87
	v_mul_f32_e32 v62, 0xbfb8aa3b, v62
	v_mul_f32_e32 v63, 0xbfb8aa3b, v63
	v_exp_f32_e32 v62, v62
	v_exp_f32_e32 v63, v63
	v_add_f32_e32 v61, 1.0, v61
	v_cvt_f32_i32_e32 v43, v43
	v_cvt_f32_i32_e32 v42, v42
	v_rcp_f32_e32 v60, v60
	v_rcp_f32_e32 v61, v61
	v_add_f32_e32 v64, 1.0, v64
	v_add_f32_e32 v65, 1.0, v65
	v_add_f32_e32 v86, 1.0, v86
	v_add_f32_e32 v87, 1.0, v87
	v_rcp_f32_e32 v64, v64
	v_rcp_f32_e32 v86, v86
	v_rcp_f32_e32 v87, v87
	v_rcp_f32_e32 v65, v65
	v_add_f32_e32 v62, 1.0, v62
	v_add_f32_e32 v63, 1.0, v63
	v_pk_mul_f32 v[92:93], v[156:157], v[74:75] op_sel_hi:[0,1]
	v_rcp_f32_e32 v62, v62
	v_rcp_f32_e32 v63, v63
	v_ashrrev_i32_e32 v91, 31, v90
	v_pk_mul_f32 v[42:43], v[92:93], v[42:43]
	v_pk_mul_f32 v[46:47], v[46:47], v[60:61]
	v_pk_mul_f32 v[60:61], v[44:45], v[86:87]
	v_pk_mul_f32 v[44:45], v[42:43], v[64:65]
	v_cvt_pk_bf16_f32 v42, v46, v47
	v_lshlrev_b64 v[46:47], 13, v[90:91]
	v_cvt_f32_i32_e32 v39, v39
	v_cvt_f32_i32_e32 v38, v38
	v_lshl_add_u64 v[46:47], s[0:1], 0, v[46:47]
	v_pk_mul_f32 v[48:49], v[48:49], v[62:63]
	v_lshl_add_u64 v[46:47], v[46:47], 0, v[146:147]
	v_cvt_pk_bf16_f32 v43, v48, v49
	v_cvt_pk_bf16_f32 v44, v44, v45
	v_cvt_pk_bf16_f32 v45, v60, v61
	global_store_dwordx4 v[46:47], v[42:45], off
	v_cvt_f32_i32_e32 v41, v41
	v_cvt_f32_i32_e32 v40, v40
	v_pk_mul_f32 v[44:45], v[156:157], v[70:71] op_sel_hi:[0,1]
	v_pk_mul_f32 v[38:39], v[44:45], v[38:39]
	s_waitcnt vmcnt(5)
	v_lshlrev_b32_e32 v44, 16, v82
	v_cvt_f32_i32_e32 v37, v37
	v_cvt_f32_i32_e32 v36, v36
	v_cvt_f32_i32_e32 v35, v35
	v_cvt_f32_i32_e32 v34, v34
	v_mul_f32_e32 v44, 0xbfb8aa3b, v44
	v_exp_f32_e32 v44, v44
	v_pk_mul_f32 v[42:43], v[156:157], v[72:73] op_sel_hi:[0,1]
	v_pk_mul_f32 v[48:49], v[156:157], v[68:69] op_sel_hi:[0,1]
	v_pk_mul_f32 v[60:61], v[156:157], v[66:67] op_sel_hi:[0,1]
	v_pk_mul_f32 v[40:41], v[42:43], v[40:41]
	v_pk_mul_f32 v[34:35], v[60:61], v[34:35]
	v_pk_mul_f32 v[36:37], v[48:49], v[36:37]
	v_and_b32_e32 v43, 0xffff0000, v82
	v_lshlrev_b32_e32 v48, 16, v84
	v_and_b32_e32 v49, 0xffff0000, v84
	v_lshlrev_b32_e32 v60, 16, v85
	v_and_b32_e32 v61, 0xffff0000, v85
	v_add_f32_e32 v42, 1.0, v44
	v_mul_f32_e32 v43, 0xbfb8aa3b, v43
	v_lshlrev_b32_e32 v44, 16, v83
	v_and_b32_e32 v45, 0xffff0000, v83
	v_mul_f32_e32 v48, 0xbfb8aa3b, v48
	v_mul_f32_e32 v49, 0xbfb8aa3b, v49
	v_mul_f32_e32 v60, 0xbfb8aa3b, v60
	v_mul_f32_e32 v61, 0xbfb8aa3b, v61
	v_exp_f32_e32 v43, v43
	v_mul_f32_e32 v44, 0xbfb8aa3b, v44
	v_mul_f32_e32 v45, 0xbfb8aa3b, v45
	v_exp_f32_e32 v48, v48
	v_exp_f32_e32 v49, v49
	v_exp_f32_e32 v60, v60
	v_exp_f32_e32 v61, v61
	v_exp_f32_e32 v44, v44
	v_exp_f32_e32 v45, v45
	v_add_f32_e32 v43, 1.0, v43
	v_add_f32_e32 v48, 1.0, v48
	v_add_f32_e32 v49, 1.0, v49
	v_add_f32_e32 v60, 1.0, v60
	v_add_f32_e32 v61, 1.0, v61
	v_rcp_f32_e32 v42, v42
	v_rcp_f32_e32 v43, v43
	v_add_f32_e32 v44, 1.0, v44
	v_add_f32_e32 v45, 1.0, v45
	v_rcp_f32_e32 v48, v48
	v_rcp_f32_e32 v60, v60
	v_rcp_f32_e32 v61, v61
	v_rcp_f32_e32 v49, v49
	v_rcp_f32_e32 v44, v44
	v_rcp_f32_e32 v45, v45
	v_pk_mul_f32 v[38:39], v[38:39], v[42:43]
	v_pk_mul_f32 v[42:43], v[36:37], v[60:61]
	v_pk_mul_f32 v[36:37], v[34:35], v[48:49]
	v_pk_mul_f32 v[40:41], v[40:41], v[44:45]
	v_cvt_pk_bf16_f32 v34, v38, v39
	v_cvt_f32_i32_e32 v31, v31
	v_cvt_pk_bf16_f32 v35, v40, v41
	v_cvt_pk_bf16_f32 v36, v36, v37
	v_cvt_pk_bf16_f32 v37, v42, v43
	v_add_u32_e32 v42, 0xb0, v152
	global_store_dwordx4 v[46:47], v[34:37], off offset:256
	v_cvt_f32_i32_e32 v30, v30
	v_pk_mul_f32 v[46:47], v[150:151], v[78:79] op_sel_hi:[0,1]
	v_mad_i64_i32 v[34:35], s[34:35], v42, s64, v[154:155]
	v_lshl_add_u64 v[34:35], v[34:35], 0, v[146:147]
	global_load_dwordx4 v[38:41], v[34:35], off nt
	s_nop 0
	global_load_dwordx4 v[34:37], v[34:35], off offset:256 nt
	v_pk_mul_f32 v[30:31], v[46:47], v[30:31]
	s_waitcnt vmcnt(5)
; __device__ __forceinline__ float sigmoidf_(float x) { return __builtin_amdgcn_rcpf(1.f + __builtin_amdgcn_exp2f(-1.4426950408889634f * x)); }
;     __device__ __forceinline__ void operator()(const f32x4 (&acc)[2][2][4][2], const Unit& u, int wr, int wc, int fr, int fq) const {
;     ...
;                 for (int bj = 0; bj < 2; ++bj) { const int col = col0 + bj * HALF; f32x4 v0 = acc[ai][bj][m][0], v1 = acc[ai][bj][m][1];
;                     if (QI8) { const f32x4 c0 = cb[bj][0] * ra[ai][m], c1 = cb[bj][1] * ra[ai][m]; const i32x4 i0 = __builtin_bit_cast(i32x4, v0), i1 = __builtin_bit_cast(i32x4, v1);
;                         v0 = (f32x4){(float)i0[0], (float)i0[1], (float)i0[2], (float)i0[3]} * c0; v1 = (f32x4){(float)i1[0], (float)i1[1], (float)i1[2], (float)i1[3]} * c1; }
;                     else if (MODE == 0) { v0 = v0 * tsc; v1 = v1 * tsc; }
;                     if (!QI8 && MODE == 1) { v0 = v0 * cb[bj][0]; v1 = v1 * cb[bj][1]; }
;                     if (MODE == 2 || MODE == 3) { const u32x4 g = gq[kb & 1][bj];
;                         f32x4 g0 = {sigmoidf_(bflo(g.x)), sigmoidf_(bfhi(g.x)), sigmoidf_(bflo(g.y)), sigmoidf_(bfhi(g.y))};
;                         f32x4 g1 = {sigmoidf_(bflo(g.z)), sigmoidf_(bfhi(g.z)), sigmoidf_(bflo(g.w)), sigmoidf_(bfhi(g.w))};
;                         v0 = v0 * g0; v1 = v1 * g1;
;                         if (MODE == 3) { const u32x4 q = aq[kb & 1][bj];
;                             v0 = v0 + (f32x4){bflo(q.x), bfhi(q.x), bflo(q.y), bfhi(q.y)}; v1 = v1 + (f32x4){bflo(q.z), bfhi(q.z), bflo(q.w), bfhi(q.w)}; } }
;                     if (MODE == 4) { v0 = v0 + rs[kb & 1][bj][0]; v1 = v1 + rs[kb & 1][bj][1]; }
;                     if (MODE == 5) { const u32x4 c = gq[kb & 1][bj], q = aq[kb & 1][bj];
;                         v0 = (f32x4){bflo(c.x) + sigmoidf_(v0[0]) * bflo(q.x), bfhi(c.x) + sigmoidf_(v0[1]) * bfhi(q.x), bflo(c.y) + sigmoidf_(v0[2]) * bflo(q.y), bfhi(c.y) + sigmoidf_(v0[3]) * bfhi(q.y)};
;                         v1 = (f32x4){bflo(c.z) + sigmoidf_(v1[0]) * bflo(q.z), bfhi(c.z) + sigmoidf_(v1[1]) * bfhi(q.z), bflo(c.w) + sigmoidf_(v1[2]) * bflo(q.w), bfhi(c.w) + sigmoidf_(v1[3]) * bfhi(q.w)}; }
;                     u32x4 w; w.x = cvtpk(v0[0], v0[1]); w.y = cvtpk(v0[2], v0[3]); w.z = cvtpk(v1[0], v1[1]); w.w = cvtpk(v1[2], v1[3]);
;                     *(u32x4*)(O + (size_t)row * ldo + col) = w;
	v_lshlrev_b32_e32 v46, 16, v54
	v_cvt_f32_i32_e32 v33, v33
	v_cvt_f32_i32_e32 v32, v32
	v_mul_f32_e32 v46, 0xbfb8aa3b, v46
	v_cvt_f32_i32_e32 v29, v29
	v_cvt_f32_i32_e32 v28, v28
	v_exp_f32_e32 v46, v46
	v_pk_mul_f32 v[44:45], v[150:151], v[80:81] op_sel_hi:[0,1]
	v_pk_mul_f32 v[48:49], v[150:151], v[76:77] op_sel_hi:[0,1]
	v_pk_mul_f32 v[32:33], v[44:45], v[32:33]
	v_and_b32_e32 v45, 0xffff0000, v54
	v_pk_mul_f32 v[28:29], v[48:49], v[28:29]
	v_add_f32_e32 v44, 1.0, v46
	v_mul_f32_e32 v45, 0xbfb8aa3b, v45
	v_lshlrev_b32_e32 v46, 16, v55
	v_and_b32_e32 v47, 0xffff0000, v55
	v_lshlrev_b32_e32 v48, 16, v56
	v_and_b32_e32 v49, 0xffff0000, v56
	v_lshlrev_b32_e32 v54, 16, v57
	v_and_b32_e32 v55, 0xffff0000, v57
	v_exp_f32_e32 v45, v45
	v_mul_f32_e32 v48, 0xbfb8aa3b, v48
	v_mul_f32_e32 v49, 0xbfb8aa3b, v49
	v_mul_f32_e32 v54, 0xbfb8aa3b, v54
	v_mul_f32_e32 v55, 0xbfb8aa3b, v55
	v_exp_f32_e32 v48, v48
	v_exp_f32_e32 v49, v49
	v_exp_f32_e32 v54, v54
	v_exp_f32_e32 v55, v55
	v_mul_f32_e32 v46, 0xbfb8aa3b, v46
	v_mul_f32_e32 v47, 0xbfb8aa3b, v47
	v_exp_f32_e32 v46, v46
	v_exp_f32_e32 v47, v47
	v_add_f32_e32 v45, 1.0, v45
	v_cvt_f32_i32_e32 v27, v27
	v_cvt_f32_i32_e32 v26, v26
	v_rcp_f32_e32 v44, v44
	v_rcp_f32_e32 v45, v45
	v_add_f32_e32 v48, 1.0, v48
	v_add_f32_e32 v49, 1.0, v49
	v_add_f32_e32 v54, 1.0, v54
	v_add_f32_e32 v55, 1.0, v55
	v_rcp_f32_e32 v48, v48
	v_rcp_f32_e32 v54, v54
	v_rcp_f32_e32 v55, v55
	v_rcp_f32_e32 v49, v49
	v_add_f32_e32 v46, 1.0, v46
	v_add_f32_e32 v47, 1.0, v47
	v_pk_mul_f32 v[60:61], v[150:151], v[74:75] op_sel_hi:[0,1]
	v_rcp_f32_e32 v46, v46
	v_rcp_f32_e32 v47, v47
	v_ashrrev_i32_e32 v59, 31, v58
	v_pk_mul_f32 v[26:27], v[60:61], v[26:27]
	v_pk_mul_f32 v[30:31], v[30:31], v[44:45]
	v_pk_mul_f32 v[44:45], v[28:29], v[54:55]
	v_pk_mul_f32 v[28:29], v[26:27], v[48:49]
	v_cvt_pk_bf16_f32 v26, v30, v31
	v_lshlrev_b64 v[30:31], 13, v[58:59]
	v_cvt_f32_i32_e32 v23, v23
	v_cvt_f32_i32_e32 v22, v22
	v_lshl_add_u64 v[30:31], s[0:1], 0, v[30:31]
	v_pk_mul_f32 v[32:33], v[32:33], v[46:47]
	v_lshl_add_u64 v[30:31], v[30:31], 0, v[146:147]
	v_cvt_pk_bf16_f32 v27, v32, v33
	v_cvt_pk_bf16_f32 v28, v28, v29
	v_cvt_pk_bf16_f32 v29, v44, v45
	global_store_dwordx4 v[30:31], v[26:29], off
	v_cvt_f32_i32_e32 v25, v25
	v_cvt_f32_i32_e32 v24, v24
	v_pk_mul_f32 v[28:29], v[150:151], v[70:71] op_sel_hi:[0,1]
	v_pk_mul_f32 v[22:23], v[28:29], v[22:23]
	s_waitcnt vmcnt(5)
	v_lshlrev_b32_e32 v28, 16, v50
	v_cvt_f32_i32_e32 v21, v21
	v_cvt_f32_i32_e32 v20, v20
	v_cvt_f32_i32_e32 v19, v19
	v_cvt_f32_i32_e32 v18, v18
	v_mul_f32_e32 v28, 0xbfb8aa3b, v28
	v_exp_f32_e32 v28, v28
	v_pk_mul_f32 v[26:27], v[150:151], v[72:73] op_sel_hi:[0,1]
	v_pk_mul_f32 v[32:33], v[150:151], v[68:69] op_sel_hi:[0,1]
	v_pk_mul_f32 v[44:45], v[150:151], v[66:67] op_sel_hi:[0,1]
	v_pk_mul_f32 v[24:25], v[26:27], v[24:25]
	v_pk_mul_f32 v[18:19], v[44:45], v[18:19]
	v_pk_mul_f32 v[20:21], v[32:33], v[20:21]
	v_and_b32_e32 v27, 0xffff0000, v50
	v_lshlrev_b32_e32 v32, 16, v52
	v_and_b32_e32 v33, 0xffff0000, v52
	v_lshlrev_b32_e32 v44, 16, v53
	v_and_b32_e32 v45, 0xffff0000, v53
	v_add_f32_e32 v26, 1.0, v28
	v_mul_f32_e32 v27, 0xbfb8aa3b, v27
	v_lshlrev_b32_e32 v28, 16, v51
	v_and_b32_e32 v29, 0xffff0000, v51
	v_mul_f32_e32 v32, 0xbfb8aa3b, v32
	v_mul_f32_e32 v33, 0xbfb8aa3b, v33
	v_mul_f32_e32 v44, 0xbfb8aa3b, v44
	v_mul_f32_e32 v45, 0xbfb8aa3b, v45
	v_exp_f32_e32 v27, v27
	v_mul_f32_e32 v28, 0xbfb8aa3b, v28
	v_mul_f32_e32 v29, 0xbfb8aa3b, v29
	v_exp_f32_e32 v32, v32
	v_exp_f32_e32 v33, v33
	v_exp_f32_e32 v44, v44
	v_exp_f32_e32 v45, v45
	v_exp_f32_e32 v28, v28
	v_exp_f32_e32 v29, v29
	v_add_f32_e32 v27, 1.0, v27
	v_add_f32_e32 v32, 1.0, v32
	v_add_f32_e32 v33, 1.0, v33
	v_add_f32_e32 v44, 1.0, v44
	v_add_f32_e32 v45, 1.0, v45
	v_rcp_f32_e32 v26, v26
	v_rcp_f32_e32 v27, v27
	v_add_f32_e32 v28, 1.0, v28
	v_add_f32_e32 v29, 1.0, v29
	v_rcp_f32_e32 v32, v32
	v_rcp_f32_e32 v44, v44
	v_rcp_f32_e32 v45, v45
	v_rcp_f32_e32 v33, v33
	v_rcp_f32_e32 v28, v28
	v_rcp_f32_e32 v29, v29
	v_cvt_f32_i32_e32 v15, v15
	v_cvt_f32_i32_e32 v14, v14
	v_pk_mul_f32 v[22:23], v[22:23], v[26:27]
	v_pk_mul_f32 v[26:27], v[20:21], v[44:45]
	v_pk_mul_f32 v[20:21], v[18:19], v[32:33]
	v_pk_mul_f32 v[24:25], v[24:25], v[28:29]
	v_cvt_pk_bf16_f32 v18, v22, v23
	v_cvt_f32_i32_e32 v17, v17
	v_cvt_pk_bf16_f32 v19, v24, v25
	v_cvt_pk_bf16_f32 v20, v20, v21
	v_cvt_pk_bf16_f32 v21, v26, v27
	global_store_dwordx4 v[30:31], v[18:21], off offset:256
	v_cvt_f32_i32_e32 v16, v16
	v_cvt_f32_i32_e32 v13, v13
	v_pk_mul_f32 v[20:21], v[78:79], v[148:149] op_sel_hi:[1,0]
	v_cvt_f32_i32_e32 v12, v12
	v_pk_mul_f32 v[14:15], v[20:21], v[14:15]
	v_cvt_f32_i32_e32 v11, v11
	v_cvt_f32_i32_e32 v10, v10
	s_waitcnt vmcnt(3)
; __device__ __forceinline__ float sigmoidf_(float x) { return __builtin_amdgcn_rcpf(1.f + __builtin_amdgcn_exp2f(-1.4426950408889634f * x)); }
;     __device__ __forceinline__ void operator()(const f32x4 (&acc)[2][2][4][2], const Unit& u, int wr, int wc, int fr, int fq) const {
;     ...
;                 for (int bj = 0; bj < 2; ++bj) { const int col = col0 + bj * HALF; f32x4 v0 = acc[ai][bj][m][0], v1 = acc[ai][bj][m][1];
;                     if (QI8) { const f32x4 c0 = cb[bj][0] * ra[ai][m], c1 = cb[bj][1] * ra[ai][m]; const i32x4 i0 = __builtin_bit_cast(i32x4, v0), i1 = __builtin_bit_cast(i32x4, v1);
;                         v0 = (f32x4){(float)i0[0], (float)i0[1], (float)i0[2], (float)i0[3]} * c0; v1 = (f32x4){(float)i1[0], (float)i1[1], (float)i1[2], (float)i1[3]} * c1; }
;                     else if (MODE == 0) { v0 = v0 * tsc; v1 = v1 * tsc; }
;                     if (!QI8 && MODE == 1) { v0 = v0 * cb[bj][0]; v1 = v1 * cb[bj][1]; }
;                     if (MODE == 2 || MODE == 3) { const u32x4 g = gq[kb & 1][bj];
;                         f32x4 g0 = {sigmoidf_(bflo(g.x)), sigmoidf_(bfhi(g.x)), sigmoidf_(bflo(g.y)), sigmoidf_(bfhi(g.y))};
;                         f32x4 g1 = {sigmoidf_(bflo(g.z)), sigmoidf_(bfhi(g.z)), sigmoidf_(bflo(g.w)), sigmoidf_(bfhi(g.w))};
;                         v0 = v0 * g0; v1 = v1 * g1;
;                         if (MODE == 3) { const u32x4 q = aq[kb & 1][bj];
;                             v0 = v0 + (f32x4){bflo(q.x), bfhi(q.x), bflo(q.y), bfhi(q.y)}; v1 = v1 + (f32x4){bflo(q.z), bfhi(q.z), bflo(q.w), bfhi(q.w)}; } }
;                     if (MODE == 4) { v0 = v0 + rs[kb & 1][bj][0]; v1 = v1 + rs[kb & 1][bj][1]; }
;                     if (MODE == 5) { const u32x4 c = gq[kb & 1][bj], q = aq[kb & 1][bj];
;                         v0 = (f32x4){bflo(c.x) + sigmoidf_(v0[0]) * bflo(q.x), bfhi(c.x) + sigmoidf_(v0[1]) * bfhi(q.x), bflo(c.y) + sigmoidf_(v0[2]) * bflo(q.y), bfhi(c.y) + sigmoidf_(v0[3]) * bfhi(q.y)};
;                         v1 = (f32x4){bflo(c.z) + sigmoidf_(v1[0]) * bflo(q.z), bfhi(c.z) + sigmoidf_(v1[1]) * bfhi(q.z), bflo(c.w) + sigmoidf_(v1[2]) * bflo(q.w), bfhi(c.w) + sigmoidf_(v1[3]) * bfhi(q.w)}; }
;                     u32x4 w; w.x = cvtpk(v0[0], v0[1]); w.y = cvtpk(v0[2], v0[3]); w.z = cvtpk(v1[0], v1[1]); w.w = cvtpk(v1[2], v1[3]);
;                     *(u32x4*)(O + (size_t)row * ldo + col) = w;
	v_lshlrev_b32_e32 v20, 16, v38
	v_mul_f32_e32 v20, 0xbfb8aa3b, v20
	v_pk_mul_f32 v[18:19], v[80:81], v[148:149] op_sel_hi:[1,0]
	v_exp_f32_e32 v20, v20
	v_pk_mul_f32 v[22:23], v[148:149], v[76:77] op_sel_hi:[0,1]
	v_pk_mul_f32 v[24:25], v[148:149], v[74:75] op_sel_hi:[0,1]
	v_pk_mul_f32 v[16:17], v[18:19], v[16:17]
	v_and_b32_e32 v19, 0xffff0000, v38
	v_pk_mul_f32 v[10:11], v[24:25], v[10:11]
	v_pk_mul_f32 v[12:13], v[22:23], v[12:13]
	v_mul_f32_e32 v19, 0xbfb8aa3b, v19
	v_lshlrev_b32_e32 v22, 16, v40
	v_and_b32_e32 v23, 0xffff0000, v40
	v_lshlrev_b32_e32 v24, 16, v41
	v_and_b32_e32 v25, 0xffff0000, v41
	v_exp_f32_e32 v19, v19
	v_mul_f32_e32 v22, 0xbfb8aa3b, v22
	v_mul_f32_e32 v23, 0xbfb8aa3b, v23
	v_mul_f32_e32 v24, 0xbfb8aa3b, v24
	v_mul_f32_e32 v25, 0xbfb8aa3b, v25
	v_add_f32_e32 v18, 1.0, v20
	v_lshlrev_b32_e32 v20, 16, v39
	v_and_b32_e32 v21, 0xffff0000, v39
	v_exp_f32_e32 v22, v22
	v_exp_f32_e32 v23, v23
	v_exp_f32_e32 v24, v24
	v_exp_f32_e32 v25, v25
	v_mul_f32_e32 v20, 0xbfb8aa3b, v20
	v_mul_f32_e32 v21, 0xbfb8aa3b, v21
	v_exp_f32_e32 v20, v20
	v_exp_f32_e32 v21, v21
	v_add_f32_e32 v19, 1.0, v19
	v_rcp_f32_e32 v18, v18
	v_rcp_f32_e32 v19, v19
	v_add_f32_e32 v22, 1.0, v22
	v_add_f32_e32 v23, 1.0, v23
	v_add_f32_e32 v24, 1.0, v24
	v_add_f32_e32 v25, 1.0, v25
	v_rcp_f32_e32 v22, v22
	v_rcp_f32_e32 v24, v24
	v_rcp_f32_e32 v25, v25
	v_rcp_f32_e32 v23, v23
	v_add_f32_e32 v20, 1.0, v20
	v_add_f32_e32 v21, 1.0, v21
	v_rcp_f32_e32 v20, v20
	v_rcp_f32_e32 v21, v21
	v_ashrrev_i32_e32 v43, 31, v42
	v_pk_mul_f32 v[14:15], v[14:15], v[18:19]
	v_pk_mul_f32 v[18:19], v[12:13], v[24:25]
	v_pk_mul_f32 v[12:13], v[10:11], v[22:23]
	v_cvt_pk_bf16_f32 v10, v14, v15
	v_lshlrev_b64 v[14:15], 13, v[42:43]
	v_cvt_f32_i32_e32 v7, v7
	v_cvt_f32_i32_e32 v6, v6
	v_lshl_add_u64 v[14:15], s[0:1], 0, v[14:15]
	v_pk_mul_f32 v[16:17], v[16:17], v[20:21]
	v_lshl_add_u64 v[14:15], v[14:15], 0, v[146:147]
	v_cvt_pk_bf16_f32 v11, v16, v17
	v_cvt_pk_bf16_f32 v12, v12, v13
	v_cvt_pk_bf16_f32 v13, v18, v19
	global_store_dwordx4 v[14:15], v[10:13], off
	v_cvt_f32_i32_e32 v9, v9
	v_cvt_f32_i32_e32 v8, v8
	v_pk_mul_f32 v[12:13], v[148:149], v[70:71] op_sel_hi:[0,1]
	v_pk_mul_f32 v[6:7], v[12:13], v[6:7]
	s_waitcnt vmcnt(3)
	v_lshlrev_b32_e32 v12, 16, v34
	v_cvt_f32_i32_e32 v5, v5
	v_cvt_f32_i32_e32 v4, v4
	v_cvt_f32_i32_e32 v3, v3
	v_cvt_f32_i32_e32 v2, v2
	v_mul_f32_e32 v12, 0xbfb8aa3b, v12
	v_exp_f32_e32 v12, v12
	v_pk_mul_f32 v[10:11], v[148:149], v[72:73] op_sel_hi:[0,1]
	v_pk_mul_f32 v[16:17], v[148:149], v[68:69] op_sel_hi:[0,1]
	v_pk_mul_f32 v[18:19], v[148:149], v[66:67] op_sel_hi:[0,1]
	v_pk_mul_f32 v[8:9], v[10:11], v[8:9]
	v_pk_mul_f32 v[2:3], v[18:19], v[2:3]
	v_pk_mul_f32 v[4:5], v[16:17], v[4:5]
	v_and_b32_e32 v11, 0xffff0000, v34
	v_lshlrev_b32_e32 v16, 16, v36
	v_and_b32_e32 v17, 0xffff0000, v36
	v_lshlrev_b32_e32 v18, 16, v37
	v_and_b32_e32 v19, 0xffff0000, v37
	v_add_f32_e32 v10, 1.0, v12
	v_mul_f32_e32 v11, 0xbfb8aa3b, v11
	v_lshlrev_b32_e32 v12, 16, v35
	v_and_b32_e32 v13, 0xffff0000, v35
	v_mul_f32_e32 v16, 0xbfb8aa3b, v16
	v_mul_f32_e32 v17, 0xbfb8aa3b, v17
	v_mul_f32_e32 v18, 0xbfb8aa3b, v18
	v_mul_f32_e32 v19, 0xbfb8aa3b, v19
	v_exp_f32_e32 v11, v11
	v_mul_f32_e32 v12, 0xbfb8aa3b, v12
	v_mul_f32_e32 v13, 0xbfb8aa3b, v13
	v_exp_f32_e32 v16, v16
	v_exp_f32_e32 v17, v17
	v_exp_f32_e32 v18, v18
	v_exp_f32_e32 v19, v19
	v_exp_f32_e32 v12, v12
	v_exp_f32_e32 v13, v13
	v_add_f32_e32 v11, 1.0, v11
	v_add_f32_e32 v16, 1.0, v16
	v_add_f32_e32 v17, 1.0, v17
	v_add_f32_e32 v18, 1.0, v18
	v_add_f32_e32 v19, 1.0, v19
	v_rcp_f32_e32 v10, v10
	v_rcp_f32_e32 v11, v11
	v_add_f32_e32 v12, 1.0, v12
	v_add_f32_e32 v13, 1.0, v13
	v_rcp_f32_e32 v16, v16
	v_rcp_f32_e32 v18, v18
	v_rcp_f32_e32 v19, v19
	v_rcp_f32_e32 v17, v17
	v_rcp_f32_e32 v12, v12
	v_rcp_f32_e32 v13, v13
	v_pk_mul_f32 v[6:7], v[6:7], v[10:11]
	v_pk_mul_f32 v[10:11], v[4:5], v[18:19]
	v_pk_mul_f32 v[4:5], v[2:3], v[16:17]
	s_andn2_b64 vcc, exec, s[6:7]
	s_mov_b64 s[6:7], -1
	v_pk_mul_f32 v[8:9], v[8:9], v[12:13]
	v_cvt_pk_bf16_f32 v2, v6, v7
	s_nop 0
	v_cvt_pk_bf16_f32 v3, v8, v9
	v_cvt_pk_bf16_f32 v4, v4, v5
	v_cvt_pk_bf16_f32 v5, v10, v11
	global_store_dwordx4 v[14:15], v[2:5], off offset:256
	s_cbranch_vccnz .LBB0_988
	s_andn2_b64 vcc, exec, s[8:9]
	s_cbranch_vccnz .LBB0_987
	s_barrier
	s_branch .LBB0_987

; __device__ __forceinline__ float sigmoidf_(float x) { return __builtin_amdgcn_rcpf(1.f + __builtin_amdgcn_exp2f(-1.4426950408889634f * x)); }
;     __device__ __forceinline__ void operator()(const f32x4 (&acc)[2][2][4][2], const Unit& u, int wr, int wc, int fr, int fq) const {
;     ...
;         EPB_LOAD(0);
; #pragma unroll
;         for (int kb = 0; kb < 8; ++kb) { const int ai = kb >> 2, m = kb & 3;
;             if (kb < 7) EPB_LOAD(kb + 1);
;             { const int row = row0 + ai * HALF + m * 16; float rmx = 0.f;
; #pragma unroll
;                 for (int bj = 0; bj < 2; ++bj) { const int col = col0 + bj * HALF; f32x4 v0 = acc[ai][bj][m][0], v1 = acc[ai][bj][m][1];
;                     if (QI8) { const f32x4 c0 = cb[bj][0] * ra[ai][m], c1 = cb[bj][1] * ra[ai][m]; const i32x4 i0 = __builtin_bit_cast(i32x4, v0), i1 = __builtin_bit_cast(i32x4, v1);
;                         v0 = (f32x4){(float)i0[0], (float)i0[1], (float)i0[2], (float)i0[3]} * c0; v1 = (f32x4){(float)i1[0], (float)i1[1], (float)i1[2], (float)i1[3]} * c1; }
;                     else if (MODE == 0) { v0 = v0 * tsc; v1 = v1 * tsc; }
;                     if (!QI8 && MODE == 1) { v0 = v0 * cb[bj][0]; v1 = v1 * cb[bj][1]; }
;                     if (MODE == 2 || MODE == 3) { const u32x4 g = gq[kb & 1][bj];
;                         f32x4 g0 = {sigmoidf_(bflo(g.x)), sigmoidf_(bfhi(g.x)), sigmoidf_(bflo(g.y)), sigmoidf_(bfhi(g.y))};
;                         f32x4 g1 = {sigmoidf_(bflo(g.z)), sigmoidf_(bfhi(g.z)), sigmoidf_(bflo(g.w)), sigmoidf_(bfhi(g.w))};
;                         v0 = v0 * g0; v1 = v1 * g1;
;                         if (MODE == 3) { const u32x4 q = aq[kb & 1][bj];
;                             v0 = v0 + (f32x4){bflo(q.x), bfhi(q.x), bflo(q.y), bfhi(q.y)}; v1 = v1 + (f32x4){bflo(q.z), bfhi(q.z), bflo(q.w), bfhi(q.w)}; } }
.LBB0_1030:
	v_lshl_or_b32 v162, s34, 8, v224
	v_lshl_add_u32 v176, s36, 8, v1
	v_ashrrev_i32_e32 v163, 31, v162
	v_mov_b64_e32 v[142:143], s[14:15]
	v_ashrrev_i32_e32 v177, 31, v176
	v_mad_i64_i32 v[144:145], s[34:35], v176, s65, v[142:143]
	v_lshlrev_b64 v[166:167], 1, v[162:163]
	v_lshl_add_u64 v[138:139], v[176:177], 2, s[4:5]
	v_lshl_add_u64 v[140:141], v[162:163], 2, s[10:11]
	v_lshl_add_u64 v[144:145], v[144:145], 0, v[166:167]
	global_load_dword v182, v[138:139], off
	global_load_dwordx4 v[66:69], v[140:141], off
	global_load_dwordx4 v[62:65], v[140:141], off offset:16
	global_load_dwordx4 v[158:161], v[144:145], off nt
	v_lshlrev_b64 v[212:213], 13, v[176:177]
	v_lshl_add_u64 v[146:147], s[0:1], 0, v[212:213]
	v_lshl_add_u64 v[146:147], v[146:147], 0, v[166:167]
	global_load_dwordx4 v[186:189], v[146:147], off nt
	v_cvt_f32_i32_e32 v215, v57
	v_cvt_f32_i32_e32 v214, v56
	v_cvt_f32_i32_e32 v217, v55
	v_cvt_f32_i32_e32 v216, v54
	v_cvt_f32_i32_e32 v219, v53
	v_cvt_f32_i32_e32 v218, v52
	v_cvt_f32_i32_e32 v221, v51
	v_cvt_f32_i32_e32 v220, v50
	global_load_dword v184, v[138:139], off offset:64
	global_load_dword v178, v[138:139], off offset:128
	global_load_dword v174, v[138:139], off offset:192
	global_load_dword v172, v[138:139], off offset:512
	global_load_dword v170, v[138:139], off offset:576
	global_load_dword v168, v[138:139], off offset:640
	global_load_dword v164, v[138:139], off offset:704
	global_load_dwordx4 v[50:53], v[140:141], off offset:528
	global_load_dwordx4 v[54:57], v[140:141], off offset:512
	global_load_dwordx4 v[190:193], v[144:145], off offset:256 nt
	v_or_b32_e32 v180, 16, v176
	v_mad_i64_i32 v[142:143], s[34:35], v180, s65, v[142:143]
	v_lshl_add_u64 v[140:141], v[142:143], 0, v[166:167]
	global_load_dwordx4 v[154:157], v[140:141], off nt
	global_load_dwordx4 v[142:145], v[140:141], off offset:256 nt
	global_load_dwordx4 v[150:153], v[146:147], off offset:256 nt
	v_ashrrev_i32_e32 v181, 31, v180
	v_lshlrev_b64 v[138:139], 13, v[180:181]
	v_lshl_add_u64 v[138:139], s[0:1], 0, v[138:139]
	v_lshl_add_u64 v[138:139], v[138:139], 0, v[166:167]
	global_load_dwordx4 v[146:149], v[138:139], off nt
	s_nop 0
	global_load_dwordx4 v[138:141], v[138:139], off offset:256 nt
	v_cvt_f32_i32_e32 v135, v135
	v_cvt_f32_i32_e32 v134, v134
	v_cvt_f32_i32_e32 v137, v137
	v_cvt_f32_i32_e32 v136, v136
	v_cvt_f32_i32_e32 v131, v131
	v_cvt_f32_i32_e32 v130, v130
	v_cvt_f32_i32_e32 v133, v133
	v_cvt_f32_i32_e32 v132, v132
	s_waitcnt vmcnt(0)
	v_pk_mul_f32 v[222:223], v[182:183], v[68:69] op_sel_hi:[0,1]
	v_pk_mul_f32 v[230:231], v[182:183], v[66:67] op_sel_hi:[0,1]
	v_lshlrev_b32_e32 v165, 16, v158
	v_lshlrev_b32_e32 v169, 16, v159
	v_lshlrev_b32_e32 v171, 16, v160
	v_and_b32_e32 v160, 0xffff0000, v160
	v_lshlrev_b32_e32 v173, 16, v161
	v_and_b32_e32 v161, 0xffff0000, v161
	v_mul_f32_e32 v165, 0xbfb8aa3b, v165
	v_mul_f32_e32 v169, 0xbfb8aa3b, v169
	v_and_b32_e32 v159, 0xffff0000, v159
	v_mul_f32_e32 v160, 0xbfb8aa3b, v160
	v_mul_f32_e32 v175, 0xbfb8aa3b, v161
	v_exp_f32_e32 v161, v165
	v_exp_f32_e32 v165, v169
	v_and_b32_e32 v158, 0xffff0000, v158
	v_mul_f32_e32 v159, 0xbfb8aa3b, v159
	v_exp_f32_e32 v160, v160
	v_mul_f32_e32 v158, 0xbfb8aa3b, v158
	v_mul_f32_e32 v171, 0xbfb8aa3b, v171
	v_exp_f32_e32 v159, v159
	v_exp_f32_e32 v158, v158
	v_exp_f32_e32 v169, v171
	v_mul_f32_e32 v173, 0xbfb8aa3b, v173
	v_add_f32_e32 v165, 1.0, v165
	v_pk_mul_f32 v[232:233], v[182:183], v[64:65] op_sel_hi:[0,1]
	v_pk_mul_f32 v[234:235], v[182:183], v[62:63] op_sel_hi:[0,1]
	v_exp_f32_e32 v171, v173
	v_add_f32_e32 v183, 1.0, v160
	v_rcp_f32_e32 v160, v165
	v_exp_f32_e32 v165, v175
	v_add_f32_e32 v161, 1.0, v161
	v_add_f32_e32 v179, 1.0, v159
	v_add_f32_e32 v173, 1.0, v158
	v_add_f32_e32 v169, 1.0, v169
	v_rcp_f32_e32 v158, v161
	v_rcp_f32_e32 v161, v179
	v_pk_mul_f32 v[214:215], v[222:223], v[214:215]
	v_rcp_f32_e32 v159, v173
	v_rcp_f32_e32 v222, v169
	v_rcp_f32_e32 v223, v183
	v_add_f32_e32 v169, 1.0, v171
	v_add_f32_e32 v165, 1.0, v165
	v_pk_mul_f32 v[216:217], v[230:231], v[216:217]
	v_pk_mul_f32 v[218:219], v[232:233], v[218:219]
	v_rcp_f32_e32 v230, v169
	v_rcp_f32_e32 v231, v165
	v_lshlrev_b32_e32 v232, 16, v186
	v_and_b32_e32 v233, 0xffff0000, v186
	v_lshlrev_b32_e32 v186, 16, v187
	v_and_b32_e32 v187, 0xffff0000, v187
	v_pk_mul_f32 v[220:221], v[234:235], v[220:221]
	v_pk_fma_f32 v[160:161], v[214:215], v[160:161], v[186:187]
	v_lshlrev_b32_e32 v186, 16, v188
	v_and_b32_e32 v187, 0xffff0000, v188
	v_pk_fma_f32 v[158:159], v[216:217], v[158:159], v[232:233]
	v_pk_fma_f32 v[186:187], v[220:221], v[222:223], v[186:187]
	v_lshlrev_b32_e32 v188, 16, v189
	v_and_b32_e32 v189, 0xffff0000, v189
	v_cvt_pk_bf16_f32 v158, v158, v159
	v_cvt_pk_bf16_f32 v159, v160, v161
	v_cvt_pk_bf16_f32 v160, v186, v187
	v_lshl_add_u64 v[186:187], s[12:13], 0, v[212:213]
	v_pk_fma_f32 v[188:189], v[218:219], v[230:231], v[188:189]
	v_lshl_add_u64 v[186:187], v[186:187], 0, v[166:167]
	v_cvt_pk_bf16_f32 v161, v188, v189
	global_store_dwordx4 v[186:187], v[158:161], off
	v_lshlrev_b32_e32 v169, 16, v161
	v_lshlrev_b32_e32 v165, 16, v158
	v_and_b32_e32 v161, 0xffff0000, v161
	v_and_b32_e32 v158, 0xffff0000, v158
	v_max_f32_e64 v161, |v161|, |v161|
	v_max_f32_e64 v169, |v169|, |v169|
	v_max_f32_e64 v158, |v158|, |v158|
	v_max_f32_e64 v165, |v165|, |v165|
	v_max_f32_e32 v161, v169, v161
	v_lshlrev_b32_e32 v169, 16, v192
	v_max_f32_e32 v158, v165, v158
	v_lshlrev_b32_e32 v165, 16, v159
	v_and_b32_e32 v159, 0xffff0000, v159
	v_mul_f32_e32 v169, 0xbfb8aa3b, v169
	v_and_b32_e32 v171, 0xffff0000, v192
	v_max_f32_e64 v159, |v159|, |v159|
	v_max_f32_e64 v165, |v165|, |v165|
; __device__ __forceinline__ unsigned cvtpk(float lo, float hi) { unsigned r; asm volatile("v_cvt_pk_bf16_f32 %0, %1, %2" : "=v"(r) : "v"(lo), "v"(hi)); return r; }
;     __device__ __forceinline__ void operator()(const f32x4 (&acc)[2][2][4][2], const Unit& u, int wr, int wc, int fr, int fq) const {
;     ...
;                     if (MODE == 2 || MODE == 3) { const u32x4 g = gq[kb & 1][bj];
;                         f32x4 g0 = {sigmoidf_(bflo(g.x)), sigmoidf_(bfhi(g.x)), sigmoidf_(bflo(g.y)), sigmoidf_(bfhi(g.y))};
;                         f32x4 g1 = {sigmoidf_(bflo(g.z)), sigmoidf_(bfhi(g.z)), sigmoidf_(bflo(g.w)), sigmoidf_(bfhi(g.w))};
;                         v0 = v0 * g0; v1 = v1 * g1;
;                         if (MODE == 3) { const u32x4 q = aq[kb & 1][bj];
;                             v0 = v0 + (f32x4){bflo(q.x), bfhi(q.x), bflo(q.y), bfhi(q.y)}; v1 = v1 + (f32x4){bflo(q.z), bfhi(q.z), bflo(q.w), bfhi(q.w)}; } }
;                     if (MODE == 4) { v0 = v0 + rs[kb & 1][bj][0]; v1 = v1 + rs[kb & 1][bj][1]; }
;                     if (MODE == 5) { const u32x4 c = gq[kb & 1][bj], q = aq[kb & 1][bj];
;                         v0 = (f32x4){bflo(c.x) + sigmoidf_(v0[0]) * bflo(q.x), bfhi(c.x) + sigmoidf_(v0[1]) * bfhi(q.x), bflo(c.y) + sigmoidf_(v0[2]) * bflo(q.y), bfhi(c.y) + sigmoidf_(v0[3]) * bfhi(q.y)};
;                         v1 = (f32x4){bflo(c.z) + sigmoidf_(v1[0]) * bflo(q.z), bfhi(c.z) + sigmoidf_(v1[1]) * bfhi(q.z), bflo(c.w) + sigmoidf_(v1[2]) * bflo(q.w), bfhi(c.w) + sigmoidf_(v1[3]) * bfhi(q.w)}; }
;                     u32x4 w; w.x = cvtpk(v0[0], v0[1]); w.y = cvtpk(v0[2], v0[3]); w.z = cvtpk(v1[0], v1[1]); w.w = cvtpk(v1[2], v1[3]);
;                     *(u32x4*)(O + (size_t)row * ldo + col) = w;
;                     if (MODE == 0) { if (dual) { const int kc = col - ZC_KV;
;                         *(u32x4*)((bf16_t*)aux + (size_t)((kc >> 7) * 512 + (row >> 4)) * 2048 + (row & 15) * 128 + (kc & 127)) = w; } }
;                     if (RMAX) rmx = fmaxf(rmx, fmaxf(fmaxf(fmaxf(fabsf(bflo(w.x)), fabsf(bfhi(w.x))), fmaxf(fabsf(bflo(w.y)), fabsf(bfhi(w.y)))), fmaxf(fmaxf(fabsf(bflo(w.z)), fabsf(bfhi(w.z))), fmaxf(fabsf(bflo(w.w)), fabsf(bfhi(w.w)))))); }
;                 if (RMAX) { rmx = fmaxf(rmx, __shfl_xor(rmx, 16)); rmx = fmaxf(rmx, __shfl_xor(rmx, 32)); if (fq == 0) atomicMax(rowmax + row, __float_as_uint(rmx)); } } }
	v_exp_f32_e32 v169, v169
	v_mul_f32_e32 v171, 0xbfb8aa3b, v171
	v_max_f32_e32 v159, v165, v159
	v_lshlrev_b32_e32 v165, 16, v160
	v_and_b32_e32 v160, 0xffff0000, v160
	v_exp_f32_e32 v171, v171
	v_max3_f32 v160, |v165|, |v160|, v161
	v_max3_f32 v165, v158, v159, v160
	v_pk_mul_f32 v[160:161], v[182:183], v[54:55] op_sel_hi:[0,1]
	v_pk_mul_f32 v[158:159], v[182:183], v[56:57] op_sel_hi:[0,1]
	v_pk_mul_f32 v[188:189], v[182:183], v[52:53] op_sel_hi:[0,1]
	v_pk_mul_f32 v[182:183], v[182:183], v[50:51] op_sel_hi:[0,1]
	v_pk_mul_f32 v[134:135], v[160:161], v[134:135]
	v_lshlrev_b32_e32 v160, 16, v191
	v_and_b32_e32 v161, 0xffff0000, v191
	v_add_f32_e32 v169, 1.0, v169
	v_pk_mul_f32 v[136:137], v[158:159], v[136:137]
	v_pk_mul_f32 v[130:131], v[182:183], v[130:131]
	v_lshlrev_b32_e32 v158, 16, v190
	v_and_b32_e32 v159, 0xffff0000, v190
	v_mul_f32_e32 v160, 0xbfb8aa3b, v160
	v_mul_f32_e32 v161, 0xbfb8aa3b, v161
	v_rcp_f32_e32 v182, v169
	v_add_f32_e32 v169, 1.0, v171
	v_lshlrev_b32_e32 v171, 16, v193
	v_mul_f32_e32 v158, 0xbfb8aa3b, v158
	v_mul_f32_e32 v159, 0xbfb8aa3b, v159
	v_exp_f32_e32 v160, v160
	v_exp_f32_e32 v161, v161
	v_mul_f32_e32 v171, 0xbfb8aa3b, v171
	v_and_b32_e32 v173, 0xffff0000, v193
	v_exp_f32_e32 v158, v158
	v_exp_f32_e32 v159, v159
	v_exp_f32_e32 v171, v171
	v_mul_f32_e32 v173, 0xbfb8aa3b, v173
	v_exp_f32_e32 v173, v173
	v_add_f32_e32 v160, 1.0, v160
	v_add_f32_e32 v161, 1.0, v161
	v_add_f32_e32 v158, 1.0, v158
	v_add_f32_e32 v159, 1.0, v159
	v_rcp_f32_e32 v160, v160
	v_rcp_f32_e32 v161, v161
	v_rcp_f32_e32 v183, v169
	v_add_f32_e32 v169, 1.0, v171
	v_pk_mul_f32 v[132:133], v[188:189], v[132:133]
	v_rcp_f32_e32 v158, v158
	v_rcp_f32_e32 v159, v159
	v_rcp_f32_e32 v188, v169
	v_add_f32_e32 v169, 1.0, v173
	v_rcp_f32_e32 v189, v169
	v_lshlrev_b32_e32 v190, 16, v150
	v_and_b32_e32 v191, 0xffff0000, v150
	v_lshlrev_b32_e32 v150, 16, v151
	v_and_b32_e32 v151, 0xffff0000, v151
	v_pk_fma_f32 v[136:137], v[136:137], v[160:161], v[150:151]
	v_lshlrev_b32_e32 v150, 16, v152
	v_and_b32_e32 v151, 0xffff0000, v152
	v_pk_fma_f32 v[134:135], v[134:135], v[158:159], v[190:191]
	v_lshlrev_b32_e32 v152, 16, v153
	v_and_b32_e32 v153, 0xffff0000, v153
	v_pk_fma_f32 v[130:131], v[130:131], v[182:183], v[150:151]
	v_pk_fma_f32 v[152:153], v[132:133], v[188:189], v[152:153]
	v_cvt_pk_bf16_f32 v132, v134, v135
	v_cvt_pk_bf16_f32 v133, v136, v137
	v_cvt_pk_bf16_f32 v134, v130, v131
	s_nop 0
	v_lshlrev_b32_e32 v130, 16, v132
	v_and_b32_e32 v131, 0xffff0000, v132
	v_max_f32_e64 v131, |v131|, |v131|
	v_max_f32_e64 v130, |v130|, |v130|
	v_cvt_pk_bf16_f32 v135, v152, v153
	v_max_f32_e32 v130, v130, v131
	v_lshlrev_b32_e32 v131, 16, v133
	v_and_b32_e32 v136, 0xffff0000, v133
	v_lshlrev_b32_e32 v150, 16, v135
	v_and_b32_e32 v151, 0xffff0000, v135
	v_max_f32_e64 v136, |v136|, |v136|
	v_max_f32_e64 v131, |v131|, |v131|
	v_max_f32_e64 v151, |v151|, |v151|
	v_max_f32_e64 v150, |v150|, |v150|
	v_max_f32_e32 v131, v131, v136
	v_lshlrev_b32_e32 v136, 16, v134
	v_and_b32_e32 v137, 0xffff0000, v134
	v_max_f32_e32 v150, v150, v151
	v_max3_f32 v136, |v136|, |v137|, v150
	v_max3_f32 v130, v130, v131, v136
	v_and_b32_e32 v136, 64, v228
	v_xor_b32_e32 v131, 16, v228
	v_add_u32_e32 v136, 64, v136
	v_cmp_lt_i32_e32 vcc, v131, v136
	v_max3_f32 v130, v165, 0, v130
	global_store_dwordx4 v[186:187], v[132:135], off offset:256
	v_cndmask_b32_e32 v131, v228, v131, vcc
	v_lshlrev_b32_e32 v165, 2, v131
	ds_bpermute_b32 v131, v165, v130
	s_waitcnt lgkmcnt(0)
	v_max_f32_e32 v131, v131, v131
	v_max_f32_e32 v130, v130, v131
	v_xor_b32_e32 v131, 32, v228
	v_cmp_lt_i32_e32 vcc, v131, v136
	s_nop 1
	v_cndmask_b32_e32 v131, v228, v131, vcc
	v_lshlrev_b32_e32 v169, 2, v131
	ds_bpermute_b32 v131, v169, v130
	s_and_saveexec_b64 s[34:35], s[6:7]
	s_cbranch_execz .LBB0_1032
	s_waitcnt lgkmcnt(0)
	v_max_f32_e32 v131, v131, v131
	v_max_f32_e32 v130, v130, v130
	v_lshl_add_u64 v[132:133], v[176:177], 2, s[16:17]
	v_max_f32_e32 v130, v130, v131
	global_atomic_umax v[132:133], v130, off
.LBB0_1032:
	s_or_b64 exec, exec, s[34:35]
	v_or_b32_e32 v182, 32, v176
	v_ashrrev_i32_e32 v183, 31, v182
	s_waitcnt lgkmcnt(0)
	v_mov_b64_e32 v[130:131], s[14:15]
	v_lshlrev_b64 v[132:133], 13, v[182:183]
	v_mad_i64_i32 v[130:131], s[34:35], v182, s65, v[130:131]
	v_lshl_add_u64 v[132:133], s[0:1], 0, v[132:133]
	v_lshl_add_u64 v[130:131], v[130:131], 0, v[166:167]
	v_lshl_add_u64 v[132:133], v[132:133], 0, v[166:167]
	global_load_dwordx4 v[158:161], v[130:131], off nt
	global_load_dwordx4 v[134:137], v[130:131], off offset:256 nt
	global_load_dwordx4 v[150:153], v[132:133], off nt
	s_nop 0
	global_load_dwordx4 v[130:133], v[132:133], off offset:256 nt
	v_lshlrev_b32_e32 v171, 16, v154
	v_and_b32_e32 v154, 0xffff0000, v154
	v_mul_f32_e32 v171, 0xbfb8aa3b, v171
	v_mul_f32_e32 v154, 0xbfb8aa3b, v154
	v_exp_f32_e32 v171, v171
	v_exp_f32_e32 v173, v154
	v_cvt_f32_i32_e32 v129, v129
	v_cvt_f32_i32_e32 v128, v128
	v_add_f32_e32 v154, 1.0, v171
	v_add_f32_e32 v171, 1.0, v173
	v_lshlrev_b32_e32 v173, 16, v155
	v_mul_f32_e32 v173, 0xbfb8aa3b, v173
	v_exp_f32_e32 v173, v173
	v_and_b32_e32 v155, 0xffff0000, v155
	v_mul_f32_e32 v155, 0xbfb8aa3b, v155
	v_exp_f32_e32 v175, v155
	v_rcp_f32_e32 v155, v171
	v_add_f32_e32 v171, 1.0, v173
	v_lshlrev_b32_e32 v173, 16, v156
	v_mul_f32_e32 v173, 0xbfb8aa3b, v173
	v_exp_f32_e32 v173, v173
	v_and_b32_e32 v156, 0xffff0000, v156
	v_pk_mul_f32 v[188:189], v[184:185], v[68:69] op_sel_hi:[0,1]
	v_mul_f32_e32 v156, 0xbfb8aa3b, v156
	v_pk_mul_f32 v[128:129], v[188:189], v[128:129]
	v_rcp_f32_e32 v188, v171
	v_add_f32_e32 v171, 1.0, v175
	v_exp_f32_e32 v175, v156
	v_add_f32_e32 v156, 1.0, v173
; __device__ __forceinline__ unsigned cvtpk(float lo, float hi) { unsigned r; asm volatile("v_cvt_pk_bf16_f32 %0, %1, %2" : "=v"(r) : "v"(lo), "v"(hi)); return r; }
;     __device__ __forceinline__ void operator()(const f32x4 (&acc)[2][2][4][2], const Unit& u, int wr, int wc, int fr, int fq) const {
;     ...
;                     if (MODE == 2 || MODE == 3) { const u32x4 g = gq[kb & 1][bj];
;                         f32x4 g0 = {sigmoidf_(bflo(g.x)), sigmoidf_(bfhi(g.x)), sigmoidf_(bflo(g.y)), sigmoidf_(bfhi(g.y))};
;                         f32x4 g1 = {sigmoidf_(bflo(g.z)), sigmoidf_(bfhi(g.z)), sigmoidf_(bflo(g.w)), sigmoidf_(bfhi(g.w))};
;                         v0 = v0 * g0; v1 = v1 * g1;
;                         if (MODE == 3) { const u32x4 q = aq[kb & 1][bj];
;                             v0 = v0 + (f32x4){bflo(q.x), bfhi(q.x), bflo(q.y), bfhi(q.y)}; v1 = v1 + (f32x4){bflo(q.z), bfhi(q.z), bflo(q.w), bfhi(q.w)}; } }
;                     if (MODE == 4) { v0 = v0 + rs[kb & 1][bj][0]; v1 = v1 + rs[kb & 1][bj][1]; }
;                     if (MODE == 5) { const u32x4 c = gq[kb & 1][bj], q = aq[kb & 1][bj];
;                         v0 = (f32x4){bflo(c.x) + sigmoidf_(v0[0]) * bflo(q.x), bfhi(c.x) + sigmoidf_(v0[1]) * bfhi(q.x), bflo(c.y) + sigmoidf_(v0[2]) * bflo(q.y), bfhi(c.y) + sigmoidf_(v0[3]) * bfhi(q.y)};
;                         v1 = (f32x4){bflo(c.z) + sigmoidf_(v1[0]) * bflo(q.z), bfhi(c.z) + sigmoidf_(v1[1]) * bfhi(q.z), bflo(c.w) + sigmoidf_(v1[2]) * bflo(q.w), bfhi(c.w) + sigmoidf_(v1[3]) * bfhi(q.w)}; }
;                     u32x4 w; w.x = cvtpk(v0[0], v0[1]); w.y = cvtpk(v0[2], v0[3]); w.z = cvtpk(v1[0], v1[1]); w.w = cvtpk(v1[2], v1[3]);
;                     *(u32x4*)(O + (size_t)row * ldo + col) = w;
;                     if (MODE == 0) { if (dual) { const int kc = col - ZC_KV;
;                         *(u32x4*)((bf16_t*)aux + (size_t)((kc >> 7) * 512 + (row >> 4)) * 2048 + (row & 15) * 128 + (kc & 127)) = w; } }
;                     if (RMAX) rmx = fmaxf(rmx, fmaxf(fmaxf(fmaxf(fabsf(bflo(w.x)), fabsf(bfhi(w.x))), fmaxf(fabsf(bflo(w.y)), fabsf(bfhi(w.y)))), fmaxf(fmaxf(fabsf(bflo(w.z)), fabsf(bfhi(w.z))), fmaxf(fabsf(bflo(w.w)), fabsf(bfhi(w.w)))))); }
;                 if (RMAX) { rmx = fmaxf(rmx, __shfl_xor(rmx, 16)); rmx = fmaxf(rmx, __shfl_xor(rmx, 32)); if (fq == 0) atomicMax(rowmax + row, __float_as_uint(rmx)); } } }
	v_lshlrev_b32_e32 v173, 16, v157
	v_mul_f32_e32 v173, 0xbfb8aa3b, v173
	v_and_b32_e32 v157, 0xffff0000, v157
	v_exp_f32_e32 v173, v173
	v_mul_f32_e32 v157, 0xbfb8aa3b, v157
	v_cvt_f32_i32_e32 v127, v127
	v_cvt_f32_i32_e32 v126, v126
	v_rcp_f32_e32 v189, v171
	v_add_f32_e32 v171, 1.0, v175
	v_exp_f32_e32 v175, v157
	v_pk_mul_f32 v[190:191], v[184:185], v[66:67] op_sel_hi:[0,1]
	v_cvt_f32_i32_e32 v125, v125
	v_cvt_f32_i32_e32 v124, v124
	v_rcp_f32_e32 v157, v171
	v_add_f32_e32 v171, 1.0, v173
	v_pk_mul_f32 v[126:127], v[190:191], v[126:127]
	v_cvt_f32_i32_e32 v123, v123
	v_cvt_f32_i32_e32 v122, v122
	v_rcp_f32_e32 v154, v154
	v_rcp_f32_e32 v190, v171
	v_add_f32_e32 v171, 1.0, v175
	v_rcp_f32_e32 v156, v156
	v_rcp_f32_e32 v191, v171
	v_pk_mul_f32 v[192:193], v[184:185], v[64:65] op_sel_hi:[0,1]
	v_pk_mul_f32 v[212:213], v[184:185], v[62:63] op_sel_hi:[0,1]
	v_pk_mul_f32 v[124:125], v[192:193], v[124:125]
	v_lshlrev_b32_e32 v192, 16, v146
	v_and_b32_e32 v193, 0xffff0000, v146
	v_lshlrev_b32_e32 v146, 16, v147
	v_and_b32_e32 v147, 0xffff0000, v147
	v_lshlrev_b64 v[186:187], 12, v[180:181]
	v_pk_mul_f32 v[122:123], v[212:213], v[122:123]
	v_pk_fma_f32 v[128:129], v[128:129], v[188:189], v[146:147]
	v_pk_fma_f32 v[126:127], v[126:127], v[154:155], v[192:193]
	v_lshlrev_b32_e32 v146, 16, v148
	v_and_b32_e32 v147, 0xffff0000, v148
	v_lshlrev_b32_e32 v148, 16, v149
	v_and_b32_e32 v149, 0xffff0000, v149
	v_pk_fma_f32 v[148:149], v[124:125], v[190:191], v[148:149]
	v_pk_fma_f32 v[124:125], v[122:123], v[156:157], v[146:147]
	v_cvt_pk_bf16_f32 v122, v126, v127
	v_lshl_add_u64 v[126:127], v[186:187], 1, s[12:13]
	v_lshl_add_u64 v[126:127], v[126:127], 0, v[166:167]
	v_cvt_pk_bf16_f32 v123, v128, v129
	v_cvt_pk_bf16_f32 v124, v124, v125
	v_cvt_pk_bf16_f32 v125, v148, v149
	global_store_dwordx4 v[126:127], v[122:125], off
	v_lshlrev_b32_e32 v128, 16, v122
	v_max_f32_e64 v128, |v128|, |v128|
	v_and_b32_e32 v122, 0xffff0000, v122
	v_max_f32_e64 v122, |v122|, |v122|
	v_max_f32_e32 v122, v128, v122
	v_lshlrev_b32_e32 v128, 16, v123
	v_and_b32_e32 v123, 0xffff0000, v123
	v_lshlrev_b32_e32 v129, 16, v125
	v_and_b32_e32 v125, 0xffff0000, v125
	v_max_f32_e64 v123, |v123|, |v123|
	v_max_f32_e64 v128, |v128|, |v128|
	v_max_f32_e64 v125, |v125|, |v125|
	v_max_f32_e64 v129, |v129|, |v129|
	v_cvt_f32_i32_e32 v121, v121
	v_cvt_f32_i32_e32 v120, v120
	v_max_f32_e32 v123, v128, v123
	v_lshlrev_b32_e32 v128, 16, v124
	v_and_b32_e32 v124, 0xffff0000, v124
	v_max_f32_e32 v125, v129, v125
	v_cvt_f32_i32_e32 v119, v119
	v_cvt_f32_i32_e32 v118, v118
	v_cvt_f32_i32_e32 v117, v117
	v_cvt_f32_i32_e32 v116, v116
	v_max3_f32 v124, |v128|, |v124|, v125
	v_max3_f32 v148, v122, v123, v124
	v_pk_mul_f32 v[122:123], v[184:185], v[56:57] op_sel_hi:[0,1]
	v_pk_mul_f32 v[124:125], v[184:185], v[54:55] op_sel_hi:[0,1]
	v_pk_mul_f32 v[128:129], v[184:185], v[52:53] op_sel_hi:[0,1]
	v_pk_mul_f32 v[120:121], v[122:123], v[120:121]
	v_lshlrev_b32_e32 v122, 16, v142
	v_and_b32_e32 v123, 0xffff0000, v142
	v_pk_mul_f32 v[118:119], v[124:125], v[118:119]
	v_mul_f32_e32 v122, 0xbfb8aa3b, v122
	v_mul_f32_e32 v123, 0xbfb8aa3b, v123
	v_pk_mul_f32 v[116:117], v[128:129], v[116:117]
	v_lshlrev_b32_e32 v124, 16, v143
	v_and_b32_e32 v125, 0xffff0000, v143
	v_lshlrev_b32_e32 v128, 16, v144
	v_and_b32_e32 v129, 0xffff0000, v144
	v_exp_f32_e32 v122, v122
	v_exp_f32_e32 v123, v123
	v_mul_f32_e32 v124, 0xbfb8aa3b, v124
	v_mul_f32_e32 v125, 0xbfb8aa3b, v125
	v_mul_f32_e32 v128, 0xbfb8aa3b, v128
	v_mul_f32_e32 v129, 0xbfb8aa3b, v129
	v_lshlrev_b32_e32 v142, 16, v145
	v_and_b32_e32 v143, 0xffff0000, v145
	v_exp_f32_e32 v124, v124
	v_exp_f32_e32 v125, v125
	v_exp_f32_e32 v128, v128
	v_exp_f32_e32 v129, v129
	v_mul_f32_e32 v142, 0xbfb8aa3b, v142
	v_mul_f32_e32 v143, 0xbfb8aa3b, v143
	v_exp_f32_e32 v142, v142
	v_exp_f32_e32 v143, v143
	v_add_f32_e32 v122, 1.0, v122
	v_add_f32_e32 v123, 1.0, v123
	v_cvt_f32_i32_e32 v115, v115
	v_cvt_f32_i32_e32 v114, v114
	v_rcp_f32_e32 v122, v122
	v_rcp_f32_e32 v123, v123
	v_add_f32_e32 v124, 1.0, v124
	v_add_f32_e32 v125, 1.0, v125
	v_add_f32_e32 v128, 1.0, v128
	v_add_f32_e32 v129, 1.0, v129
	v_rcp_f32_e32 v124, v124
	v_rcp_f32_e32 v125, v125
	v_rcp_f32_e32 v128, v128
	v_rcp_f32_e32 v129, v129
	v_add_f32_e32 v142, 1.0, v142
	v_add_f32_e32 v143, 1.0, v143
	v_rcp_f32_e32 v142, v142
	v_rcp_f32_e32 v143, v143
	v_pk_mul_f32 v[146:147], v[184:185], v[50:51] op_sel_hi:[0,1]
	v_lshlrev_b32_e32 v144, 16, v138
	v_and_b32_e32 v145, 0xffff0000, v138
	v_pk_mul_f32 v[114:115], v[146:147], v[114:115]
	v_lshlrev_b32_e32 v138, 16, v139
	v_and_b32_e32 v139, 0xffff0000, v139
	v_pk_fma_f32 v[118:119], v[118:119], v[122:123], v[144:145]
	v_lshlrev_b32_e32 v122, 16, v140
	v_and_b32_e32 v123, 0xffff0000, v140
	v_pk_fma_f32 v[120:121], v[120:121], v[124:125], v[138:139]
	v_lshlrev_b32_e32 v124, 16, v141
	v_and_b32_e32 v125, 0xffff0000, v141
	v_pk_fma_f32 v[114:115], v[114:115], v[128:129], v[122:123]
	v_pk_fma_f32 v[124:125], v[116:117], v[142:143], v[124:125]
	v_cvt_pk_bf16_f32 v116, v118, v119
	v_cvt_pk_bf16_f32 v117, v120, v121
	v_cvt_pk_bf16_f32 v118, v114, v115
	s_nop 0
	v_lshlrev_b32_e32 v114, 16, v116
	v_and_b32_e32 v115, 0xffff0000, v116
	v_max_f32_e64 v115, |v115|, |v115|
	v_max_f32_e64 v114, |v114|, |v114|
	v_cvt_pk_bf16_f32 v119, v124, v125
	v_max_f32_e32 v114, v114, v115
	v_lshlrev_b32_e32 v115, 16, v117
	v_and_b32_e32 v120, 0xffff0000, v117
	v_lshlrev_b32_e32 v122, 16, v119
	v_and_b32_e32 v123, 0xffff0000, v119
	v_max_f32_e64 v120, |v120|, |v120|
	v_max_f32_e64 v115, |v115|, |v115|
	v_max_f32_e64 v123, |v123|, |v123|
	v_max_f32_e64 v122, |v122|, |v122|
	v_max_f32_e32 v115, v115, v120
	v_lshlrev_b32_e32 v120, 16, v118
	v_and_b32_e32 v121, 0xffff0000, v118
	v_max_f32_e32 v122, v122, v123
	v_max3_f32 v120, |v120|, |v121|, v122
	v_max3_f32 v114, v114, v115, v120
	v_max3_f32 v114, v148, 0, v114
	ds_bpermute_b32 v115, v165, v114
	global_store_dwordx4 v[126:127], v[116:119], off offset:256
	s_waitcnt lgkmcnt(0)
	v_max_f32_e32 v115, v115, v115
	v_max_f32_e32 v114, v114, v115
	ds_bpermute_b32 v115, v169, v114
	s_and_saveexec_b64 s[34:35], s[6:7]
	s_cbranch_execz .LBB0_1034
	s_waitcnt lgkmcnt(0)
	v_max_f32_e32 v115, v115, v115
	v_max_f32_e32 v114, v114, v114
	v_lshl_add_u64 v[116:117], v[180:181], 2, s[16:17]
	v_max_f32_e32 v114, v114, v115
	global_atomic_umax v[116:117], v114, off
;     __device__ __forceinline__ void operator()(const f32x4 (&acc)[2][2][4][2], const Unit& u, int wr, int wc, int fr, int fq) const {
;     ...
;         EPB_LOAD(0);
; #pragma unroll
;         for (int kb = 0; kb < 8; ++kb) { const int ai = kb >> 2, m = kb & 3;
;             if (kb < 7) EPB_LOAD(kb + 1);
;             { const int row = row0 + ai * HALF + m * 16; float rmx = 0.f;
; #pragma unroll
;                 for (int bj = 0; bj < 2; ++bj) { const int col = col0 + bj * HALF; f32x4 v0 = acc[ai][bj][m][0], v1 = acc[ai][bj][m][1];
;                     if (QI8) { const f32x4 c0 = cb[bj][0] * ra[ai][m], c1 = cb[bj][1] * ra[ai][m]; const i32x4 i0 = __builtin_bit_cast(i32x4, v0), i1 = __builtin_bit_cast(i32x4, v1);
;                         v0 = (f32x4){(float)i0[0], (float)i0[1], (float)i0[2], (float)i0[3]} * c0; v1 = (f32x4){(float)i1[0], (float)i1[1], (float)i1[2], (float)i1[3]} * c1; }
;                     else if (MODE == 0) { v0 = v0 * tsc; v1 = v1 * tsc; }
;                     if (!QI8 && MODE == 1) { v0 = v0 * cb[bj][0]; v1 = v1 * cb[bj][1]; }
;                     if (MODE == 2 || MODE == 3) { const u32x4 g = gq[kb & 1][bj];
;                         f32x4 g0 = {sigmoidf_(bflo(g.x)), sigmoidf_(bfhi(g.x)), sigmoidf_(bflo(g.y)), sigmoidf_(bfhi(g.y))};
;                         f32x4 g1 = {sigmoidf_(bflo(g.z)), sigmoidf_(bfhi(g.z)), sigmoidf_(bflo(g.w)), sigmoidf_(bfhi(g.w))};
;                         v0 = v0 * g0; v1 = v1 * g1;
;                         if (MODE == 3) { const u32x4 q = aq[kb & 1][bj];
;                             v0 = v0 + (f32x4){bflo(q.x), bfhi(q.x), bflo(q.y), bfhi(q.y)}; v1 = v1 + (f32x4){bflo(q.z), bfhi(q.z), bflo(q.w), bfhi(q.w)}; } }
;                     if (MODE == 4) { v0 = v0 + rs[kb & 1][bj][0]; v1 = v1 + rs[kb & 1][bj][1]; }
;                     if (MODE == 5) { const u32x4 c = gq[kb & 1][bj], q = aq[kb & 1][bj];
;                         v0 = (f32x4){bflo(c.x) + sigmoidf_(v0[0]) * bflo(q.x), bfhi(c.x) + sigmoidf_(v0[1]) * bfhi(q.x), bflo(c.y) + sigmoidf_(v0[2]) * bflo(q.y), bfhi(c.y) + sigmoidf_(v0[3]) * bfhi(q.y)};
;                         v1 = (f32x4){bflo(c.z) + sigmoidf_(v1[0]) * bflo(q.z), bfhi(c.z) + sigmoidf_(v1[1]) * bfhi(q.z), bflo(c.w) + sigmoidf_(v1[2]) * bflo(q.w), bfhi(c.w) + sigmoidf_(v1[3]) * bfhi(q.w)}; }
.LBB0_1034:
	s_or_b64 exec, exec, s[34:35]
	v_or_b32_e32 v138, 48, v176
	v_ashrrev_i32_e32 v139, 31, v138
	s_waitcnt lgkmcnt(0)
	v_mov_b64_e32 v[114:115], s[14:15]
	v_lshlrev_b64 v[116:117], 13, v[138:139]
	v_mad_i64_i32 v[114:115], s[34:35], v138, s65, v[114:115]
	v_lshl_add_u64 v[116:117], s[0:1], 0, v[116:117]
	v_lshl_add_u64 v[114:115], v[114:115], 0, v[166:167]
	v_lshl_add_u64 v[116:117], v[116:117], 0, v[166:167]
	global_load_dwordx4 v[126:129], v[114:115], off nt
	global_load_dwordx4 v[118:121], v[114:115], off offset:256 nt
	global_load_dwordx4 v[122:125], v[116:117], off nt
	s_nop 0
	global_load_dwordx4 v[114:117], v[116:117], off offset:256 nt
	v_cvt_f32_i32_e32 v111, v111
	v_cvt_f32_i32_e32 v110, v110
	v_cvt_f32_i32_e32 v113, v113
	v_cvt_f32_i32_e32 v112, v112
	v_cvt_f32_i32_e32 v107, v107
	v_cvt_f32_i32_e32 v106, v106
	v_cvt_f32_i32_e32 v109, v109
	v_cvt_f32_i32_e32 v108, v108
	v_pk_mul_f32 v[142:143], v[178:179], v[68:69] op_sel_hi:[0,1]
	v_pk_mul_f32 v[144:145], v[178:179], v[66:67] op_sel_hi:[0,1]
	v_pk_mul_f32 v[146:147], v[178:179], v[64:65] op_sel_hi:[0,1]
	v_pk_mul_f32 v[148:149], v[178:179], v[62:63] op_sel_hi:[0,1]
	v_pk_mul_f32 v[110:111], v[144:145], v[110:111]
	v_pk_mul_f32 v[112:113], v[142:143], v[112:113]
	s_waitcnt vmcnt(9)
	v_lshlrev_b32_e32 v142, 16, v158
	v_and_b32_e32 v143, 0xffff0000, v158
	v_lshlrev_b32_e32 v144, 16, v159
	v_and_b32_e32 v145, 0xffff0000, v159
	v_pk_mul_f32 v[106:107], v[148:149], v[106:107]
	v_mul_f32_e32 v142, 0xbfb8aa3b, v142
	v_mul_f32_e32 v143, 0xbfb8aa3b, v143
	v_pk_mul_f32 v[108:109], v[146:147], v[108:109]
	v_mul_f32_e32 v144, 0xbfb8aa3b, v144
	v_mul_f32_e32 v145, 0xbfb8aa3b, v145
	v_lshlrev_b32_e32 v146, 16, v160
	v_and_b32_e32 v147, 0xffff0000, v160
	v_lshlrev_b32_e32 v148, 16, v161
	v_and_b32_e32 v149, 0xffff0000, v161
	v_exp_f32_e32 v142, v142
	v_exp_f32_e32 v143, v143
	v_exp_f32_e32 v144, v144
	v_exp_f32_e32 v145, v145
	v_mul_f32_e32 v146, 0xbfb8aa3b, v146
	v_mul_f32_e32 v147, 0xbfb8aa3b, v147
	v_mul_f32_e32 v148, 0xbfb8aa3b, v148
	v_mul_f32_e32 v149, 0xbfb8aa3b, v149
	v_exp_f32_e32 v146, v146
	v_exp_f32_e32 v147, v147
	v_exp_f32_e32 v148, v148
	v_exp_f32_e32 v149, v149
	v_add_f32_e32 v142, 1.0, v142
	v_add_f32_e32 v143, 1.0, v143
	v_add_f32_e32 v144, 1.0, v144
	v_add_f32_e32 v145, 1.0, v145
	v_rcp_f32_e32 v142, v142
	v_rcp_f32_e32 v143, v143
	v_rcp_f32_e32 v144, v144
	v_rcp_f32_e32 v145, v145
	v_add_f32_e32 v146, 1.0, v146
	v_add_f32_e32 v147, 1.0, v147
	v_add_f32_e32 v148, 1.0, v148
	v_add_f32_e32 v149, 1.0, v149
	v_rcp_f32_e32 v146, v146
	v_rcp_f32_e32 v147, v147
	v_rcp_f32_e32 v148, v148
	v_rcp_f32_e32 v149, v149
	s_waitcnt vmcnt(7)
	v_lshlrev_b32_e32 v154, 16, v150
	v_and_b32_e32 v155, 0xffff0000, v150
	v_lshlrev_b32_e32 v150, 16, v151
	v_and_b32_e32 v151, 0xffff0000, v151
	v_lshlrev_b64 v[140:141], 12, v[182:183]
	v_pk_fma_f32 v[112:113], v[112:113], v[144:145], v[150:151]
	v_pk_fma_f32 v[110:111], v[110:111], v[142:143], v[154:155]
	v_lshlrev_b32_e32 v142, 16, v152
	v_and_b32_e32 v143, 0xffff0000, v152
	v_lshlrev_b32_e32 v144, 16, v153
	v_and_b32_e32 v145, 0xffff0000, v153
	v_pk_fma_f32 v[144:145], v[108:109], v[148:149], v[144:145]
	v_pk_fma_f32 v[108:109], v[106:107], v[146:147], v[142:143]
	v_cvt_pk_bf16_f32 v106, v110, v111
	v_lshl_add_u64 v[110:111], v[140:141], 1, s[12:13]
	v_lshl_add_u64 v[110:111], v[110:111], 0, v[166:167]
	v_cvt_pk_bf16_f32 v107, v112, v113
	v_cvt_pk_bf16_f32 v108, v108, v109
	v_cvt_pk_bf16_f32 v109, v144, v145
	global_store_dwordx4 v[110:111], v[106:109], off
	v_lshlrev_b32_e32 v112, 16, v106
	v_max_f32_e64 v112, |v112|, |v112|
	v_and_b32_e32 v106, 0xffff0000, v106
	v_max_f32_e64 v106, |v106|, |v106|
	v_max_f32_e32 v106, v112, v106
	v_lshlrev_b32_e32 v112, 16, v107
	v_and_b32_e32 v107, 0xffff0000, v107
	v_lshlrev_b32_e32 v113, 16, v109
	v_and_b32_e32 v109, 0xffff0000, v109
	v_max_f32_e64 v107, |v107|, |v107|
	v_max_f32_e64 v112, |v112|, |v112|
	v_max_f32_e64 v109, |v109|, |v109|
	v_max_f32_e64 v113, |v113|, |v113|
	v_cvt_f32_i32_e32 v105, v105
	v_cvt_f32_i32_e32 v104, v104
	v_max_f32_e32 v107, v112, v107
	v_lshlrev_b32_e32 v112, 16, v108
	v_and_b32_e32 v108, 0xffff0000, v108
	v_max_f32_e32 v109, v113, v109
	v_cvt_f32_i32_e32 v103, v103
	v_cvt_f32_i32_e32 v102, v102
	v_cvt_f32_i32_e32 v101, v101
	v_cvt_f32_i32_e32 v100, v100
	v_max3_f32 v108, |v112|, |v108|, v109
	v_max3_f32 v142, v106, v107, v108
	v_pk_mul_f32 v[106:107], v[178:179], v[56:57] op_sel_hi:[0,1]
	v_pk_mul_f32 v[108:109], v[178:179], v[54:55] op_sel_hi:[0,1]
	v_pk_mul_f32 v[112:113], v[178:179], v[52:53] op_sel_hi:[0,1]
	v_pk_mul_f32 v[104:105], v[106:107], v[104:105]
	v_lshlrev_b32_e32 v106, 16, v134
	v_and_b32_e32 v107, 0xffff0000, v134
	v_pk_mul_f32 v[102:103], v[108:109], v[102:103]
	v_mul_f32_e32 v106, 0xbfb8aa3b, v106
	v_mul_f32_e32 v107, 0xbfb8aa3b, v107
	v_pk_mul_f32 v[100:101], v[112:113], v[100:101]
	v_lshlrev_b32_e32 v108, 16, v135
	v_and_b32_e32 v109, 0xffff0000, v135
	v_lshlrev_b32_e32 v112, 16, v136
	v_and_b32_e32 v113, 0xffff0000, v136
	v_exp_f32_e32 v106, v106
	v_exp_f32_e32 v107, v107
	v_mul_f32_e32 v108, 0xbfb8aa3b, v108
	v_mul_f32_e32 v109, 0xbfb8aa3b, v109
	v_mul_f32_e32 v112, 0xbfb8aa3b, v112
	v_mul_f32_e32 v113, 0xbfb8aa3b, v113
	v_lshlrev_b32_e32 v134, 16, v137
	v_and_b32_e32 v135, 0xffff0000, v137
	v_exp_f32_e32 v108, v108
	v_exp_f32_e32 v109, v109
	v_exp_f32_e32 v112, v112
	v_exp_f32_e32 v113, v113
	v_mul_f32_e32 v134, 0xbfb8aa3b, v134
	v_mul_f32_e32 v135, 0xbfb8aa3b, v135
	v_exp_f32_e32 v134, v134
	v_exp_f32_e32 v135, v135
	v_add_f32_e32 v106, 1.0, v106
	v_add_f32_e32 v107, 1.0, v107
	v_cvt_f32_i32_e32 v99, v99
	v_cvt_f32_i32_e32 v98, v98
	v_rcp_f32_e32 v106, v106
	v_rcp_f32_e32 v107, v107
	v_add_f32_e32 v108, 1.0, v108
	v_add_f32_e32 v109, 1.0, v109
	v_add_f32_e32 v112, 1.0, v112
	v_add_f32_e32 v113, 1.0, v113
	v_rcp_f32_e32 v108, v108
	v_rcp_f32_e32 v109, v109
	v_rcp_f32_e32 v112, v112
	v_rcp_f32_e32 v113, v113
	v_add_f32_e32 v134, 1.0, v134
	v_add_f32_e32 v135, 1.0, v135
	v_rcp_f32_e32 v134, v134
	v_rcp_f32_e32 v135, v135
	v_pk_mul_f32 v[140:141], v[178:179], v[50:51] op_sel_hi:[0,1]
	s_waitcnt vmcnt(7)
;     __device__ __forceinline__ void operator()(const f32x4 (&acc)[2][2][4][2], const Unit& u, int wr, int wc, int fr, int fq) const {
;     ...
;         EPB_LOAD(0);
; #pragma unroll
;         for (int kb = 0; kb < 8; ++kb) { const int ai = kb >> 2, m = kb & 3;
;             if (kb < 7) EPB_LOAD(kb + 1);
;             { const int row = row0 + ai * HALF + m * 16; float rmx = 0.f;
; #pragma unroll
;                 for (int bj = 0; bj < 2; ++bj) { const int col = col0 + bj * HALF; f32x4 v0 = acc[ai][bj][m][0], v1 = acc[ai][bj][m][1];
;                     if (QI8) { const f32x4 c0 = cb[bj][0] * ra[ai][m], c1 = cb[bj][1] * ra[ai][m]; const i32x4 i0 = __builtin_bit_cast(i32x4, v0), i1 = __builtin_bit_cast(i32x4, v1);
;                         v0 = (f32x4){(float)i0[0], (float)i0[1], (float)i0[2], (float)i0[3]} * c0; v1 = (f32x4){(float)i1[0], (float)i1[1], (float)i1[2], (float)i1[3]} * c1; }
;                     else if (MODE == 0) { v0 = v0 * tsc; v1 = v1 * tsc; }
;                     if (!QI8 && MODE == 1) { v0 = v0 * cb[bj][0]; v1 = v1 * cb[bj][1]; }
;                     if (MODE == 2 || MODE == 3) { const u32x4 g = gq[kb & 1][bj];
;                         f32x4 g0 = {sigmoidf_(bflo(g.x)), sigmoidf_(bfhi(g.x)), sigmoidf_(bflo(g.y)), sigmoidf_(bfhi(g.y))};
;                         f32x4 g1 = {sigmoidf_(bflo(g.z)), sigmoidf_(bfhi(g.z)), sigmoidf_(bflo(g.w)), sigmoidf_(bfhi(g.w))};
;                         v0 = v0 * g0; v1 = v1 * g1;
;                         if (MODE == 3) { const u32x4 q = aq[kb & 1][bj];
;                             v0 = v0 + (f32x4){bflo(q.x), bfhi(q.x), bflo(q.y), bfhi(q.y)}; v1 = v1 + (f32x4){bflo(q.z), bfhi(q.z), bflo(q.w), bfhi(q.w)}; } }
;                     if (MODE == 4) { v0 = v0 + rs[kb & 1][bj][0]; v1 = v1 + rs[kb & 1][bj][1]; }
;                     if (MODE == 5) { const u32x4 c = gq[kb & 1][bj], q = aq[kb & 1][bj];
;                         v0 = (f32x4){bflo(c.x) + sigmoidf_(v0[0]) * bflo(q.x), bfhi(c.x) + sigmoidf_(v0[1]) * bfhi(q.x), bflo(c.y) + sigmoidf_(v0[2]) * bflo(q.y), bfhi(c.y) + sigmoidf_(v0[3]) * bfhi(q.y)};
;                         v1 = (f32x4){bflo(c.z) + sigmoidf_(v1[0]) * bflo(q.z), bfhi(c.z) + sigmoidf_(v1[1]) * bfhi(q.z), bflo(c.w) + sigmoidf_(v1[2]) * bflo(q.w), bfhi(c.w) + sigmoidf_(v1[3]) * bfhi(q.w)}; }
	v_lshlrev_b32_e32 v136, 16, v130
	v_and_b32_e32 v137, 0xffff0000, v130
	v_pk_mul_f32 v[98:99], v[140:141], v[98:99]
	v_lshlrev_b32_e32 v130, 16, v131
	v_and_b32_e32 v131, 0xffff0000, v131
	v_pk_fma_f32 v[102:103], v[102:103], v[106:107], v[136:137]
	v_lshlrev_b32_e32 v106, 16, v132
	v_and_b32_e32 v107, 0xffff0000, v132
	v_pk_fma_f32 v[104:105], v[104:105], v[108:109], v[130:131]
	v_lshlrev_b32_e32 v108, 16, v133
	v_and_b32_e32 v109, 0xffff0000, v133
	v_pk_fma_f32 v[98:99], v[98:99], v[112:113], v[106:107]
	v_pk_fma_f32 v[108:109], v[100:101], v[134:135], v[108:109]
	v_cvt_pk_bf16_f32 v100, v102, v103
	v_cvt_pk_bf16_f32 v101, v104, v105
	v_cvt_pk_bf16_f32 v102, v98, v99
	s_nop 0
	v_lshlrev_b32_e32 v98, 16, v100
	v_and_b32_e32 v99, 0xffff0000, v100
	v_max_f32_e64 v99, |v99|, |v99|
	v_max_f32_e64 v98, |v98|, |v98|
	v_cvt_pk_bf16_f32 v103, v108, v109
	v_max_f32_e32 v98, v98, v99
	v_lshlrev_b32_e32 v99, 16, v101
	v_and_b32_e32 v104, 0xffff0000, v101
	v_lshlrev_b32_e32 v106, 16, v103
	v_and_b32_e32 v107, 0xffff0000, v103
	v_max_f32_e64 v104, |v104|, |v104|
	v_max_f32_e64 v99, |v99|, |v99|
	v_max_f32_e64 v107, |v107|, |v107|
	v_max_f32_e64 v106, |v106|, |v106|
	v_max_f32_e32 v99, v99, v104
	v_lshlrev_b32_e32 v104, 16, v102
	v_and_b32_e32 v105, 0xffff0000, v102
	v_max_f32_e32 v106, v106, v107
	v_max3_f32 v104, |v104|, |v105|, v106
	v_max3_f32 v98, v98, v99, v104
	v_max3_f32 v98, v142, 0, v98
	ds_bpermute_b32 v99, v165, v98
	global_store_dwordx4 v[110:111], v[100:103], off offset:256
	s_waitcnt lgkmcnt(0)
	v_max_f32_e32 v99, v99, v99
	v_max_f32_e32 v98, v98, v99
	ds_bpermute_b32 v99, v169, v98
	s_and_saveexec_b64 s[34:35], s[6:7]
	s_cbranch_execz .LBB0_1036
	s_waitcnt lgkmcnt(0)
	v_max_f32_e32 v99, v99, v99
	v_max_f32_e32 v98, v98, v98
	v_lshl_add_u64 v[100:101], v[182:183], 2, s[16:17]
	v_max_f32_e32 v98, v98, v99
	global_atomic_umax v[100:101], v98, off
.LBB0_1036:
	s_or_b64 exec, exec, s[34:35]
	v_add_u32_e32 v130, 0x80, v176
	v_ashrrev_i32_e32 v131, 31, v130
	s_waitcnt lgkmcnt(0)
	v_mov_b64_e32 v[98:99], s[14:15]
	v_lshlrev_b64 v[100:101], 13, v[130:131]
	v_mad_i64_i32 v[98:99], s[34:35], v130, s65, v[98:99]
	v_lshl_add_u64 v[100:101], s[0:1], 0, v[100:101]
	v_lshl_add_u64 v[98:99], v[98:99], 0, v[166:167]
	v_lshl_add_u64 v[100:101], v[100:101], 0, v[166:167]
	global_load_dwordx4 v[110:113], v[98:99], off nt
	global_load_dwordx4 v[102:105], v[98:99], off offset:256 nt
	global_load_dwordx4 v[106:109], v[100:101], off nt
	s_nop 0
	global_load_dwordx4 v[98:101], v[100:101], off offset:256 nt
	v_cvt_f32_i32_e32 v97, v97
	v_cvt_f32_i32_e32 v96, v96
	v_pk_mul_f32 v[134:135], v[174:175], v[68:69] op_sel_hi:[0,1]
	v_cvt_f32_i32_e32 v95, v95
	v_cvt_f32_i32_e32 v94, v94
	v_pk_mul_f32 v[96:97], v[134:135], v[96:97]
	s_waitcnt vmcnt(9)
	v_lshlrev_b32_e32 v134, 16, v126
	v_and_b32_e32 v126, 0xffff0000, v126
	v_mul_f32_e32 v134, 0xbfb8aa3b, v134
	v_mul_f32_e32 v126, 0xbfb8aa3b, v126
	v_exp_f32_e32 v134, v134
	v_exp_f32_e32 v135, v126
	v_pk_mul_f32 v[136:137], v[174:175], v[66:67] op_sel_hi:[0,1]
	v_pk_mul_f32 v[94:95], v[136:137], v[94:95]
	v_add_f32_e32 v126, 1.0, v134
	v_add_f32_e32 v134, 1.0, v135
	v_lshlrev_b32_e32 v135, 16, v127
	v_and_b32_e32 v127, 0xffff0000, v127
	v_mul_f32_e32 v135, 0xbfb8aa3b, v135
	v_mul_f32_e32 v127, 0xbfb8aa3b, v127
	v_exp_f32_e32 v135, v135
	v_exp_f32_e32 v136, v127
	v_rcp_f32_e32 v127, v134
	v_cvt_f32_i32_e32 v93, v93
	v_add_f32_e32 v134, 1.0, v135
	v_add_f32_e32 v135, 1.0, v136
	v_lshlrev_b32_e32 v136, 16, v128
	v_and_b32_e32 v128, 0xffff0000, v128
	v_mul_f32_e32 v136, 0xbfb8aa3b, v136
	v_mul_f32_e32 v128, 0xbfb8aa3b, v128
	v_exp_f32_e32 v136, v136
	v_exp_f32_e32 v137, v128
	v_cvt_f32_i32_e32 v92, v92
	v_pk_mul_f32 v[140:141], v[174:175], v[64:65] op_sel_hi:[0,1]
	v_add_f32_e32 v128, 1.0, v136
	v_add_f32_e32 v136, 1.0, v137
	v_lshlrev_b32_e32 v137, 16, v129
	v_and_b32_e32 v129, 0xffff0000, v129
	v_mul_f32_e32 v137, 0xbfb8aa3b, v137
	v_mul_f32_e32 v129, 0xbfb8aa3b, v129
	v_pk_mul_f32 v[92:93], v[140:141], v[92:93]
	v_exp_f32_e32 v137, v137
	v_exp_f32_e32 v140, v129
	v_cvt_f32_i32_e32 v91, v91
	v_cvt_f32_i32_e32 v90, v90
	v_rcp_f32_e32 v126, v126
	v_rcp_f32_e32 v134, v134
	v_rcp_f32_e32 v135, v135
	v_rcp_f32_e32 v129, v136
	v_add_f32_e32 v136, 1.0, v137
	v_add_f32_e32 v137, 1.0, v140
	v_rcp_f32_e32 v128, v128
	v_rcp_f32_e32 v136, v136
	v_rcp_f32_e32 v137, v137
	v_pk_mul_f32 v[142:143], v[174:175], v[62:63] op_sel_hi:[0,1]
	s_waitcnt vmcnt(7)
; __device__ __forceinline__ unsigned cvtpk(float lo, float hi) { unsigned r; asm volatile("v_cvt_pk_bf16_f32 %0, %1, %2" : "=v"(r) : "v"(lo), "v"(hi)); return r; }
;     __device__ __forceinline__ void operator()(const f32x4 (&acc)[2][2][4][2], const Unit& u, int wr, int wc, int fr, int fq) const {
;     ...
;                     if (MODE == 2 || MODE == 3) { const u32x4 g = gq[kb & 1][bj];
;                         f32x4 g0 = {sigmoidf_(bflo(g.x)), sigmoidf_(bfhi(g.x)), sigmoidf_(bflo(g.y)), sigmoidf_(bfhi(g.y))};
;                         f32x4 g1 = {sigmoidf_(bflo(g.z)), sigmoidf_(bfhi(g.z)), sigmoidf_(bflo(g.w)), sigmoidf_(bfhi(g.w))};
;                         v0 = v0 * g0; v1 = v1 * g1;
;                         if (MODE == 3) { const u32x4 q = aq[kb & 1][bj];
;                             v0 = v0 + (f32x4){bflo(q.x), bfhi(q.x), bflo(q.y), bfhi(q.y)}; v1 = v1 + (f32x4){bflo(q.z), bfhi(q.z), bflo(q.w), bfhi(q.w)}; } }
;                     if (MODE == 4) { v0 = v0 + rs[kb & 1][bj][0]; v1 = v1 + rs[kb & 1][bj][1]; }
;                     if (MODE == 5) { const u32x4 c = gq[kb & 1][bj], q = aq[kb & 1][bj];
;                         v0 = (f32x4){bflo(c.x) + sigmoidf_(v0[0]) * bflo(q.x), bfhi(c.x) + sigmoidf_(v0[1]) * bfhi(q.x), bflo(c.y) + sigmoidf_(v0[2]) * bflo(q.y), bfhi(c.y) + sigmoidf_(v0[3]) * bfhi(q.y)};
;                         v1 = (f32x4){bflo(c.z) + sigmoidf_(v1[0]) * bflo(q.z), bfhi(c.z) + sigmoidf_(v1[1]) * bfhi(q.z), bflo(c.w) + sigmoidf_(v1[2]) * bflo(q.w), bfhi(c.w) + sigmoidf_(v1[3]) * bfhi(q.w)}; }
;                     u32x4 w; w.x = cvtpk(v0[0], v0[1]); w.y = cvtpk(v0[2], v0[3]); w.z = cvtpk(v1[0], v1[1]); w.w = cvtpk(v1[2], v1[3]);
;                     *(u32x4*)(O + (size_t)row * ldo + col) = w;
;                     if (MODE == 0) { if (dual) { const int kc = col - ZC_KV;
;                         *(u32x4*)((bf16_t*)aux + (size_t)((kc >> 7) * 512 + (row >> 4)) * 2048 + (row & 15) * 128 + (kc & 127)) = w; } }
;                     if (RMAX) rmx = fmaxf(rmx, fmaxf(fmaxf(fmaxf(fabsf(bflo(w.x)), fabsf(bfhi(w.x))), fmaxf(fabsf(bflo(w.y)), fabsf(bfhi(w.y)))), fmaxf(fmaxf(fabsf(bflo(w.z)), fabsf(bfhi(w.z))), fmaxf(fabsf(bflo(w.w)), fabsf(bfhi(w.w)))))); }
;                 if (RMAX) { rmx = fmaxf(rmx, __shfl_xor(rmx, 16)); rmx = fmaxf(rmx, __shfl_xor(rmx, 32)); if (fq == 0) atomicMax(rowmax + row, __float_as_uint(rmx)); } } }
	v_lshlrev_b32_e32 v140, 16, v122
	v_and_b32_e32 v141, 0xffff0000, v122
	v_lshlrev_b32_e32 v122, 16, v123
	v_and_b32_e32 v123, 0xffff0000, v123
	v_lshlrev_b64 v[132:133], 12, v[138:139]
	v_pk_mul_f32 v[90:91], v[142:143], v[90:91]
	v_pk_fma_f32 v[96:97], v[96:97], v[134:135], v[122:123]
	v_pk_fma_f32 v[94:95], v[94:95], v[126:127], v[140:141]
	v_lshlrev_b32_e32 v122, 16, v124
	v_and_b32_e32 v123, 0xffff0000, v124
	v_lshlrev_b32_e32 v124, 16, v125
	v_and_b32_e32 v125, 0xffff0000, v125
	v_pk_fma_f32 v[124:125], v[92:93], v[136:137], v[124:125]
	v_pk_fma_f32 v[92:93], v[90:91], v[128:129], v[122:123]
	v_cvt_pk_bf16_f32 v90, v94, v95
	v_lshl_add_u64 v[94:95], v[132:133], 1, s[12:13]
	v_lshl_add_u64 v[94:95], v[94:95], 0, v[166:167]
	v_cvt_pk_bf16_f32 v91, v96, v97
	v_cvt_pk_bf16_f32 v92, v92, v93
	v_cvt_pk_bf16_f32 v93, v124, v125
	global_store_dwordx4 v[94:95], v[90:93], off
	v_lshlrev_b32_e32 v96, 16, v90
	v_max_f32_e64 v96, |v96|, |v96|
	v_and_b32_e32 v90, 0xffff0000, v90
	v_max_f32_e64 v90, |v90|, |v90|
	v_max_f32_e32 v90, v96, v90
	v_lshlrev_b32_e32 v96, 16, v91
	v_and_b32_e32 v91, 0xffff0000, v91
	v_lshlrev_b32_e32 v97, 16, v93
	v_and_b32_e32 v93, 0xffff0000, v93
	v_max_f32_e64 v91, |v91|, |v91|
	v_max_f32_e64 v96, |v96|, |v96|
	v_max_f32_e64 v93, |v93|, |v93|
	v_max_f32_e64 v97, |v97|, |v97|
	v_cvt_f32_i32_e32 v89, v89
	v_cvt_f32_i32_e32 v88, v88
	v_max_f32_e32 v91, v96, v91
	v_lshlrev_b32_e32 v96, 16, v92
	v_and_b32_e32 v92, 0xffff0000, v92
	v_max_f32_e32 v93, v97, v93
	v_cvt_f32_i32_e32 v87, v87
	v_cvt_f32_i32_e32 v86, v86
	v_cvt_f32_i32_e32 v85, v85
	v_cvt_f32_i32_e32 v84, v84
	v_max3_f32 v92, |v96|, |v92|, v93
	v_max3_f32 v124, v90, v91, v92
	v_pk_mul_f32 v[90:91], v[174:175], v[56:57] op_sel_hi:[0,1]
	v_pk_mul_f32 v[92:93], v[174:175], v[54:55] op_sel_hi:[0,1]
	v_pk_mul_f32 v[96:97], v[174:175], v[52:53] op_sel_hi:[0,1]
	v_pk_mul_f32 v[88:89], v[90:91], v[88:89]
	v_lshlrev_b32_e32 v90, 16, v118
	v_and_b32_e32 v91, 0xffff0000, v118
	v_pk_mul_f32 v[86:87], v[92:93], v[86:87]
	v_mul_f32_e32 v90, 0xbfb8aa3b, v90
	v_mul_f32_e32 v91, 0xbfb8aa3b, v91
	v_pk_mul_f32 v[84:85], v[96:97], v[84:85]
	v_lshlrev_b32_e32 v92, 16, v119
	v_and_b32_e32 v93, 0xffff0000, v119
	v_lshlrev_b32_e32 v96, 16, v120
	v_and_b32_e32 v97, 0xffff0000, v120
	v_exp_f32_e32 v90, v90
	v_exp_f32_e32 v91, v91
	v_mul_f32_e32 v92, 0xbfb8aa3b, v92
	v_mul_f32_e32 v93, 0xbfb8aa3b, v93
	v_mul_f32_e32 v96, 0xbfb8aa3b, v96
	v_mul_f32_e32 v97, 0xbfb8aa3b, v97
	v_lshlrev_b32_e32 v118, 16, v121
	v_and_b32_e32 v119, 0xffff0000, v121
	v_exp_f32_e32 v92, v92
	v_exp_f32_e32 v93, v93
	v_exp_f32_e32 v96, v96
	v_exp_f32_e32 v97, v97
	v_mul_f32_e32 v118, 0xbfb8aa3b, v118
	v_mul_f32_e32 v119, 0xbfb8aa3b, v119
	v_exp_f32_e32 v118, v118
	v_exp_f32_e32 v119, v119
	v_add_f32_e32 v90, 1.0, v90
	v_add_f32_e32 v91, 1.0, v91
	v_cvt_f32_i32_e32 v83, v83
	v_cvt_f32_i32_e32 v82, v82
	v_rcp_f32_e32 v90, v90
	v_rcp_f32_e32 v91, v91
	v_add_f32_e32 v92, 1.0, v92
	v_add_f32_e32 v93, 1.0, v93
	v_add_f32_e32 v96, 1.0, v96
	v_add_f32_e32 v97, 1.0, v97
	v_rcp_f32_e32 v92, v92
	v_rcp_f32_e32 v93, v93
	v_rcp_f32_e32 v96, v96
	v_rcp_f32_e32 v97, v97
	v_add_f32_e32 v118, 1.0, v118
	v_add_f32_e32 v119, 1.0, v119
	v_rcp_f32_e32 v118, v118
	v_rcp_f32_e32 v119, v119
	v_pk_mul_f32 v[122:123], v[174:175], v[50:51] op_sel_hi:[0,1]
	s_waitcnt vmcnt(7)
	v_lshlrev_b32_e32 v120, 16, v114
	v_and_b32_e32 v121, 0xffff0000, v114
	v_pk_mul_f32 v[82:83], v[122:123], v[82:83]
	v_lshlrev_b32_e32 v114, 16, v115
	v_and_b32_e32 v115, 0xffff0000, v115
	v_pk_fma_f32 v[86:87], v[86:87], v[90:91], v[120:121]
	v_lshlrev_b32_e32 v90, 16, v116
	v_and_b32_e32 v91, 0xffff0000, v116
	v_pk_fma_f32 v[88:89], v[88:89], v[92:93], v[114:115]
	v_lshlrev_b32_e32 v92, 16, v117
	v_and_b32_e32 v93, 0xffff0000, v117
	v_pk_fma_f32 v[82:83], v[82:83], v[96:97], v[90:91]
	v_pk_fma_f32 v[92:93], v[84:85], v[118:119], v[92:93]
	v_cvt_pk_bf16_f32 v84, v86, v87
	v_cvt_pk_bf16_f32 v85, v88, v89
	v_cvt_pk_bf16_f32 v86, v82, v83
	s_nop 0
	v_lshlrev_b32_e32 v82, 16, v84
	v_and_b32_e32 v83, 0xffff0000, v84
	v_max_f32_e64 v83, |v83|, |v83|
	v_max_f32_e64 v82, |v82|, |v82|
	v_cvt_pk_bf16_f32 v87, v92, v93
	v_max_f32_e32 v82, v82, v83
	v_lshlrev_b32_e32 v83, 16, v85
	v_and_b32_e32 v88, 0xffff0000, v85
	v_lshlrev_b32_e32 v90, 16, v87
	v_and_b32_e32 v91, 0xffff0000, v87
	v_max_f32_e64 v88, |v88|, |v88|
	v_max_f32_e64 v83, |v83|, |v83|
	v_max_f32_e64 v91, |v91|, |v91|
	v_max_f32_e64 v90, |v90|, |v90|
	v_max_f32_e32 v83, v83, v88
	v_lshlrev_b32_e32 v88, 16, v86
	v_and_b32_e32 v89, 0xffff0000, v86
	v_max_f32_e32 v90, v90, v91
	v_max3_f32 v88, |v88|, |v89|, v90
	v_max3_f32 v82, v82, v83, v88
	v_max3_f32 v82, v124, 0, v82
	ds_bpermute_b32 v83, v165, v82
	global_store_dwordx4 v[94:95], v[84:87], off offset:256
	s_waitcnt lgkmcnt(0)
	v_max_f32_e32 v83, v83, v83
	v_max_f32_e32 v82, v82, v83
	ds_bpermute_b32 v83, v169, v82
	s_and_saveexec_b64 s[34:35], s[6:7]
	s_cbranch_execz .LBB0_1038
	s_waitcnt lgkmcnt(0)
	v_max_f32_e32 v83, v83, v83
	v_max_f32_e32 v82, v82, v82
	v_lshl_add_u64 v[84:85], v[138:139], 2, s[16:17]
	v_max_f32_e32 v82, v82, v83
	global_atomic_umax v[84:85], v82, off
;     __device__ __forceinline__ void operator()(const f32x4 (&acc)[2][2][4][2], const Unit& u, int wr, int wc, int fr, int fq) const {
;     ...
;         EPB_LOAD(0);
; #pragma unroll
;         for (int kb = 0; kb < 8; ++kb) { const int ai = kb >> 2, m = kb & 3;
;             if (kb < 7) EPB_LOAD(kb + 1);
;             { const int row = row0 + ai * HALF + m * 16; float rmx = 0.f;
; #pragma unroll
;                 for (int bj = 0; bj < 2; ++bj) { const int col = col0 + bj * HALF; f32x4 v0 = acc[ai][bj][m][0], v1 = acc[ai][bj][m][1];
;                     if (QI8) { const f32x4 c0 = cb[bj][0] * ra[ai][m], c1 = cb[bj][1] * ra[ai][m]; const i32x4 i0 = __builtin_bit_cast(i32x4, v0), i1 = __builtin_bit_cast(i32x4, v1);
;                         v0 = (f32x4){(float)i0[0], (float)i0[1], (float)i0[2], (float)i0[3]} * c0; v1 = (f32x4){(float)i1[0], (float)i1[1], (float)i1[2], (float)i1[3]} * c1; }
;                     else if (MODE == 0) { v0 = v0 * tsc; v1 = v1 * tsc; }
;                     if (!QI8 && MODE == 1) { v0 = v0 * cb[bj][0]; v1 = v1 * cb[bj][1]; }
;                     if (MODE == 2 || MODE == 3) { const u32x4 g = gq[kb & 1][bj];
;                         f32x4 g0 = {sigmoidf_(bflo(g.x)), sigmoidf_(bfhi(g.x)), sigmoidf_(bflo(g.y)), sigmoidf_(bfhi(g.y))};
;                         f32x4 g1 = {sigmoidf_(bflo(g.z)), sigmoidf_(bfhi(g.z)), sigmoidf_(bflo(g.w)), sigmoidf_(bfhi(g.w))};
;                         v0 = v0 * g0; v1 = v1 * g1;
;                         if (MODE == 3) { const u32x4 q = aq[kb & 1][bj];
;                             v0 = v0 + (f32x4){bflo(q.x), bfhi(q.x), bflo(q.y), bfhi(q.y)}; v1 = v1 + (f32x4){bflo(q.z), bfhi(q.z), bflo(q.w), bfhi(q.w)}; } }
;                     if (MODE == 4) { v0 = v0 + rs[kb & 1][bj][0]; v1 = v1 + rs[kb & 1][bj][1]; }
;                     if (MODE == 5) { const u32x4 c = gq[kb & 1][bj], q = aq[kb & 1][bj];
;                         v0 = (f32x4){bflo(c.x) + sigmoidf_(v0[0]) * bflo(q.x), bfhi(c.x) + sigmoidf_(v0[1]) * bfhi(q.x), bflo(c.y) + sigmoidf_(v0[2]) * bflo(q.y), bfhi(c.y) + sigmoidf_(v0[3]) * bfhi(q.y)};
;                         v1 = (f32x4){bflo(c.z) + sigmoidf_(v1[0]) * bflo(q.z), bfhi(c.z) + sigmoidf_(v1[1]) * bfhi(q.z), bflo(c.w) + sigmoidf_(v1[2]) * bflo(q.w), bfhi(c.w) + sigmoidf_(v1[3]) * bfhi(q.w)}; }
.LBB0_1038:
	s_or_b64 exec, exec, s[34:35]
	v_or_b32_e32 v114, 16, v130
	v_ashrrev_i32_e32 v115, 31, v114
	s_waitcnt lgkmcnt(0)
	v_mov_b64_e32 v[82:83], s[14:15]
	v_lshlrev_b64 v[84:85], 13, v[114:115]
	v_mad_i64_i32 v[82:83], s[34:35], v114, s65, v[82:83]
	v_lshl_add_u64 v[84:85], s[0:1], 0, v[84:85]
	v_lshl_add_u64 v[82:83], v[82:83], 0, v[166:167]
	v_lshl_add_u64 v[84:85], v[84:85], 0, v[166:167]
	global_load_dwordx4 v[94:97], v[82:83], off nt
	global_load_dwordx4 v[86:89], v[82:83], off offset:256 nt
	global_load_dwordx4 v[90:93], v[84:85], off nt
	s_nop 0
	global_load_dwordx4 v[82:85], v[84:85], off offset:256 nt
	v_cvt_f32_i32_e32 v81, v81
	v_cvt_f32_i32_e32 v80, v80
	v_pk_mul_f32 v[118:119], v[172:173], v[68:69] op_sel_hi:[0,1]
	v_cvt_f32_i32_e32 v79, v79
	v_cvt_f32_i32_e32 v78, v78
	v_pk_mul_f32 v[80:81], v[118:119], v[80:81]
	s_waitcnt vmcnt(9)
	v_lshlrev_b32_e32 v118, 16, v110
	v_and_b32_e32 v110, 0xffff0000, v110
	v_mul_f32_e32 v118, 0xbfb8aa3b, v118
	v_mul_f32_e32 v110, 0xbfb8aa3b, v110
	v_exp_f32_e32 v118, v118
	v_exp_f32_e32 v119, v110
	v_pk_mul_f32 v[120:121], v[172:173], v[66:67] op_sel_hi:[0,1]
	v_pk_mul_f32 v[78:79], v[120:121], v[78:79]
	v_add_f32_e32 v110, 1.0, v118
	v_add_f32_e32 v118, 1.0, v119
	v_lshlrev_b32_e32 v119, 16, v111
	v_and_b32_e32 v111, 0xffff0000, v111
	v_mul_f32_e32 v119, 0xbfb8aa3b, v119
	v_mul_f32_e32 v111, 0xbfb8aa3b, v111
	v_exp_f32_e32 v119, v119
	v_exp_f32_e32 v120, v111
	v_rcp_f32_e32 v111, v118
	v_cvt_f32_i32_e32 v77, v77
	v_add_f32_e32 v118, 1.0, v119
	v_add_f32_e32 v119, 1.0, v120
	v_lshlrev_b32_e32 v120, 16, v112
	v_and_b32_e32 v112, 0xffff0000, v112
	v_mul_f32_e32 v120, 0xbfb8aa3b, v120
	v_mul_f32_e32 v112, 0xbfb8aa3b, v112
	v_exp_f32_e32 v120, v120
	v_exp_f32_e32 v121, v112
	v_cvt_f32_i32_e32 v76, v76
	v_pk_mul_f32 v[122:123], v[172:173], v[64:65] op_sel_hi:[0,1]
	v_add_f32_e32 v112, 1.0, v120
	v_add_f32_e32 v120, 1.0, v121
	v_lshlrev_b32_e32 v121, 16, v113
	v_and_b32_e32 v113, 0xffff0000, v113
	v_mul_f32_e32 v121, 0xbfb8aa3b, v121
	v_mul_f32_e32 v113, 0xbfb8aa3b, v113
	v_pk_mul_f32 v[76:77], v[122:123], v[76:77]
	v_exp_f32_e32 v121, v121
	v_exp_f32_e32 v122, v113
	v_cvt_f32_i32_e32 v75, v75
	v_cvt_f32_i32_e32 v74, v74
	v_rcp_f32_e32 v110, v110
	v_rcp_f32_e32 v118, v118
	v_rcp_f32_e32 v119, v119
	v_rcp_f32_e32 v113, v120
	v_add_f32_e32 v120, 1.0, v121
	v_add_f32_e32 v121, 1.0, v122
	v_rcp_f32_e32 v112, v112
	v_rcp_f32_e32 v120, v120
	v_rcp_f32_e32 v121, v121
	v_pk_mul_f32 v[124:125], v[172:173], v[62:63] op_sel_hi:[0,1]
	s_waitcnt vmcnt(7)
	v_lshlrev_b32_e32 v122, 16, v106
	v_and_b32_e32 v123, 0xffff0000, v106
	v_lshlrev_b32_e32 v106, 16, v107
	v_and_b32_e32 v107, 0xffff0000, v107
	v_lshlrev_b64 v[116:117], 12, v[130:131]
	v_pk_mul_f32 v[74:75], v[124:125], v[74:75]
	v_pk_fma_f32 v[80:81], v[80:81], v[118:119], v[106:107]
	v_pk_fma_f32 v[78:79], v[78:79], v[110:111], v[122:123]
	v_lshlrev_b32_e32 v106, 16, v108
	v_and_b32_e32 v107, 0xffff0000, v108
	v_lshlrev_b32_e32 v108, 16, v109
	v_and_b32_e32 v109, 0xffff0000, v109
	v_pk_fma_f32 v[108:109], v[76:77], v[120:121], v[108:109]
	v_pk_fma_f32 v[76:77], v[74:75], v[112:113], v[106:107]
	v_cvt_pk_bf16_f32 v74, v78, v79
	v_lshl_add_u64 v[78:79], v[116:117], 1, s[12:13]
	v_lshl_add_u64 v[78:79], v[78:79], 0, v[166:167]
	v_cvt_pk_bf16_f32 v75, v80, v81
	v_cvt_pk_bf16_f32 v76, v76, v77
	v_cvt_pk_bf16_f32 v77, v108, v109
	global_store_dwordx4 v[78:79], v[74:77], off
	v_lshlrev_b32_e32 v80, 16, v74
	v_max_f32_e64 v80, |v80|, |v80|
	v_and_b32_e32 v74, 0xffff0000, v74
	v_max_f32_e64 v74, |v74|, |v74|
	v_max_f32_e32 v74, v80, v74
	v_lshlrev_b32_e32 v80, 16, v75
	v_and_b32_e32 v75, 0xffff0000, v75
	v_lshlrev_b32_e32 v81, 16, v77
	v_and_b32_e32 v77, 0xffff0000, v77
	v_max_f32_e64 v75, |v75|, |v75|
	v_max_f32_e64 v80, |v80|, |v80|
	v_max_f32_e64 v77, |v77|, |v77|
	v_max_f32_e64 v81, |v81|, |v81|
	v_cvt_f32_i32_e32 v73, v73
	v_cvt_f32_i32_e32 v72, v72
	v_max_f32_e32 v75, v80, v75
	v_lshlrev_b32_e32 v80, 16, v76
	v_and_b32_e32 v76, 0xffff0000, v76
	v_max_f32_e32 v77, v81, v77
	v_cvt_f32_i32_e32 v71, v71
	v_cvt_f32_i32_e32 v70, v70
	v_cvt_f32_i32_e32 v61, v61
	v_cvt_f32_i32_e32 v60, v60
	v_max3_f32 v76, |v80|, |v76|, v77
	v_max3_f32 v108, v74, v75, v76
	v_pk_mul_f32 v[74:75], v[172:173], v[56:57] op_sel_hi:[0,1]
	v_pk_mul_f32 v[76:77], v[172:173], v[54:55] op_sel_hi:[0,1]
	v_pk_mul_f32 v[80:81], v[172:173], v[52:53] op_sel_hi:[0,1]
	v_pk_mul_f32 v[72:73], v[74:75], v[72:73]
	v_lshlrev_b32_e32 v74, 16, v102
	v_and_b32_e32 v75, 0xffff0000, v102
	v_pk_mul_f32 v[70:71], v[76:77], v[70:71]
	v_mul_f32_e32 v74, 0xbfb8aa3b, v74
	v_mul_f32_e32 v75, 0xbfb8aa3b, v75
	v_pk_mul_f32 v[60:61], v[80:81], v[60:61]
	v_lshlrev_b32_e32 v76, 16, v103
	v_and_b32_e32 v77, 0xffff0000, v103
	v_lshlrev_b32_e32 v80, 16, v104
	v_and_b32_e32 v81, 0xffff0000, v104
	v_exp_f32_e32 v74, v74
	v_exp_f32_e32 v75, v75
	v_mul_f32_e32 v76, 0xbfb8aa3b, v76
	v_mul_f32_e32 v77, 0xbfb8aa3b, v77
	v_mul_f32_e32 v80, 0xbfb8aa3b, v80
	v_mul_f32_e32 v81, 0xbfb8aa3b, v81
	v_exp_f32_e32 v76, v76
	v_exp_f32_e32 v77, v77
	v_exp_f32_e32 v80, v80
	v_exp_f32_e32 v81, v81
	v_lshlrev_b32_e32 v102, 16, v105
	v_and_b32_e32 v103, 0xffff0000, v105
	v_mul_f32_e32 v102, 0xbfb8aa3b, v102
	v_mul_f32_e32 v103, 0xbfb8aa3b, v103
	v_exp_f32_e32 v102, v102
	v_exp_f32_e32 v103, v103
	v_add_f32_e32 v74, 1.0, v74
	v_add_f32_e32 v75, 1.0, v75
	v_cvt_f32_i32_e32 v59, v59
	v_cvt_f32_i32_e32 v58, v58
	v_rcp_f32_e32 v74, v74
	v_rcp_f32_e32 v75, v75
	v_add_f32_e32 v76, 1.0, v76
	v_add_f32_e32 v77, 1.0, v77
	v_add_f32_e32 v80, 1.0, v80
	v_add_f32_e32 v81, 1.0, v81
	v_rcp_f32_e32 v76, v76
	v_rcp_f32_e32 v77, v77
	v_rcp_f32_e32 v80, v80
	v_rcp_f32_e32 v81, v81
	v_add_f32_e32 v102, 1.0, v102
	v_add_f32_e32 v103, 1.0, v103
	v_pk_mul_f32 v[106:107], v[172:173], v[50:51] op_sel_hi:[0,1]
	v_rcp_f32_e32 v102, v102
	v_rcp_f32_e32 v103, v103
	s_waitcnt vmcnt(7)
;     __device__ __forceinline__ void operator()(const f32x4 (&acc)[2][2][4][2], const Unit& u, int wr, int wc, int fr, int fq) const {
;     ...
;         EPB_LOAD(0);
; #pragma unroll
;         for (int kb = 0; kb < 8; ++kb) { const int ai = kb >> 2, m = kb & 3;
;             if (kb < 7) EPB_LOAD(kb + 1);
;             { const int row = row0 + ai * HALF + m * 16; float rmx = 0.f;
; #pragma unroll
;                 for (int bj = 0; bj < 2; ++bj) { const int col = col0 + bj * HALF; f32x4 v0 = acc[ai][bj][m][0], v1 = acc[ai][bj][m][1];
;                     if (QI8) { const f32x4 c0 = cb[bj][0] * ra[ai][m], c1 = cb[bj][1] * ra[ai][m]; const i32x4 i0 = __builtin_bit_cast(i32x4, v0), i1 = __builtin_bit_cast(i32x4, v1);
;                         v0 = (f32x4){(float)i0[0], (float)i0[1], (float)i0[2], (float)i0[3]} * c0; v1 = (f32x4){(float)i1[0], (float)i1[1], (float)i1[2], (float)i1[3]} * c1; }
;                     else if (MODE == 0) { v0 = v0 * tsc; v1 = v1 * tsc; }
;                     if (!QI8 && MODE == 1) { v0 = v0 * cb[bj][0]; v1 = v1 * cb[bj][1]; }
;                     if (MODE == 2 || MODE == 3) { const u32x4 g = gq[kb & 1][bj];
;                         f32x4 g0 = {sigmoidf_(bflo(g.x)), sigmoidf_(bfhi(g.x)), sigmoidf_(bflo(g.y)), sigmoidf_(bfhi(g.y))};
;                         f32x4 g1 = {sigmoidf_(bflo(g.z)), sigmoidf_(bfhi(g.z)), sigmoidf_(bflo(g.w)), sigmoidf_(bfhi(g.w))};
;                         v0 = v0 * g0; v1 = v1 * g1;
;                         if (MODE == 3) { const u32x4 q = aq[kb & 1][bj];
;                             v0 = v0 + (f32x4){bflo(q.x), bfhi(q.x), bflo(q.y), bfhi(q.y)}; v1 = v1 + (f32x4){bflo(q.z), bfhi(q.z), bflo(q.w), bfhi(q.w)}; } }
;                     if (MODE == 4) { v0 = v0 + rs[kb & 1][bj][0]; v1 = v1 + rs[kb & 1][bj][1]; }
;                     if (MODE == 5) { const u32x4 c = gq[kb & 1][bj], q = aq[kb & 1][bj];
;                         v0 = (f32x4){bflo(c.x) + sigmoidf_(v0[0]) * bflo(q.x), bfhi(c.x) + sigmoidf_(v0[1]) * bfhi(q.x), bflo(c.y) + sigmoidf_(v0[2]) * bflo(q.y), bfhi(c.y) + sigmoidf_(v0[3]) * bfhi(q.y)};
;                         v1 = (f32x4){bflo(c.z) + sigmoidf_(v1[0]) * bflo(q.z), bfhi(c.z) + sigmoidf_(v1[1]) * bfhi(q.z), bflo(c.w) + sigmoidf_(v1[2]) * bflo(q.w), bfhi(c.w) + sigmoidf_(v1[3]) * bfhi(q.w)}; }
	v_lshlrev_b32_e32 v104, 16, v98
	v_and_b32_e32 v105, 0xffff0000, v98
	v_pk_mul_f32 v[58:59], v[106:107], v[58:59]
	v_lshlrev_b32_e32 v98, 16, v99
	v_and_b32_e32 v99, 0xffff0000, v99
	v_pk_fma_f32 v[70:71], v[70:71], v[74:75], v[104:105]
	v_lshlrev_b32_e32 v74, 16, v100
	v_and_b32_e32 v75, 0xffff0000, v100
	v_pk_fma_f32 v[72:73], v[72:73], v[76:77], v[98:99]
	v_pk_fma_f32 v[58:59], v[58:59], v[80:81], v[74:75]
	v_lshlrev_b32_e32 v76, 16, v101
	v_and_b32_e32 v77, 0xffff0000, v101
	v_cvt_pk_bf16_f32 v70, v70, v71
	v_cvt_pk_bf16_f32 v71, v72, v73
	v_cvt_pk_bf16_f32 v72, v58, v59
	v_pk_fma_f32 v[60:61], v[60:61], v[102:103], v[76:77]
	v_lshlrev_b32_e32 v58, 16, v70
	v_and_b32_e32 v59, 0xffff0000, v70
	v_max_f32_e64 v59, |v59|, |v59|
	v_max_f32_e64 v58, |v58|, |v58|
	v_cvt_pk_bf16_f32 v73, v60, v61
	v_max_f32_e32 v58, v58, v59
	v_lshlrev_b32_e32 v59, 16, v71
	v_and_b32_e32 v60, 0xffff0000, v71
	v_lshlrev_b32_e32 v74, 16, v73
	v_and_b32_e32 v75, 0xffff0000, v73
	v_max_f32_e64 v60, |v60|, |v60|
	v_max_f32_e64 v59, |v59|, |v59|
	v_max_f32_e64 v75, |v75|, |v75|
	v_max_f32_e64 v74, |v74|, |v74|
	v_max_f32_e32 v59, v59, v60
	v_lshlrev_b32_e32 v60, 16, v72
	v_and_b32_e32 v61, 0xffff0000, v72
	v_max_f32_e32 v74, v74, v75
	v_max3_f32 v60, |v60|, |v61|, v74
	v_max3_f32 v58, v58, v59, v60
	v_max3_f32 v58, v108, 0, v58
	ds_bpermute_b32 v59, v165, v58
	global_store_dwordx4 v[78:79], v[70:73], off offset:256
	s_waitcnt lgkmcnt(0)
	v_max_f32_e32 v59, v59, v59
	v_max_f32_e32 v58, v58, v59
	ds_bpermute_b32 v59, v169, v58
	s_and_saveexec_b64 s[34:35], s[6:7]
	s_cbranch_execz .LBB0_1040
	s_waitcnt lgkmcnt(0)
	v_max_f32_e32 v59, v59, v59
	v_max_f32_e32 v58, v58, v58
	v_lshl_add_u64 v[60:61], v[130:131], 2, s[16:17]
	v_max_f32_e32 v58, v58, v59
	global_atomic_umax v[60:61], v58, off
.LBB0_1040:
	s_or_b64 exec, exec, s[34:35]
	v_or_b32_e32 v98, 32, v130
	v_ashrrev_i32_e32 v99, 31, v98
	s_waitcnt lgkmcnt(0)
	v_mov_b64_e32 v[58:59], s[14:15]
	v_lshlrev_b64 v[60:61], 13, v[98:99]
	v_mad_i64_i32 v[58:59], s[34:35], v98, s65, v[58:59]
	v_lshl_add_u64 v[60:61], s[0:1], 0, v[60:61]
	v_lshl_add_u64 v[58:59], v[58:59], 0, v[166:167]
	v_lshl_add_u64 v[60:61], v[60:61], 0, v[166:167]
	global_load_dwordx4 v[78:81], v[58:59], off nt
	global_load_dwordx4 v[70:73], v[58:59], off offset:256 nt
	global_load_dwordx4 v[74:77], v[60:61], off nt
	s_nop 0
	global_load_dwordx4 v[58:61], v[60:61], off offset:256 nt
	v_cvt_f32_i32_e32 v49, v49
	v_cvt_f32_i32_e32 v48, v48
	v_pk_mul_f32 v[102:103], v[170:171], v[68:69] op_sel_hi:[0,1]
	v_cvt_f32_i32_e32 v47, v47
	v_cvt_f32_i32_e32 v46, v46
	v_pk_mul_f32 v[48:49], v[102:103], v[48:49]
	s_waitcnt vmcnt(9)
	v_lshlrev_b32_e32 v102, 16, v94
	v_and_b32_e32 v94, 0xffff0000, v94
	v_mul_f32_e32 v102, 0xbfb8aa3b, v102
	v_mul_f32_e32 v94, 0xbfb8aa3b, v94
	v_exp_f32_e32 v102, v102
	v_exp_f32_e32 v103, v94
	v_pk_mul_f32 v[104:105], v[170:171], v[66:67] op_sel_hi:[0,1]
	v_pk_mul_f32 v[46:47], v[104:105], v[46:47]
	v_add_f32_e32 v94, 1.0, v102
	v_add_f32_e32 v102, 1.0, v103
	v_lshlrev_b32_e32 v103, 16, v95
	v_and_b32_e32 v95, 0xffff0000, v95
	v_mul_f32_e32 v103, 0xbfb8aa3b, v103
	v_mul_f32_e32 v95, 0xbfb8aa3b, v95
	v_exp_f32_e32 v103, v103
	v_exp_f32_e32 v104, v95
	v_rcp_f32_e32 v95, v102
	v_cvt_f32_i32_e32 v45, v45
	v_add_f32_e32 v102, 1.0, v103
	v_add_f32_e32 v103, 1.0, v104
	v_lshlrev_b32_e32 v104, 16, v96
	v_and_b32_e32 v96, 0xffff0000, v96
	v_mul_f32_e32 v104, 0xbfb8aa3b, v104
	v_mul_f32_e32 v96, 0xbfb8aa3b, v96
	v_exp_f32_e32 v104, v104
	v_exp_f32_e32 v105, v96
	v_cvt_f32_i32_e32 v44, v44
	v_pk_mul_f32 v[106:107], v[170:171], v[64:65] op_sel_hi:[0,1]
	v_add_f32_e32 v96, 1.0, v104
	v_add_f32_e32 v104, 1.0, v105
	v_lshlrev_b32_e32 v105, 16, v97
	v_and_b32_e32 v97, 0xffff0000, v97
	v_mul_f32_e32 v105, 0xbfb8aa3b, v105
	v_mul_f32_e32 v97, 0xbfb8aa3b, v97
	v_pk_mul_f32 v[44:45], v[106:107], v[44:45]
	v_exp_f32_e32 v105, v105
	v_exp_f32_e32 v106, v97
	v_cvt_f32_i32_e32 v43, v43
	v_cvt_f32_i32_e32 v42, v42
	v_rcp_f32_e32 v94, v94
	v_rcp_f32_e32 v102, v102
	v_rcp_f32_e32 v103, v103
	v_rcp_f32_e32 v97, v104
	v_add_f32_e32 v104, 1.0, v105
	v_add_f32_e32 v105, 1.0, v106
	v_rcp_f32_e32 v96, v96
	v_rcp_f32_e32 v104, v104
	v_rcp_f32_e32 v105, v105
	v_pk_mul_f32 v[108:109], v[170:171], v[62:63] op_sel_hi:[0,1]
	s_waitcnt vmcnt(7)
; __device__ __forceinline__ unsigned cvtpk(float lo, float hi) { unsigned r; asm volatile("v_cvt_pk_bf16_f32 %0, %1, %2" : "=v"(r) : "v"(lo), "v"(hi)); return r; }
;     __device__ __forceinline__ void operator()(const f32x4 (&acc)[2][2][4][2], const Unit& u, int wr, int wc, int fr, int fq) const {
;     ...
;                     if (MODE == 2 || MODE == 3) { const u32x4 g = gq[kb & 1][bj];
;                         f32x4 g0 = {sigmoidf_(bflo(g.x)), sigmoidf_(bfhi(g.x)), sigmoidf_(bflo(g.y)), sigmoidf_(bfhi(g.y))};
;                         f32x4 g1 = {sigmoidf_(bflo(g.z)), sigmoidf_(bfhi(g.z)), sigmoidf_(bflo(g.w)), sigmoidf_(bfhi(g.w))};
;                         v0 = v0 * g0; v1 = v1 * g1;
;                         if (MODE == 3) { const u32x4 q = aq[kb & 1][bj];
;                             v0 = v0 + (f32x4){bflo(q.x), bfhi(q.x), bflo(q.y), bfhi(q.y)}; v1 = v1 + (f32x4){bflo(q.z), bfhi(q.z), bflo(q.w), bfhi(q.w)}; } }
;                     if (MODE == 4) { v0 = v0 + rs[kb & 1][bj][0]; v1 = v1 + rs[kb & 1][bj][1]; }
;                     if (MODE == 5) { const u32x4 c = gq[kb & 1][bj], q = aq[kb & 1][bj];
;                         v0 = (f32x4){bflo(c.x) + sigmoidf_(v0[0]) * bflo(q.x), bfhi(c.x) + sigmoidf_(v0[1]) * bfhi(q.x), bflo(c.y) + sigmoidf_(v0[2]) * bflo(q.y), bfhi(c.y) + sigmoidf_(v0[3]) * bfhi(q.y)};
;                         v1 = (f32x4){bflo(c.z) + sigmoidf_(v1[0]) * bflo(q.z), bfhi(c.z) + sigmoidf_(v1[1]) * bfhi(q.z), bflo(c.w) + sigmoidf_(v1[2]) * bflo(q.w), bfhi(c.w) + sigmoidf_(v1[3]) * bfhi(q.w)}; }
;                     u32x4 w; w.x = cvtpk(v0[0], v0[1]); w.y = cvtpk(v0[2], v0[3]); w.z = cvtpk(v1[0], v1[1]); w.w = cvtpk(v1[2], v1[3]);
;                     *(u32x4*)(O + (size_t)row * ldo + col) = w;
;                     if (MODE == 0) { if (dual) { const int kc = col - ZC_KV;
;                         *(u32x4*)((bf16_t*)aux + (size_t)((kc >> 7) * 512 + (row >> 4)) * 2048 + (row & 15) * 128 + (kc & 127)) = w; } }
;                     if (RMAX) rmx = fmaxf(rmx, fmaxf(fmaxf(fmaxf(fabsf(bflo(w.x)), fabsf(bfhi(w.x))), fmaxf(fabsf(bflo(w.y)), fabsf(bfhi(w.y)))), fmaxf(fmaxf(fabsf(bflo(w.z)), fabsf(bfhi(w.z))), fmaxf(fabsf(bflo(w.w)), fabsf(bfhi(w.w)))))); }
;                 if (RMAX) { rmx = fmaxf(rmx, __shfl_xor(rmx, 16)); rmx = fmaxf(rmx, __shfl_xor(rmx, 32)); if (fq == 0) atomicMax(rowmax + row, __float_as_uint(rmx)); } } }
	v_lshlrev_b32_e32 v106, 16, v90
	v_and_b32_e32 v107, 0xffff0000, v90
	v_lshlrev_b32_e32 v90, 16, v91
	v_and_b32_e32 v91, 0xffff0000, v91
	v_lshlrev_b64 v[100:101], 12, v[114:115]
	v_pk_mul_f32 v[42:43], v[108:109], v[42:43]
	v_pk_fma_f32 v[48:49], v[48:49], v[102:103], v[90:91]
	v_pk_fma_f32 v[46:47], v[46:47], v[94:95], v[106:107]
	v_lshlrev_b32_e32 v90, 16, v92
	v_and_b32_e32 v91, 0xffff0000, v92
	v_lshlrev_b32_e32 v92, 16, v93
	v_and_b32_e32 v93, 0xffff0000, v93
	v_pk_fma_f32 v[92:93], v[44:45], v[104:105], v[92:93]
	v_pk_fma_f32 v[44:45], v[42:43], v[96:97], v[90:91]
	v_cvt_pk_bf16_f32 v42, v46, v47
	v_lshl_add_u64 v[46:47], v[100:101], 1, s[12:13]
	v_lshl_add_u64 v[46:47], v[46:47], 0, v[166:167]
	v_cvt_pk_bf16_f32 v43, v48, v49
	v_cvt_pk_bf16_f32 v44, v44, v45
	v_cvt_pk_bf16_f32 v45, v92, v93
	global_store_dwordx4 v[46:47], v[42:45], off
	v_lshlrev_b32_e32 v48, 16, v42
	v_max_f32_e64 v48, |v48|, |v48|
	v_and_b32_e32 v42, 0xffff0000, v42
	v_max_f32_e64 v42, |v42|, |v42|
	v_max_f32_e32 v42, v48, v42
	v_lshlrev_b32_e32 v48, 16, v43
	v_and_b32_e32 v43, 0xffff0000, v43
	v_lshlrev_b32_e32 v49, 16, v45
	v_and_b32_e32 v45, 0xffff0000, v45
	v_max_f32_e64 v43, |v43|, |v43|
	v_max_f32_e64 v48, |v48|, |v48|
	v_max_f32_e64 v45, |v45|, |v45|
	v_max_f32_e64 v49, |v49|, |v49|
	v_cvt_f32_i32_e32 v41, v41
	v_cvt_f32_i32_e32 v40, v40
	v_max_f32_e32 v43, v48, v43
	v_lshlrev_b32_e32 v48, 16, v44
	v_and_b32_e32 v44, 0xffff0000, v44
	v_max_f32_e32 v45, v49, v45
	v_cvt_f32_i32_e32 v39, v39
	v_cvt_f32_i32_e32 v38, v38
	v_cvt_f32_i32_e32 v37, v37
	v_cvt_f32_i32_e32 v36, v36
	v_max3_f32 v44, |v48|, |v44|, v45
	v_max3_f32 v92, v42, v43, v44
	v_pk_mul_f32 v[42:43], v[170:171], v[56:57] op_sel_hi:[0,1]
	v_pk_mul_f32 v[44:45], v[170:171], v[54:55] op_sel_hi:[0,1]
	v_pk_mul_f32 v[48:49], v[170:171], v[52:53] op_sel_hi:[0,1]
	v_pk_mul_f32 v[40:41], v[42:43], v[40:41]
	v_lshlrev_b32_e32 v42, 16, v86
	v_and_b32_e32 v43, 0xffff0000, v86
	v_pk_mul_f32 v[38:39], v[44:45], v[38:39]
	v_mul_f32_e32 v42, 0xbfb8aa3b, v42
	v_mul_f32_e32 v43, 0xbfb8aa3b, v43
	v_pk_mul_f32 v[36:37], v[48:49], v[36:37]
	v_lshlrev_b32_e32 v44, 16, v87
	v_and_b32_e32 v45, 0xffff0000, v87
	v_lshlrev_b32_e32 v48, 16, v88
	v_and_b32_e32 v49, 0xffff0000, v88
	v_exp_f32_e32 v42, v42
	v_exp_f32_e32 v43, v43
	v_mul_f32_e32 v44, 0xbfb8aa3b, v44
	v_mul_f32_e32 v45, 0xbfb8aa3b, v45
	v_mul_f32_e32 v48, 0xbfb8aa3b, v48
	v_mul_f32_e32 v49, 0xbfb8aa3b, v49
	v_lshlrev_b32_e32 v86, 16, v89
	v_and_b32_e32 v87, 0xffff0000, v89
	v_exp_f32_e32 v44, v44
	v_exp_f32_e32 v45, v45
	v_exp_f32_e32 v48, v48
	v_exp_f32_e32 v49, v49
	v_mul_f32_e32 v86, 0xbfb8aa3b, v86
	v_mul_f32_e32 v87, 0xbfb8aa3b, v87
	v_exp_f32_e32 v86, v86
	v_exp_f32_e32 v87, v87
	v_add_f32_e32 v42, 1.0, v42
	v_add_f32_e32 v43, 1.0, v43
	v_cvt_f32_i32_e32 v35, v35
	v_cvt_f32_i32_e32 v34, v34
	v_rcp_f32_e32 v42, v42
	v_rcp_f32_e32 v43, v43
	v_add_f32_e32 v44, 1.0, v44
	v_add_f32_e32 v45, 1.0, v45
	v_add_f32_e32 v48, 1.0, v48
	v_add_f32_e32 v49, 1.0, v49
	v_rcp_f32_e32 v44, v44
	v_rcp_f32_e32 v45, v45
	v_rcp_f32_e32 v48, v48
	v_rcp_f32_e32 v49, v49
	v_add_f32_e32 v86, 1.0, v86
	v_add_f32_e32 v87, 1.0, v87
	v_rcp_f32_e32 v86, v86
	v_rcp_f32_e32 v87, v87
	v_pk_mul_f32 v[90:91], v[170:171], v[50:51] op_sel_hi:[0,1]
	s_waitcnt vmcnt(7)
	v_lshlrev_b32_e32 v88, 16, v82
	v_and_b32_e32 v89, 0xffff0000, v82
	v_pk_mul_f32 v[34:35], v[90:91], v[34:35]
	v_lshlrev_b32_e32 v82, 16, v83
	v_and_b32_e32 v83, 0xffff0000, v83
	v_pk_fma_f32 v[38:39], v[38:39], v[42:43], v[88:89]
	v_lshlrev_b32_e32 v42, 16, v84
	v_and_b32_e32 v43, 0xffff0000, v84
	v_pk_fma_f32 v[40:41], v[40:41], v[44:45], v[82:83]
	v_lshlrev_b32_e32 v44, 16, v85
	v_and_b32_e32 v45, 0xffff0000, v85
	v_pk_fma_f32 v[34:35], v[34:35], v[48:49], v[42:43]
	v_pk_fma_f32 v[44:45], v[36:37], v[86:87], v[44:45]
	v_cvt_pk_bf16_f32 v36, v38, v39
	v_cvt_pk_bf16_f32 v37, v40, v41
	v_cvt_pk_bf16_f32 v38, v34, v35
	s_nop 0
	v_lshlrev_b32_e32 v34, 16, v36
	v_and_b32_e32 v35, 0xffff0000, v36
	v_max_f32_e64 v35, |v35|, |v35|
	v_max_f32_e64 v34, |v34|, |v34|
	v_cvt_pk_bf16_f32 v39, v44, v45
	v_max_f32_e32 v34, v34, v35
	v_lshlrev_b32_e32 v35, 16, v37
	v_and_b32_e32 v40, 0xffff0000, v37
	v_lshlrev_b32_e32 v42, 16, v39
	v_and_b32_e32 v43, 0xffff0000, v39
	v_max_f32_e64 v40, |v40|, |v40|
	v_max_f32_e64 v35, |v35|, |v35|
	v_max_f32_e64 v43, |v43|, |v43|
	v_max_f32_e64 v42, |v42|, |v42|
	v_max_f32_e32 v35, v35, v40
	v_lshlrev_b32_e32 v40, 16, v38
	v_and_b32_e32 v41, 0xffff0000, v38
	v_max_f32_e32 v42, v42, v43
	v_max3_f32 v40, |v40|, |v41|, v42
	v_max3_f32 v34, v34, v35, v40
	v_max3_f32 v34, v92, 0, v34
	ds_bpermute_b32 v35, v165, v34
	global_store_dwordx4 v[46:47], v[36:39], off offset:256
	s_waitcnt lgkmcnt(0)
	v_max_f32_e32 v35, v35, v35
	v_max_f32_e32 v34, v34, v35
	ds_bpermute_b32 v35, v169, v34
	s_and_saveexec_b64 s[34:35], s[6:7]
	s_cbranch_execz .LBB0_1042
	s_waitcnt lgkmcnt(0)
	v_max_f32_e32 v35, v35, v35
	v_max_f32_e32 v34, v34, v34
	v_lshl_add_u64 v[36:37], v[114:115], 2, s[16:17]
	v_max_f32_e32 v34, v34, v35
	global_atomic_umax v[36:37], v34, off
; __device__ __forceinline__ float sigmoidf_(float x) { return __builtin_amdgcn_rcpf(1.f + __builtin_amdgcn_exp2f(-1.4426950408889634f * x)); }
;     __device__ __forceinline__ void operator()(const f32x4 (&acc)[2][2][4][2], const Unit& u, int wr, int wc, int fr, int fq) const {
;     ...
;         EPB_LOAD(0);
; #pragma unroll
;         for (int kb = 0; kb < 8; ++kb) { const int ai = kb >> 2, m = kb & 3;
;             if (kb < 7) EPB_LOAD(kb + 1);
;             { const int row = row0 + ai * HALF + m * 16; float rmx = 0.f;
; #pragma unroll
;                 for (int bj = 0; bj < 2; ++bj) { const int col = col0 + bj * HALF; f32x4 v0 = acc[ai][bj][m][0], v1 = acc[ai][bj][m][1];
;                     if (QI8) { const f32x4 c0 = cb[bj][0] * ra[ai][m], c1 = cb[bj][1] * ra[ai][m]; const i32x4 i0 = __builtin_bit_cast(i32x4, v0), i1 = __builtin_bit_cast(i32x4, v1);
;                         v0 = (f32x4){(float)i0[0], (float)i0[1], (float)i0[2], (float)i0[3]} * c0; v1 = (f32x4){(float)i1[0], (float)i1[1], (float)i1[2], (float)i1[3]} * c1; }
;                     else if (MODE == 0) { v0 = v0 * tsc; v1 = v1 * tsc; }
;                     if (!QI8 && MODE == 1) { v0 = v0 * cb[bj][0]; v1 = v1 * cb[bj][1]; }
;                     if (MODE == 2 || MODE == 3) { const u32x4 g = gq[kb & 1][bj];
;                         f32x4 g0 = {sigmoidf_(bflo(g.x)), sigmoidf_(bfhi(g.x)), sigmoidf_(bflo(g.y)), sigmoidf_(bfhi(g.y))};
;                         f32x4 g1 = {sigmoidf_(bflo(g.z)), sigmoidf_(bfhi(g.z)), sigmoidf_(bflo(g.w)), sigmoidf_(bfhi(g.w))};
;                         v0 = v0 * g0; v1 = v1 * g1;
;                         if (MODE == 3) { const u32x4 q = aq[kb & 1][bj];
;                             v0 = v0 + (f32x4){bflo(q.x), bfhi(q.x), bflo(q.y), bfhi(q.y)}; v1 = v1 + (f32x4){bflo(q.z), bfhi(q.z), bflo(q.w), bfhi(q.w)}; } }
.LBB0_1042:
	s_or_b64 exec, exec, s[34:35]
	v_or_b32_e32 v82, 48, v130
	v_ashrrev_i32_e32 v83, 31, v82
	s_waitcnt lgkmcnt(0)
	v_mov_b64_e32 v[34:35], s[14:15]
	v_lshlrev_b64 v[36:37], 13, v[82:83]
	v_mad_i64_i32 v[34:35], s[34:35], v82, s65, v[34:35]
	v_lshl_add_u64 v[36:37], s[0:1], 0, v[36:37]
	v_lshl_add_u64 v[34:35], v[34:35], 0, v[166:167]
	v_lshl_add_u64 v[36:37], v[36:37], 0, v[166:167]
	global_load_dwordx4 v[46:49], v[34:35], off nt
	global_load_dwordx4 v[38:41], v[34:35], off offset:256 nt
	global_load_dwordx4 v[42:45], v[36:37], off nt
	s_nop 0
	global_load_dwordx4 v[34:37], v[36:37], off offset:256 nt
	v_cvt_f32_i32_e32 v33, v33
	v_cvt_f32_i32_e32 v32, v32
	v_pk_mul_f32 v[86:87], v[168:169], v[68:69] op_sel_hi:[0,1]
	v_cvt_f32_i32_e32 v31, v31
	v_cvt_f32_i32_e32 v30, v30
	v_pk_mul_f32 v[32:33], v[86:87], v[32:33]
	s_waitcnt vmcnt(9)
	v_lshlrev_b32_e32 v86, 16, v78
	v_and_b32_e32 v78, 0xffff0000, v78
	v_mul_f32_e32 v86, 0xbfb8aa3b, v86
	v_mul_f32_e32 v78, 0xbfb8aa3b, v78
	v_exp_f32_e32 v86, v86
	v_exp_f32_e32 v87, v78
	v_pk_mul_f32 v[88:89], v[168:169], v[66:67] op_sel_hi:[0,1]
	v_pk_mul_f32 v[30:31], v[88:89], v[30:31]
	v_add_f32_e32 v78, 1.0, v86
	v_add_f32_e32 v86, 1.0, v87
	v_lshlrev_b32_e32 v87, 16, v79
	v_and_b32_e32 v79, 0xffff0000, v79
	v_mul_f32_e32 v87, 0xbfb8aa3b, v87
	v_mul_f32_e32 v79, 0xbfb8aa3b, v79
	v_exp_f32_e32 v87, v87
	v_exp_f32_e32 v88, v79
	v_rcp_f32_e32 v79, v86
	v_cvt_f32_i32_e32 v29, v29
	v_add_f32_e32 v86, 1.0, v87
	v_add_f32_e32 v87, 1.0, v88
	v_lshlrev_b32_e32 v88, 16, v80
	v_and_b32_e32 v80, 0xffff0000, v80
	v_mul_f32_e32 v88, 0xbfb8aa3b, v88
	v_mul_f32_e32 v80, 0xbfb8aa3b, v80
	v_exp_f32_e32 v88, v88
	v_exp_f32_e32 v89, v80
	v_cvt_f32_i32_e32 v28, v28
	v_pk_mul_f32 v[90:91], v[168:169], v[64:65] op_sel_hi:[0,1]
	v_add_f32_e32 v80, 1.0, v88
	v_add_f32_e32 v88, 1.0, v89
	v_lshlrev_b32_e32 v89, 16, v81
	v_and_b32_e32 v81, 0xffff0000, v81
	v_mul_f32_e32 v89, 0xbfb8aa3b, v89
	v_mul_f32_e32 v81, 0xbfb8aa3b, v81
	v_pk_mul_f32 v[28:29], v[90:91], v[28:29]
	v_exp_f32_e32 v89, v89
	v_exp_f32_e32 v90, v81
	v_cvt_f32_i32_e32 v27, v27
	v_cvt_f32_i32_e32 v26, v26
	v_rcp_f32_e32 v78, v78
	v_rcp_f32_e32 v86, v86
	v_rcp_f32_e32 v87, v87
	v_rcp_f32_e32 v81, v88
	v_add_f32_e32 v88, 1.0, v89
	v_add_f32_e32 v89, 1.0, v90
	v_rcp_f32_e32 v80, v80
	v_rcp_f32_e32 v88, v88
	v_rcp_f32_e32 v89, v89
	v_pk_mul_f32 v[92:93], v[168:169], v[62:63] op_sel_hi:[0,1]
	s_waitcnt vmcnt(7)
;     __device__ __forceinline__ void operator()(const f32x4 (&acc)[2][2][4][2], const Unit& u, int wr, int wc, int fr, int fq) const {
;     ...
;                 for (int bj = 0; bj < 2; ++bj) { const int col = col0 + bj * HALF; f32x4 v0 = acc[ai][bj][m][0], v1 = acc[ai][bj][m][1];
;                     if (QI8) { const f32x4 c0 = cb[bj][0] * ra[ai][m], c1 = cb[bj][1] * ra[ai][m]; const i32x4 i0 = __builtin_bit_cast(i32x4, v0), i1 = __builtin_bit_cast(i32x4, v1);
;                         v0 = (f32x4){(float)i0[0], (float)i0[1], (float)i0[2], (float)i0[3]} * c0; v1 = (f32x4){(float)i1[0], (float)i1[1], (float)i1[2], (float)i1[3]} * c1; }
;                     else if (MODE == 0) { v0 = v0 * tsc; v1 = v1 * tsc; }
;                     if (!QI8 && MODE == 1) { v0 = v0 * cb[bj][0]; v1 = v1 * cb[bj][1]; }
;                     if (MODE == 2 || MODE == 3) { const u32x4 g = gq[kb & 1][bj];
;                         f32x4 g0 = {sigmoidf_(bflo(g.x)), sigmoidf_(bfhi(g.x)), sigmoidf_(bflo(g.y)), sigmoidf_(bfhi(g.y))};
;                         f32x4 g1 = {sigmoidf_(bflo(g.z)), sigmoidf_(bfhi(g.z)), sigmoidf_(bflo(g.w)), sigmoidf_(bfhi(g.w))};
;                         v0 = v0 * g0; v1 = v1 * g1;
;                         if (MODE == 3) { const u32x4 q = aq[kb & 1][bj];
;                             v0 = v0 + (f32x4){bflo(q.x), bfhi(q.x), bflo(q.y), bfhi(q.y)}; v1 = v1 + (f32x4){bflo(q.z), bfhi(q.z), bflo(q.w), bfhi(q.w)}; } }
;                     if (MODE == 4) { v0 = v0 + rs[kb & 1][bj][0]; v1 = v1 + rs[kb & 1][bj][1]; }
;                     if (MODE == 5) { const u32x4 c = gq[kb & 1][bj], q = aq[kb & 1][bj];
;                         v0 = (f32x4){bflo(c.x) + sigmoidf_(v0[0]) * bflo(q.x), bfhi(c.x) + sigmoidf_(v0[1]) * bfhi(q.x), bflo(c.y) + sigmoidf_(v0[2]) * bflo(q.y), bfhi(c.y) + sigmoidf_(v0[3]) * bfhi(q.y)};
;                         v1 = (f32x4){bflo(c.z) + sigmoidf_(v1[0]) * bflo(q.z), bfhi(c.z) + sigmoidf_(v1[1]) * bfhi(q.z), bflo(c.w) + sigmoidf_(v1[2]) * bflo(q.w), bfhi(c.w) + sigmoidf_(v1[3]) * bfhi(q.w)}; }
;                     u32x4 w; w.x = cvtpk(v0[0], v0[1]); w.y = cvtpk(v0[2], v0[3]); w.z = cvtpk(v1[0], v1[1]); w.w = cvtpk(v1[2], v1[3]);
;                     *(u32x4*)(O + (size_t)row * ldo + col) = w;
;                     if (MODE == 0) { if (dual) { const int kc = col - ZC_KV;
	v_lshlrev_b32_e32 v90, 16, v74
	v_and_b32_e32 v91, 0xffff0000, v74
	v_lshlrev_b32_e32 v74, 16, v75
	v_and_b32_e32 v75, 0xffff0000, v75
	v_lshlrev_b64 v[84:85], 12, v[98:99]
	v_pk_mul_f32 v[26:27], v[92:93], v[26:27]
	v_pk_fma_f32 v[32:33], v[32:33], v[86:87], v[74:75]
	v_pk_fma_f32 v[30:31], v[30:31], v[78:79], v[90:91]
	v_lshlrev_b32_e32 v74, 16, v76
	v_and_b32_e32 v75, 0xffff0000, v76
	v_lshlrev_b32_e32 v76, 16, v77
	v_and_b32_e32 v77, 0xffff0000, v77
	v_pk_fma_f32 v[76:77], v[28:29], v[88:89], v[76:77]
	v_pk_fma_f32 v[28:29], v[26:27], v[80:81], v[74:75]
	v_cvt_pk_bf16_f32 v26, v30, v31
	v_lshl_add_u64 v[30:31], v[84:85], 1, s[12:13]
	v_lshl_add_u64 v[30:31], v[30:31], 0, v[166:167]
	v_cvt_pk_bf16_f32 v27, v32, v33
	v_cvt_pk_bf16_f32 v28, v28, v29
	v_cvt_pk_bf16_f32 v29, v76, v77
	global_store_dwordx4 v[30:31], v[26:29], off
	v_lshlrev_b32_e32 v32, 16, v26
	v_max_f32_e64 v32, |v32|, |v32|
	v_and_b32_e32 v26, 0xffff0000, v26
	v_max_f32_e64 v26, |v26|, |v26|
	v_max_f32_e32 v26, v32, v26
	v_lshlrev_b32_e32 v32, 16, v27
	v_and_b32_e32 v27, 0xffff0000, v27
	v_lshlrev_b32_e32 v33, 16, v29
	v_and_b32_e32 v29, 0xffff0000, v29
	v_max_f32_e64 v27, |v27|, |v27|
	v_max_f32_e64 v32, |v32|, |v32|
	v_max_f32_e64 v29, |v29|, |v29|
	v_max_f32_e64 v33, |v33|, |v33|
	v_cvt_f32_i32_e32 v25, v25
	v_cvt_f32_i32_e32 v24, v24
	v_max_f32_e32 v27, v32, v27
	v_lshlrev_b32_e32 v32, 16, v28
	v_and_b32_e32 v28, 0xffff0000, v28
	v_max_f32_e32 v29, v33, v29
	v_cvt_f32_i32_e32 v23, v23
	v_cvt_f32_i32_e32 v22, v22
	v_cvt_f32_i32_e32 v21, v21
	v_cvt_f32_i32_e32 v20, v20
	v_max3_f32 v28, |v32|, |v28|, v29
	v_max3_f32 v76, v26, v27, v28
	v_pk_mul_f32 v[26:27], v[168:169], v[56:57] op_sel_hi:[0,1]
	v_pk_mul_f32 v[28:29], v[168:169], v[54:55] op_sel_hi:[0,1]
	v_pk_mul_f32 v[32:33], v[168:169], v[52:53] op_sel_hi:[0,1]
	v_pk_mul_f32 v[24:25], v[26:27], v[24:25]
	v_lshlrev_b32_e32 v26, 16, v70
	v_and_b32_e32 v27, 0xffff0000, v70
	v_pk_mul_f32 v[22:23], v[28:29], v[22:23]
	v_mul_f32_e32 v26, 0xbfb8aa3b, v26
	v_mul_f32_e32 v27, 0xbfb8aa3b, v27
	v_pk_mul_f32 v[20:21], v[32:33], v[20:21]
	v_lshlrev_b32_e32 v28, 16, v71
	v_and_b32_e32 v29, 0xffff0000, v71
	v_lshlrev_b32_e32 v32, 16, v72
	v_and_b32_e32 v33, 0xffff0000, v72
	v_exp_f32_e32 v26, v26
	v_exp_f32_e32 v27, v27
	v_mul_f32_e32 v28, 0xbfb8aa3b, v28
	v_mul_f32_e32 v29, 0xbfb8aa3b, v29
	v_mul_f32_e32 v32, 0xbfb8aa3b, v32
	v_mul_f32_e32 v33, 0xbfb8aa3b, v33
	v_lshlrev_b32_e32 v70, 16, v73
	v_and_b32_e32 v71, 0xffff0000, v73
	v_exp_f32_e32 v28, v28
	v_exp_f32_e32 v29, v29
	v_exp_f32_e32 v32, v32
	v_exp_f32_e32 v33, v33
	v_mul_f32_e32 v70, 0xbfb8aa3b, v70
	v_mul_f32_e32 v71, 0xbfb8aa3b, v71
	v_exp_f32_e32 v70, v70
	v_exp_f32_e32 v71, v71
	v_add_f32_e32 v26, 1.0, v26
	v_add_f32_e32 v27, 1.0, v27
	v_cvt_f32_i32_e32 v19, v19
	v_cvt_f32_i32_e32 v18, v18
	v_rcp_f32_e32 v26, v26
	v_rcp_f32_e32 v27, v27
	v_add_f32_e32 v28, 1.0, v28
	v_add_f32_e32 v29, 1.0, v29
	v_add_f32_e32 v32, 1.0, v32
	v_add_f32_e32 v33, 1.0, v33
	v_rcp_f32_e32 v28, v28
	v_rcp_f32_e32 v29, v29
	v_rcp_f32_e32 v32, v32
	v_rcp_f32_e32 v33, v33
	v_add_f32_e32 v70, 1.0, v70
	v_add_f32_e32 v71, 1.0, v71
	v_rcp_f32_e32 v70, v70
	v_rcp_f32_e32 v71, v71
	v_pk_mul_f32 v[74:75], v[168:169], v[50:51] op_sel_hi:[0,1]
	s_waitcnt vmcnt(7)
	v_lshlrev_b32_e32 v72, 16, v58
	v_and_b32_e32 v73, 0xffff0000, v58
	v_pk_mul_f32 v[18:19], v[74:75], v[18:19]
	v_lshlrev_b32_e32 v58, 16, v59
	v_and_b32_e32 v59, 0xffff0000, v59
	v_pk_fma_f32 v[22:23], v[22:23], v[26:27], v[72:73]
	v_lshlrev_b32_e32 v26, 16, v60
	v_and_b32_e32 v27, 0xffff0000, v60
	v_pk_fma_f32 v[24:25], v[24:25], v[28:29], v[58:59]
	v_lshlrev_b32_e32 v28, 16, v61
	v_and_b32_e32 v29, 0xffff0000, v61
	v_pk_fma_f32 v[18:19], v[18:19], v[32:33], v[26:27]
	v_pk_fma_f32 v[28:29], v[20:21], v[70:71], v[28:29]
	v_cvt_pk_bf16_f32 v20, v22, v23
	v_cvt_pk_bf16_f32 v21, v24, v25
	v_cvt_pk_bf16_f32 v22, v18, v19
	s_nop 0
	v_lshlrev_b32_e32 v18, 16, v20
	v_and_b32_e32 v19, 0xffff0000, v20
	v_max_f32_e64 v19, |v19|, |v19|
	v_max_f32_e64 v18, |v18|, |v18|
	v_cvt_pk_bf16_f32 v23, v28, v29
	v_max_f32_e32 v18, v18, v19
	v_lshlrev_b32_e32 v19, 16, v21
	v_and_b32_e32 v24, 0xffff0000, v21
	v_lshlrev_b32_e32 v26, 16, v23
	v_and_b32_e32 v27, 0xffff0000, v23
	v_max_f32_e64 v24, |v24|, |v24|
	v_max_f32_e64 v19, |v19|, |v19|
	v_max_f32_e64 v27, |v27|, |v27|
	v_max_f32_e64 v26, |v26|, |v26|
	v_max_f32_e32 v19, v19, v24
	v_lshlrev_b32_e32 v24, 16, v22
	v_and_b32_e32 v25, 0xffff0000, v22
	v_max_f32_e32 v26, v26, v27
	v_max3_f32 v24, |v24|, |v25|, v26
	v_max3_f32 v18, v18, v19, v24
	v_max3_f32 v18, v76, 0, v18
	ds_bpermute_b32 v19, v165, v18
	global_store_dwordx4 v[30:31], v[20:23], off offset:256
	s_waitcnt lgkmcnt(0)
	v_max_f32_e32 v19, v19, v19
	v_max_f32_e32 v18, v18, v19
	ds_bpermute_b32 v19, v169, v18
	s_and_saveexec_b64 s[34:35], s[6:7]
	s_cbranch_execz .LBB0_1044
	s_waitcnt lgkmcnt(0)
	v_max_f32_e32 v19, v19, v19
	v_max_f32_e32 v18, v18, v18
	v_lshl_add_u64 v[20:21], v[98:99], 2, s[16:17]
	v_max_f32_e32 v18, v18, v19
	global_atomic_umax v[20:21], v18, off

;     __device__ __forceinline__ void operator()(const f32x4 (&acc)[2][2][4][2], const Unit& u, int wr, int wc, int fr, int fq) const {
;     ...
;         if (QI8) {
; #pragma unroll
;             for (int ai = 0; ai < 2; ++ai)
; #pragma unroll
;                 for (int m = 0; m < 4; ++m) ra[ai][m] = sa[row0 + ai * HALF + m * 16];
; #pragma unroll
;             for (int bj = 0; bj < 2; ++bj) { cb[bj][0] = *(const f32x4*)(sb + col0 + bj * HALF) * tsc; cb[bj][1] = *(const f32x4*)(sb + col0 + bj * HALF + 4) * tsc; } }
;         else if (MODE == 1) {
; #pragma unroll
;             for (int bj = 0; bj < 2; ++bj) { cb[bj][0] = *(const f32x4*)(colscale + col0 + bj * HALF); cb[bj][1] = *(const f32x4*)(colscale + col0 + bj * HALF + 4); } }
;         const bool dual = (MODE == 0) && aux != nullptr && u.pn >= ZC_KV / 256 && u.pn < ZC_KV / 256 + 4;
;         u32x4 gq[2][2], aq[2][2]; f32x4 rs[2][2][2];
;     ...
;         EPB_LOAD(0);
; #pragma unroll
;         for (int kb = 0; kb < 8; ++kb) { const int ai = kb >> 2, m = kb & 3;
;             if (kb < 7) EPB_LOAD(kb + 1);
;             { const int row = row0 + ai * HALF + m * 16; float rmx = 0.f;
; #pragma unroll
;                 for (int bj = 0; bj < 2; ++bj) { const int col = col0 + bj * HALF; f32x4 v0 = acc[ai][bj][m][0], v1 = acc[ai][bj][m][1];
;                     if (QI8) { const f32x4 c0 = cb[bj][0] * ra[ai][m], c1 = cb[bj][1] * ra[ai][m]; const i32x4 i0 = __builtin_bit_cast(i32x4, v0), i1 = __builtin_bit_cast(i32x4, v1);
;                         v0 = (f32x4){(float)i0[0], (float)i0[1], (float)i0[2], (float)i0[3]} * c0; v1 = (f32x4){(float)i1[0], (float)i1[1], (float)i1[2], (float)i1[3]} * c1; }
;                     else if (MODE == 0) { v0 = v0 * tsc; v1 = v1 * tsc; }
;                     if (!QI8 && MODE == 1) { v0 = v0 * cb[bj][0]; v1 = v1 * cb[bj][1]; }
;                     if (MODE == 2 || MODE == 3) { const u32x4 g = gq[kb & 1][bj];
;                         f32x4 g0 = {sigmoidf_(bflo(g.x)), sigmoidf_(bfhi(g.x)), sigmoidf_(bflo(g.y)), sigmoidf_(bfhi(g.y))};
;                         f32x4 g1 = {sigmoidf_(bflo(g.z)), sigmoidf_(bfhi(g.z)), sigmoidf_(bflo(g.w)), sigmoidf_(bfhi(g.w))};
;                         v0 = v0 * g0; v1 = v1 * g1;
;                         if (MODE == 3) { const u32x4 q = aq[kb & 1][bj];
.LBB0_1737:
	v_lshl_add_u32 v166, s28, 8, v195
	v_ashrrev_i32_e32 v167, 31, v166
	v_lshl_or_b32 v138, s60, 8, v223
	v_lshl_add_u64 v[136:137], v[166:167], 2, s[2:3]
	v_ashrrev_i32_e32 v139, 31, v138
	global_load_dword v180, v[136:137], off
	v_lshl_add_u64 v[140:141], v[138:139], 2, s[4:5]
	global_load_dwordx4 v[76:79], v[140:141], off
	global_load_dwordx4 v[72:75], v[140:141], off offset:16
	v_lshlrev_b64 v[210:211], 13, v[166:167]
	v_lshl_add_u64 v[142:143], s[8:9], 0, v[210:211]
	v_lshl_add_u64 v[148:149], s[10:11], 0, v[210:211]
	v_lshlrev_b64 v[160:161], 1, v[138:139]
	v_lshl_add_u64 v[138:139], v[142:143], 0, v[160:161]
	v_lshl_add_u64 v[142:143], v[148:149], 0, v[160:161]
	global_load_dwordx4 v[144:147], v[138:139], off nt
	global_load_dwordx4 v[148:151], v[142:143], off nt
	v_cvt_f32_i32_e32 v213, v61
	v_cvt_f32_i32_e32 v212, v60
	v_cvt_f32_i32_e32 v215, v63
	v_cvt_f32_i32_e32 v214, v62
	v_cvt_f32_i32_e32 v217, v57
	v_cvt_f32_i32_e32 v216, v56
	v_cvt_f32_i32_e32 v219, v59
	v_cvt_f32_i32_e32 v218, v58
	global_load_dword v178, v[136:137], off offset:64
	global_load_dword v176, v[136:137], off offset:128
	global_load_dword v174, v[136:137], off offset:192
	global_load_dword v170, v[136:137], off offset:512
	global_load_dword v168, v[136:137], off offset:576
	global_load_dword v164, v[136:137], off offset:640
	global_load_dword v162, v[136:137], off offset:704
	global_load_dwordx4 v[56:59], v[140:141], off offset:528
	global_load_dwordx4 v[60:63], v[140:141], off offset:512
	global_load_dwordx4 v[184:187], v[138:139], off offset:256 nt
	global_load_dwordx4 v[188:191], v[142:143], off offset:256 nt
	v_or_b32_e32 v152, 16, v166
	v_ashrrev_i32_e32 v153, 31, v152
	v_lshlrev_b64 v[182:183], 13, v[152:153]
	v_lshl_add_u64 v[136:137], s[8:9], 0, v[182:183]
	v_lshl_add_u64 v[140:141], s[10:11], 0, v[182:183]
	v_lshl_add_u64 v[136:137], v[136:137], 0, v[160:161]
	v_lshl_add_u64 v[140:141], v[140:141], 0, v[160:161]
	global_load_dwordx4 v[152:155], v[136:137], off nt
	s_nop 0
	global_load_dwordx4 v[136:139], v[136:137], off offset:256 nt
	s_nop 0
	global_load_dwordx4 v[156:159], v[140:141], off nt
	s_nop 0
	global_load_dwordx4 v[140:143], v[140:141], off offset:256 nt
	v_readlane_b32 s30, v245, 9
	v_readlane_b32 s31, v245, 10
	v_cvt_f32_i32_e32 v133, v133
	v_cvt_f32_i32_e32 v132, v132
	v_cvt_f32_i32_e32 v135, v135
	v_cvt_f32_i32_e32 v134, v134
	v_cvt_f32_i32_e32 v129, v129
	v_cvt_f32_i32_e32 v128, v128
	v_cvt_f32_i32_e32 v131, v131
	v_cvt_f32_i32_e32 v130, v130
	v_cvt_f32_i32_e32 v125, v125
	v_cvt_f32_i32_e32 v124, v124
	v_cvt_f32_i32_e32 v127, v127
	v_cvt_f32_i32_e32 v126, v126
	v_cvt_f32_i32_e32 v121, v121
	v_cvt_f32_i32_e32 v120, v120
	v_cvt_f32_i32_e32 v123, v123
	v_cvt_f32_i32_e32 v122, v122
	v_cvt_f32_i32_e32 v117, v117
	v_cvt_f32_i32_e32 v116, v116
	v_cvt_f32_i32_e32 v119, v119
	v_cvt_f32_i32_e32 v118, v118
	v_cvt_f32_i32_e32 v113, v113
	v_cvt_f32_i32_e32 v112, v112
	v_cvt_f32_i32_e32 v115, v115
	v_cvt_f32_i32_e32 v114, v114
	v_cvt_f32_i32_e32 v109, v109
	v_cvt_f32_i32_e32 v108, v108
	v_cvt_f32_i32_e32 v111, v111
	v_cvt_f32_i32_e32 v110, v110
	v_cvt_f32_i32_e32 v105, v105
	v_cvt_f32_i32_e32 v104, v104
	v_cvt_f32_i32_e32 v107, v107
	v_cvt_f32_i32_e32 v106, v106
	v_cvt_f32_i32_e32 v101, v101
	v_cvt_f32_i32_e32 v100, v100
	v_cvt_f32_i32_e32 v103, v103
	v_cvt_f32_i32_e32 v102, v102
	v_cvt_f32_i32_e32 v97, v97
	v_cvt_f32_i32_e32 v96, v96
	v_cvt_f32_i32_e32 v99, v99
	v_cvt_f32_i32_e32 v98, v98
	v_cvt_f32_i32_e32 v93, v93
	v_cvt_f32_i32_e32 v92, v92
	v_lshl_add_u64 v[172:173], v[210:211], 0, s[16:17]
	v_cvt_f32_i32_e32 v95, v95
	v_cvt_f32_i32_e32 v94, v94
	v_cvt_f32_i32_e32 v89, v89
	v_cvt_f32_i32_e32 v88, v88
	v_cvt_f32_i32_e32 v91, v91
	v_cvt_f32_i32_e32 v90, v90
	v_cvt_f32_i32_e32 v85, v85
	s_waitcnt vmcnt(0)
	v_pk_mul_f32 v[220:221], v[180:181], v[76:77] op_sel_hi:[0,1]
	v_pk_mul_f32 v[228:229], v[180:181], v[78:79] op_sel_hi:[0,1]
	v_pk_mul_f32 v[230:231], v[180:181], v[72:73] op_sel_hi:[0,1]
	v_pk_mul_f32 v[212:213], v[220:221], v[212:213]
	v_pk_mul_f32 v[214:215], v[228:229], v[214:215]
	v_pk_mul_f32 v[216:217], v[230:231], v[216:217]
	v_mul_f32_e32 v169, 0xbfb8aa3b, v213
	v_mul_f32_e32 v175, 0xbfb8aa3b, v214
	v_mul_f32_e32 v214, 0xbfb8aa3b, v217
	v_exp_f32_e32 v169, v169
	v_exp_f32_e32 v214, v214
	v_pk_mul_f32 v[232:233], v[180:181], v[74:75] op_sel_hi:[0,1]
	v_lshlrev_b32_e32 v163, 16, v144
	v_add_f32_e32 v169, 1.0, v169
	v_add_f32_e32 v214, 1.0, v214
	v_rcp_f32_e32 v169, v169
	v_rcp_f32_e32 v214, v214
	v_lshlrev_b32_e32 v167, 16, v148
	v_and_b32_e32 v144, 0xffff0000, v144
	v_and_b32_e32 v148, 0xffff0000, v148
	v_pk_mul_f32 v[218:219], v[232:233], v[218:219]
	v_mul_f32_e32 v165, 0xbfb8aa3b, v212
	v_mul_f32_e32 v179, 0xbfb8aa3b, v215
	v_lshlrev_b32_e32 v181, 16, v146
	v_and_b32_e32 v146, 0xffff0000, v146
	v_fmac_f32_e32 v144, v169, v148
	v_and_b32_e32 v148, 0xffff0000, v150
	v_exp_f32_e32 v165, v165
	v_exp_f32_e32 v179, v179
	v_fmac_f32_e32 v146, v214, v148
	v_mul_f32_e32 v148, 0xbfb8aa3b, v218
	v_lshlrev_b32_e32 v213, 16, v150
	v_exp_f32_e32 v148, v148
	v_mul_f32_e32 v150, 0xbfb8aa3b, v219
	v_mul_f32_e32 v212, 0xbfb8aa3b, v216
	v_exp_f32_e32 v150, v150
	v_exp_f32_e32 v175, v175
	v_exp_f32_e32 v212, v212
	v_add_f32_e32 v165, 1.0, v165
	v_add_f32_e32 v179, 1.0, v179
	v_rcp_f32_e32 v165, v165
	v_rcp_f32_e32 v179, v179
	v_add_f32_e32 v148, 1.0, v148
	v_rcp_f32_e32 v148, v148
	v_add_f32_e32 v150, 1.0, v150
	v_add_f32_e32 v175, 1.0, v175
	v_add_f32_e32 v212, 1.0, v212
	v_rcp_f32_e32 v150, v150
	v_lshlrev_b32_e32 v171, 16, v145
	v_lshlrev_b32_e32 v177, 16, v149
	v_and_b32_e32 v145, 0xffff0000, v145
	v_and_b32_e32 v149, 0xffff0000, v149
;     __device__ __forceinline__ void operator()(const f32x4 (&acc)[2][2][4][2], const Unit& u, int wr, int wc, int fr, int fq) const {
;     ...
;         EPB_LOAD(0);
; #pragma unroll
;         for (int kb = 0; kb < 8; ++kb) { const int ai = kb >> 2, m = kb & 3;
;             if (kb < 7) EPB_LOAD(kb + 1);
;             { const int row = row0 + ai * HALF + m * 16; float rmx = 0.f;
; #pragma unroll
;                 for (int bj = 0; bj < 2; ++bj) { const int col = col0 + bj * HALF; f32x4 v0 = acc[ai][bj][m][0], v1 = acc[ai][bj][m][1];
;                     if (QI8) { const f32x4 c0 = cb[bj][0] * ra[ai][m], c1 = cb[bj][1] * ra[ai][m]; const i32x4 i0 = __builtin_bit_cast(i32x4, v0), i1 = __builtin_bit_cast(i32x4, v1);
;                         v0 = (f32x4){(float)i0[0], (float)i0[1], (float)i0[2], (float)i0[3]} * c0; v1 = (f32x4){(float)i1[0], (float)i1[1], (float)i1[2], (float)i1[3]} * c1; }
;                     else if (MODE == 0) { v0 = v0 * tsc; v1 = v1 * tsc; }
;                     if (!QI8 && MODE == 1) { v0 = v0 * cb[bj][0]; v1 = v1 * cb[bj][1]; }
;                     if (MODE == 2 || MODE == 3) { const u32x4 g = gq[kb & 1][bj];
;                         f32x4 g0 = {sigmoidf_(bflo(g.x)), sigmoidf_(bfhi(g.x)), sigmoidf_(bflo(g.y)), sigmoidf_(bfhi(g.y))};
;                         f32x4 g1 = {sigmoidf_(bflo(g.z)), sigmoidf_(bfhi(g.z)), sigmoidf_(bflo(g.w)), sigmoidf_(bfhi(g.w))};
;                         v0 = v0 * g0; v1 = v1 * g1;
;                         if (MODE == 3) { const u32x4 q = aq[kb & 1][bj];
;                             v0 = v0 + (f32x4){bflo(q.x), bfhi(q.x), bflo(q.y), bfhi(q.y)}; v1 = v1 + (f32x4){bflo(q.z), bfhi(q.z), bflo(q.w), bfhi(q.w)}; } }
;                     if (MODE == 4) { v0 = v0 + rs[kb & 1][bj][0]; v1 = v1 + rs[kb & 1][bj][1]; }
;                     if (MODE == 5) { const u32x4 c = gq[kb & 1][bj], q = aq[kb & 1][bj];
;                         v0 = (f32x4){bflo(c.x) + sigmoidf_(v0[0]) * bflo(q.x), bfhi(c.x) + sigmoidf_(v0[1]) * bfhi(q.x), bflo(c.y) + sigmoidf_(v0[2]) * bflo(q.y), bfhi(c.y) + sigmoidf_(v0[3]) * bfhi(q.y)};
;                         v1 = (f32x4){bflo(c.z) + sigmoidf_(v1[0]) * bflo(q.z), bfhi(c.z) + sigmoidf_(v1[1]) * bfhi(q.z), bflo(c.w) + sigmoidf_(v1[2]) * bflo(q.w), bfhi(c.w) + sigmoidf_(v1[3]) * bfhi(q.w)}; }
	v_rcp_f32_e32 v175, v175
	v_rcp_f32_e32 v212, v212
	v_fmac_f32_e32 v163, v165, v167
	v_fmac_f32_e32 v145, v179, v149
	v_lshlrev_b32_e32 v149, 16, v147
	v_lshlrev_b32_e32 v165, 16, v151
	v_fmac_f32_e32 v149, v148, v165
	v_and_b32_e32 v147, 0xffff0000, v147
	v_and_b32_e32 v148, 0xffff0000, v151
	v_fmac_f32_e32 v147, v150, v148
	v_fmac_f32_e32 v171, v175, v177
	v_fmac_f32_e32 v181, v212, v213
	v_cvt_pk_bf16_f32 v144, v163, v144
	v_cvt_pk_bf16_f32 v145, v171, v145
	v_cvt_pk_bf16_f32 v146, v181, v146
	v_cvt_pk_bf16_f32 v147, v149, v147
	v_lshl_add_u64 v[148:149], s[30:31], 0, v[210:211]
	v_lshl_add_u64 v[148:149], v[148:149], 0, v[160:161]
	global_store_dwordx4 v[148:149], v[144:147], off
	v_pk_mul_f32 v[150:151], v[180:181], v[56:57] op_sel_hi:[0,1]
	v_pk_mul_f32 v[128:129], v[150:151], v[128:129]
	v_pk_mul_f32 v[144:145], v[180:181], v[60:61] op_sel_hi:[0,1]
	v_pk_mul_f32 v[132:133], v[144:145], v[132:133]
	v_pk_mul_f32 v[146:147], v[180:181], v[62:63] op_sel_hi:[0,1]
	v_mul_f32_e32 v132, 0xbfb8aa3b, v132
	v_exp_f32_e32 v132, v132
	v_mul_f32_e32 v133, 0xbfb8aa3b, v133
	v_exp_f32_e32 v133, v133
	v_lshlrev_b32_e32 v144, 16, v184
	v_add_f32_e32 v132, 1.0, v132
	v_rcp_f32_e32 v132, v132
	v_add_f32_e32 v133, 1.0, v133
	v_rcp_f32_e32 v133, v133
	v_lshlrev_b32_e32 v145, 16, v188
	v_pk_mul_f32 v[134:135], v[146:147], v[134:135]
	v_fmac_f32_e32 v144, v132, v145
	v_and_b32_e32 v132, 0xffff0000, v184
	v_and_b32_e32 v145, 0xffff0000, v188
	v_fmac_f32_e32 v132, v133, v145
	v_mul_f32_e32 v133, 0xbfb8aa3b, v134
	v_exp_f32_e32 v133, v133
	v_mul_f32_e32 v135, 0xbfb8aa3b, v135
	v_exp_f32_e32 v135, v135
	v_mul_f32_e32 v128, 0xbfb8aa3b, v128
	v_exp_f32_e32 v128, v128
	v_mul_f32_e32 v129, 0xbfb8aa3b, v129
	v_exp_f32_e32 v129, v129
	v_add_f32_e32 v133, 1.0, v133
	v_rcp_f32_e32 v133, v133
	v_add_f32_e32 v135, 1.0, v135
	v_rcp_f32_e32 v135, v135
	v_add_f32_e32 v128, 1.0, v128
	v_rcp_f32_e32 v128, v128
	v_add_f32_e32 v129, 1.0, v129
	v_lshlrev_b32_e32 v134, 16, v185
	v_lshlrev_b32_e32 v145, 16, v189
	v_rcp_f32_e32 v129, v129
	v_fmac_f32_e32 v134, v133, v145
	v_and_b32_e32 v133, 0xffff0000, v185
	v_and_b32_e32 v145, 0xffff0000, v189
	v_pk_mul_f32 v[180:181], v[180:181], v[58:59] op_sel_hi:[0,1]
	v_fmac_f32_e32 v133, v135, v145
	v_lshlrev_b32_e32 v135, 16, v186
	v_lshlrev_b32_e32 v145, 16, v190
	v_pk_mul_f32 v[130:131], v[180:181], v[130:131]
	v_fmac_f32_e32 v135, v128, v145
	v_and_b32_e32 v145, 0xffff0000, v186
	v_and_b32_e32 v128, 0xffff0000, v190
	v_fmac_f32_e32 v145, v129, v128
	v_mul_f32_e32 v128, 0xbfb8aa3b, v130
	v_exp_f32_e32 v128, v128
	v_mul_f32_e32 v129, 0xbfb8aa3b, v131
	v_exp_f32_e32 v129, v129
	v_lshlrev_b32_e32 v146, 16, v187
	v_add_f32_e32 v128, 1.0, v128
	v_rcp_f32_e32 v128, v128
	v_add_f32_e32 v129, 1.0, v129
	v_rcp_f32_e32 v129, v129
	v_lshlrev_b32_e32 v130, 16, v191
	v_fmac_f32_e32 v146, v128, v130
	v_and_b32_e32 v131, 0xffff0000, v187
	v_and_b32_e32 v128, 0xffff0000, v191
	v_pk_mul_f32 v[184:185], v[178:179], v[76:77] op_sel_hi:[0,1]
	v_fmac_f32_e32 v131, v129, v128
	v_cvt_pk_bf16_f32 v128, v144, v132
	v_pk_mul_f32 v[124:125], v[184:185], v[124:125]
	v_cvt_pk_bf16_f32 v129, v134, v133
	v_cvt_pk_bf16_f32 v130, v135, v145
	v_cvt_pk_bf16_f32 v131, v146, v131
	global_store_dwordx4 v[148:149], v[128:131], off offset:256
	v_mul_f32_e32 v124, 0xbfb8aa3b, v124
	v_exp_f32_e32 v124, v124
	v_or_b32_e32 v128, 32, v166
	v_ashrrev_i32_e32 v129, 31, v128
	v_mul_f32_e32 v125, 0xbfb8aa3b, v125
	v_lshlrev_b64 v[180:181], 13, v[128:129]
	v_exp_f32_e32 v125, v125
	v_lshl_add_u64 v[128:129], s[8:9], 0, v[180:181]
	v_lshl_add_u64 v[130:131], s[10:11], 0, v[180:181]
	v_lshl_add_u64 v[128:129], v[128:129], 0, v[160:161]
	v_lshl_add_u64 v[132:133], v[130:131], 0, v[160:161]
	global_load_dwordx4 v[144:147], v[128:129], off nt
	s_nop 0
	global_load_dwordx4 v[128:131], v[128:129], off offset:256 nt
	s_nop 0
	global_load_dwordx4 v[148:151], v[132:133], off nt
	s_nop 0
	global_load_dwordx4 v[132:135], v[132:133], off offset:256 nt
	v_add_f32_e32 v124, 1.0, v124
	v_rcp_f32_e32 v124, v124
	v_add_f32_e32 v125, 1.0, v125
	v_rcp_f32_e32 v125, v125
	v_pk_mul_f32 v[186:187], v[178:179], v[78:79] op_sel_hi:[0,1]
	v_lshlrev_b32_e32 v163, 16, v152
	v_lshlrev_b32_e32 v165, 16, v156
	v_pk_mul_f32 v[126:127], v[186:187], v[126:127]
	v_fmac_f32_e32 v163, v124, v165
	v_and_b32_e32 v124, 0xffff0000, v152
	v_and_b32_e32 v152, 0xffff0000, v156
	v_pk_mul_f32 v[188:189], v[178:179], v[72:73] op_sel_hi:[0,1]
	v_fmac_f32_e32 v124, v125, v152
	v_mul_f32_e32 v125, 0xbfb8aa3b, v126
	v_pk_mul_f32 v[120:121], v[188:189], v[120:121]
	v_exp_f32_e32 v125, v125
	v_mul_f32_e32 v127, 0xbfb8aa3b, v127
	v_exp_f32_e32 v127, v127
	v_mul_f32_e32 v120, 0xbfb8aa3b, v120
	v_exp_f32_e32 v120, v120
	v_mul_f32_e32 v121, 0xbfb8aa3b, v121
	v_exp_f32_e32 v121, v121
	v_add_f32_e32 v125, 1.0, v125
	v_rcp_f32_e32 v125, v125
	v_add_f32_e32 v127, 1.0, v127
	v_rcp_f32_e32 v127, v127
	v_add_f32_e32 v120, 1.0, v120
	v_rcp_f32_e32 v120, v120
	v_add_f32_e32 v121, 1.0, v121
	v_lshlrev_b32_e32 v126, 16, v153
	v_lshlrev_b32_e32 v152, 16, v157
	v_rcp_f32_e32 v121, v121
	v_fmac_f32_e32 v126, v125, v152
	v_and_b32_e32 v125, 0xffff0000, v153
	v_and_b32_e32 v152, 0xffff0000, v157
	v_pk_mul_f32 v[190:191], v[178:179], v[74:75] op_sel_hi:[0,1]
	v_fmac_f32_e32 v125, v127, v152
	v_lshlrev_b32_e32 v127, 16, v154
	v_lshlrev_b32_e32 v152, 16, v158
	v_pk_mul_f32 v[122:123], v[190:191], v[122:123]
	v_fmac_f32_e32 v127, v120, v152
	v_and_b32_e32 v152, 0xffff0000, v154
	v_and_b32_e32 v120, 0xffff0000, v158
	v_fmac_f32_e32 v152, v121, v120
	v_mul_f32_e32 v120, 0xbfb8aa3b, v122
	v_exp_f32_e32 v120, v120
	v_mul_f32_e32 v121, 0xbfb8aa3b, v123
;     __device__ __forceinline__ void operator()(const f32x4 (&acc)[2][2][4][2], const Unit& u, int wr, int wc, int fr, int fq) const {
;     ...
;         EPB_LOAD(0);
; #pragma unroll
;         for (int kb = 0; kb < 8; ++kb) { const int ai = kb >> 2, m = kb & 3;
;             if (kb < 7) EPB_LOAD(kb + 1);
;             { const int row = row0 + ai * HALF + m * 16; float rmx = 0.f;
; #pragma unroll
;                 for (int bj = 0; bj < 2; ++bj) { const int col = col0 + bj * HALF; f32x4 v0 = acc[ai][bj][m][0], v1 = acc[ai][bj][m][1];
;                     if (QI8) { const f32x4 c0 = cb[bj][0] * ra[ai][m], c1 = cb[bj][1] * ra[ai][m]; const i32x4 i0 = __builtin_bit_cast(i32x4, v0), i1 = __builtin_bit_cast(i32x4, v1);
;                         v0 = (f32x4){(float)i0[0], (float)i0[1], (float)i0[2], (float)i0[3]} * c0; v1 = (f32x4){(float)i1[0], (float)i1[1], (float)i1[2], (float)i1[3]} * c1; }
;                     else if (MODE == 0) { v0 = v0 * tsc; v1 = v1 * tsc; }
;                     if (!QI8 && MODE == 1) { v0 = v0 * cb[bj][0]; v1 = v1 * cb[bj][1]; }
;                     if (MODE == 2 || MODE == 3) { const u32x4 g = gq[kb & 1][bj];
;                         f32x4 g0 = {sigmoidf_(bflo(g.x)), sigmoidf_(bfhi(g.x)), sigmoidf_(bflo(g.y)), sigmoidf_(bfhi(g.y))};
;                         f32x4 g1 = {sigmoidf_(bflo(g.z)), sigmoidf_(bfhi(g.z)), sigmoidf_(bflo(g.w)), sigmoidf_(bfhi(g.w))};
;                         v0 = v0 * g0; v1 = v1 * g1;
;                         if (MODE == 3) { const u32x4 q = aq[kb & 1][bj];
;                             v0 = v0 + (f32x4){bflo(q.x), bfhi(q.x), bflo(q.y), bfhi(q.y)}; v1 = v1 + (f32x4){bflo(q.z), bfhi(q.z), bflo(q.w), bfhi(q.w)}; } }
;                     if (MODE == 4) { v0 = v0 + rs[kb & 1][bj][0]; v1 = v1 + rs[kb & 1][bj][1]; }
;                     if (MODE == 5) { const u32x4 c = gq[kb & 1][bj], q = aq[kb & 1][bj];
;                         v0 = (f32x4){bflo(c.x) + sigmoidf_(v0[0]) * bflo(q.x), bfhi(c.x) + sigmoidf_(v0[1]) * bfhi(q.x), bflo(c.y) + sigmoidf_(v0[2]) * bflo(q.y), bfhi(c.y) + sigmoidf_(v0[3]) * bfhi(q.y)};
;                         v1 = (f32x4){bflo(c.z) + sigmoidf_(v1[0]) * bflo(q.z), bfhi(c.z) + sigmoidf_(v1[1]) * bfhi(q.z), bflo(c.w) + sigmoidf_(v1[2]) * bflo(q.w), bfhi(c.w) + sigmoidf_(v1[3]) * bfhi(q.w)}; }
	v_exp_f32_e32 v121, v121
	v_lshlrev_b32_e32 v153, 16, v155
	v_add_f32_e32 v120, 1.0, v120
	v_rcp_f32_e32 v120, v120
	v_add_f32_e32 v121, 1.0, v121
	v_rcp_f32_e32 v121, v121
	v_lshlrev_b32_e32 v122, 16, v159
	v_fmac_f32_e32 v153, v120, v122
	v_and_b32_e32 v123, 0xffff0000, v155
	v_and_b32_e32 v120, 0xffff0000, v159
	v_fmac_f32_e32 v123, v121, v120
	v_cvt_pk_bf16_f32 v120, v163, v124
	v_cvt_pk_bf16_f32 v121, v126, v125
	v_lshl_add_u64 v[124:125], s[30:31], 0, v[182:183]
	v_lshl_add_u64 v[124:125], v[124:125], 0, v[160:161]
	v_cvt_pk_bf16_f32 v122, v127, v152
	v_cvt_pk_bf16_f32 v123, v153, v123
	global_store_dwordx4 v[124:125], v[120:123], off
	v_pk_mul_f32 v[126:127], v[178:179], v[56:57] op_sel_hi:[0,1]
	v_pk_mul_f32 v[112:113], v[126:127], v[112:113]
	v_pk_mul_f32 v[120:121], v[178:179], v[60:61] op_sel_hi:[0,1]
	v_pk_mul_f32 v[116:117], v[120:121], v[116:117]
	v_pk_mul_f32 v[122:123], v[178:179], v[62:63] op_sel_hi:[0,1]
	v_mul_f32_e32 v116, 0xbfb8aa3b, v116
	v_exp_f32_e32 v116, v116
	v_mul_f32_e32 v117, 0xbfb8aa3b, v117
	v_exp_f32_e32 v117, v117
	v_lshlrev_b32_e32 v120, 16, v136
	v_add_f32_e32 v116, 1.0, v116
	v_rcp_f32_e32 v116, v116
	v_add_f32_e32 v117, 1.0, v117
	v_rcp_f32_e32 v117, v117
	v_lshlrev_b32_e32 v121, 16, v140
	v_pk_mul_f32 v[118:119], v[122:123], v[118:119]
	v_fmac_f32_e32 v120, v116, v121
	v_and_b32_e32 v116, 0xffff0000, v136
	v_and_b32_e32 v121, 0xffff0000, v140
	v_fmac_f32_e32 v116, v117, v121
	v_mul_f32_e32 v117, 0xbfb8aa3b, v118
	v_exp_f32_e32 v117, v117
	v_mul_f32_e32 v119, 0xbfb8aa3b, v119
	v_exp_f32_e32 v119, v119
	v_mul_f32_e32 v112, 0xbfb8aa3b, v112
	v_exp_f32_e32 v112, v112
	v_mul_f32_e32 v113, 0xbfb8aa3b, v113
	v_exp_f32_e32 v113, v113
	v_add_f32_e32 v117, 1.0, v117
	v_rcp_f32_e32 v117, v117
	v_add_f32_e32 v119, 1.0, v119
	v_rcp_f32_e32 v119, v119
	v_add_f32_e32 v112, 1.0, v112
	v_rcp_f32_e32 v112, v112
	v_add_f32_e32 v113, 1.0, v113
	v_lshlrev_b32_e32 v118, 16, v137
	v_lshlrev_b32_e32 v121, 16, v141
	v_rcp_f32_e32 v113, v113
	v_fmac_f32_e32 v118, v117, v121
	v_and_b32_e32 v117, 0xffff0000, v137
	v_and_b32_e32 v121, 0xffff0000, v141
	v_pk_mul_f32 v[152:153], v[178:179], v[58:59] op_sel_hi:[0,1]
	v_fmac_f32_e32 v117, v119, v121
	v_lshlrev_b32_e32 v119, 16, v138
	v_lshlrev_b32_e32 v121, 16, v142
	v_pk_mul_f32 v[114:115], v[152:153], v[114:115]
	v_fmac_f32_e32 v119, v112, v121
	v_and_b32_e32 v121, 0xffff0000, v138
	v_and_b32_e32 v112, 0xffff0000, v142
	v_fmac_f32_e32 v121, v113, v112
	v_mul_f32_e32 v112, 0xbfb8aa3b, v114
	v_exp_f32_e32 v112, v112
	v_mul_f32_e32 v113, 0xbfb8aa3b, v115
	v_exp_f32_e32 v113, v113
	v_lshlrev_b32_e32 v122, 16, v139
	v_add_f32_e32 v112, 1.0, v112
	v_rcp_f32_e32 v112, v112
	v_add_f32_e32 v113, 1.0, v113
	v_rcp_f32_e32 v113, v113
	v_lshlrev_b32_e32 v114, 16, v143
	v_fmac_f32_e32 v122, v112, v114
	v_and_b32_e32 v115, 0xffff0000, v139
	v_and_b32_e32 v112, 0xffff0000, v143
	v_pk_mul_f32 v[138:139], v[176:177], v[76:77] op_sel_hi:[0,1]
	v_fmac_f32_e32 v115, v113, v112
	v_cvt_pk_bf16_f32 v112, v120, v116
	v_pk_mul_f32 v[108:109], v[138:139], v[108:109]
	v_cvt_pk_bf16_f32 v113, v118, v117
	v_cvt_pk_bf16_f32 v114, v119, v121
	v_cvt_pk_bf16_f32 v115, v122, v115
	global_store_dwordx4 v[124:125], v[112:115], off offset:256
	v_mul_f32_e32 v108, 0xbfb8aa3b, v108
	v_exp_f32_e32 v108, v108
	v_or_b32_e32 v112, 48, v166
	v_ashrrev_i32_e32 v113, 31, v112
	v_mul_f32_e32 v109, 0xbfb8aa3b, v109
	v_lshlrev_b64 v[136:137], 13, v[112:113]
	v_exp_f32_e32 v109, v109
	v_lshl_add_u64 v[112:113], s[8:9], 0, v[136:137]
	v_lshl_add_u64 v[114:115], s[10:11], 0, v[136:137]
	v_lshl_add_u64 v[112:113], v[112:113], 0, v[160:161]
	v_lshl_add_u64 v[116:117], v[114:115], 0, v[160:161]
	global_load_dwordx4 v[120:123], v[112:113], off nt
	s_nop 0
	global_load_dwordx4 v[112:115], v[112:113], off offset:256 nt
	s_nop 0
	global_load_dwordx4 v[124:127], v[116:117], off nt
	s_nop 0
	global_load_dwordx4 v[116:119], v[116:117], off offset:256 nt
	v_add_f32_e32 v108, 1.0, v108
	v_rcp_f32_e32 v108, v108
	v_add_f32_e32 v109, 1.0, v109
	v_rcp_f32_e32 v109, v109
	v_pk_mul_f32 v[140:141], v[176:177], v[78:79] op_sel_hi:[0,1]
	s_waitcnt vmcnt(9)
	v_lshlrev_b32_e32 v138, 16, v144
	s_waitcnt vmcnt(7)
	v_lshlrev_b32_e32 v139, 16, v148
	v_pk_mul_f32 v[110:111], v[140:141], v[110:111]
	v_fmac_f32_e32 v138, v108, v139
	v_and_b32_e32 v108, 0xffff0000, v144
	v_and_b32_e32 v139, 0xffff0000, v148
	v_pk_mul_f32 v[142:143], v[176:177], v[72:73] op_sel_hi:[0,1]
	v_fmac_f32_e32 v108, v109, v139
	v_mul_f32_e32 v109, 0xbfb8aa3b, v110
	v_pk_mul_f32 v[104:105], v[142:143], v[104:105]
	v_exp_f32_e32 v109, v109
	v_mul_f32_e32 v111, 0xbfb8aa3b, v111
	v_exp_f32_e32 v111, v111
	v_mul_f32_e32 v104, 0xbfb8aa3b, v104
	v_exp_f32_e32 v104, v104
	v_mul_f32_e32 v105, 0xbfb8aa3b, v105
	v_exp_f32_e32 v105, v105
	v_add_f32_e32 v109, 1.0, v109
	v_rcp_f32_e32 v109, v109
	v_add_f32_e32 v111, 1.0, v111
	v_rcp_f32_e32 v111, v111
	v_add_f32_e32 v104, 1.0, v104
	v_rcp_f32_e32 v104, v104
	v_add_f32_e32 v105, 1.0, v105
	v_lshlrev_b32_e32 v110, 16, v145
	v_lshlrev_b32_e32 v139, 16, v149
	v_rcp_f32_e32 v105, v105
	v_fmac_f32_e32 v110, v109, v139
	v_and_b32_e32 v109, 0xffff0000, v145
	v_and_b32_e32 v139, 0xffff0000, v149
	v_pk_mul_f32 v[152:153], v[176:177], v[74:75] op_sel_hi:[0,1]
	v_fmac_f32_e32 v109, v111, v139
	v_lshlrev_b32_e32 v111, 16, v146
	v_lshlrev_b32_e32 v139, 16, v150
	v_pk_mul_f32 v[106:107], v[152:153], v[106:107]
	v_fmac_f32_e32 v111, v104, v139
	v_and_b32_e32 v139, 0xffff0000, v146
	v_and_b32_e32 v104, 0xffff0000, v150
	v_fmac_f32_e32 v139, v105, v104
	v_mul_f32_e32 v104, 0xbfb8aa3b, v106
	v_exp_f32_e32 v104, v104
	v_mul_f32_e32 v105, 0xbfb8aa3b, v107
	v_exp_f32_e32 v105, v105
	v_lshlrev_b32_e32 v140, 16, v147
	v_add_f32_e32 v104, 1.0, v104
	v_rcp_f32_e32 v104, v104
	v_add_f32_e32 v105, 1.0, v105
	v_rcp_f32_e32 v105, v105
	v_lshlrev_b32_e32 v106, 16, v151
	v_fmac_f32_e32 v140, v104, v106
	v_and_b32_e32 v107, 0xffff0000, v147
	v_and_b32_e32 v104, 0xffff0000, v151
	v_fmac_f32_e32 v107, v105, v104
	v_cvt_pk_bf16_f32 v104, v138, v108
	v_cvt_pk_bf16_f32 v105, v110, v109
	v_lshl_add_u64 v[108:109], s[30:31], 0, v[180:181]
	v_lshl_add_u64 v[108:109], v[108:109], 0, v[160:161]
	v_cvt_pk_bf16_f32 v106, v111, v139
	v_cvt_pk_bf16_f32 v107, v140, v107
	global_store_dwordx4 v[108:109], v[104:107], off
	v_pk_mul_f32 v[110:111], v[176:177], v[56:57] op_sel_hi:[0,1]
	v_pk_mul_f32 v[96:97], v[110:111], v[96:97]
	v_pk_mul_f32 v[104:105], v[176:177], v[60:61] op_sel_hi:[0,1]
	v_pk_mul_f32 v[100:101], v[104:105], v[100:101]
	v_pk_mul_f32 v[106:107], v[176:177], v[62:63] op_sel_hi:[0,1]
	v_mul_f32_e32 v100, 0xbfb8aa3b, v100
	v_exp_f32_e32 v100, v100
	v_mul_f32_e32 v101, 0xbfb8aa3b, v101
	v_exp_f32_e32 v101, v101
	v_lshlrev_b32_e32 v104, 16, v128
	v_add_f32_e32 v100, 1.0, v100
	v_rcp_f32_e32 v100, v100
	v_add_f32_e32 v101, 1.0, v101
	v_rcp_f32_e32 v101, v101
	s_waitcnt vmcnt(7)
;     __device__ __forceinline__ void operator()(const f32x4 (&acc)[2][2][4][2], const Unit& u, int wr, int wc, int fr, int fq) const {
;     ...
;         EPB_LOAD(0);
; #pragma unroll
;         for (int kb = 0; kb < 8; ++kb) { const int ai = kb >> 2, m = kb & 3;
;             if (kb < 7) EPB_LOAD(kb + 1);
;             { const int row = row0 + ai * HALF + m * 16; float rmx = 0.f;
; #pragma unroll
;                 for (int bj = 0; bj < 2; ++bj) { const int col = col0 + bj * HALF; f32x4 v0 = acc[ai][bj][m][0], v1 = acc[ai][bj][m][1];
;                     if (QI8) { const f32x4 c0 = cb[bj][0] * ra[ai][m], c1 = cb[bj][1] * ra[ai][m]; const i32x4 i0 = __builtin_bit_cast(i32x4, v0), i1 = __builtin_bit_cast(i32x4, v1);
;                         v0 = (f32x4){(float)i0[0], (float)i0[1], (float)i0[2], (float)i0[3]} * c0; v1 = (f32x4){(float)i1[0], (float)i1[1], (float)i1[2], (float)i1[3]} * c1; }
;                     else if (MODE == 0) { v0 = v0 * tsc; v1 = v1 * tsc; }
;                     if (!QI8 && MODE == 1) { v0 = v0 * cb[bj][0]; v1 = v1 * cb[bj][1]; }
;                     if (MODE == 2 || MODE == 3) { const u32x4 g = gq[kb & 1][bj];
;                         f32x4 g0 = {sigmoidf_(bflo(g.x)), sigmoidf_(bfhi(g.x)), sigmoidf_(bflo(g.y)), sigmoidf_(bfhi(g.y))};
;                         f32x4 g1 = {sigmoidf_(bflo(g.z)), sigmoidf_(bfhi(g.z)), sigmoidf_(bflo(g.w)), sigmoidf_(bfhi(g.w))};
;                         v0 = v0 * g0; v1 = v1 * g1;
;                         if (MODE == 3) { const u32x4 q = aq[kb & 1][bj];
;                             v0 = v0 + (f32x4){bflo(q.x), bfhi(q.x), bflo(q.y), bfhi(q.y)}; v1 = v1 + (f32x4){bflo(q.z), bfhi(q.z), bflo(q.w), bfhi(q.w)}; } }
;                     if (MODE == 4) { v0 = v0 + rs[kb & 1][bj][0]; v1 = v1 + rs[kb & 1][bj][1]; }
;                     if (MODE == 5) { const u32x4 c = gq[kb & 1][bj], q = aq[kb & 1][bj];
;                         v0 = (f32x4){bflo(c.x) + sigmoidf_(v0[0]) * bflo(q.x), bfhi(c.x) + sigmoidf_(v0[1]) * bfhi(q.x), bflo(c.y) + sigmoidf_(v0[2]) * bflo(q.y), bfhi(c.y) + sigmoidf_(v0[3]) * bfhi(q.y)};
;                         v1 = (f32x4){bflo(c.z) + sigmoidf_(v1[0]) * bflo(q.z), bfhi(c.z) + sigmoidf_(v1[1]) * bfhi(q.z), bflo(c.w) + sigmoidf_(v1[2]) * bflo(q.w), bfhi(c.w) + sigmoidf_(v1[3]) * bfhi(q.w)}; }
	v_lshlrev_b32_e32 v105, 16, v132
	v_pk_mul_f32 v[102:103], v[106:107], v[102:103]
	v_fmac_f32_e32 v104, v100, v105
	v_and_b32_e32 v100, 0xffff0000, v128
	v_and_b32_e32 v105, 0xffff0000, v132
	v_fmac_f32_e32 v100, v101, v105
	v_mul_f32_e32 v101, 0xbfb8aa3b, v102
	v_exp_f32_e32 v101, v101
	v_mul_f32_e32 v103, 0xbfb8aa3b, v103
	v_exp_f32_e32 v103, v103
	v_mul_f32_e32 v96, 0xbfb8aa3b, v96
	v_exp_f32_e32 v96, v96
	v_mul_f32_e32 v97, 0xbfb8aa3b, v97
	v_exp_f32_e32 v97, v97
	v_add_f32_e32 v101, 1.0, v101
	v_rcp_f32_e32 v101, v101
	v_add_f32_e32 v103, 1.0, v103
	v_rcp_f32_e32 v103, v103
	v_add_f32_e32 v96, 1.0, v96
	v_rcp_f32_e32 v96, v96
	v_add_f32_e32 v97, 1.0, v97
	v_lshlrev_b32_e32 v102, 16, v129
	v_lshlrev_b32_e32 v105, 16, v133
	v_rcp_f32_e32 v97, v97
	v_fmac_f32_e32 v102, v101, v105
	v_and_b32_e32 v101, 0xffff0000, v129
	v_and_b32_e32 v105, 0xffff0000, v133
	v_pk_mul_f32 v[138:139], v[176:177], v[58:59] op_sel_hi:[0,1]
	v_fmac_f32_e32 v101, v103, v105
	v_lshlrev_b32_e32 v103, 16, v130
	v_lshlrev_b32_e32 v105, 16, v134
	v_pk_mul_f32 v[98:99], v[138:139], v[98:99]
	v_fmac_f32_e32 v103, v96, v105
	v_and_b32_e32 v105, 0xffff0000, v130
	v_and_b32_e32 v96, 0xffff0000, v134
	v_fmac_f32_e32 v105, v97, v96
	v_mul_f32_e32 v96, 0xbfb8aa3b, v98
	v_exp_f32_e32 v96, v96
	v_mul_f32_e32 v97, 0xbfb8aa3b, v99
	v_exp_f32_e32 v97, v97
	v_lshlrev_b32_e32 v106, 16, v131
	v_add_f32_e32 v96, 1.0, v96
	v_rcp_f32_e32 v96, v96
	v_add_f32_e32 v97, 1.0, v97
	v_rcp_f32_e32 v97, v97
	v_lshlrev_b32_e32 v98, 16, v135
	v_fmac_f32_e32 v106, v96, v98
	v_and_b32_e32 v99, 0xffff0000, v131
	v_and_b32_e32 v96, 0xffff0000, v135
	v_pk_mul_f32 v[128:129], v[174:175], v[76:77] op_sel_hi:[0,1]
	v_fmac_f32_e32 v99, v97, v96
	v_pk_mul_f32 v[92:93], v[128:129], v[92:93]
	v_cvt_pk_bf16_f32 v96, v104, v100
	v_cvt_pk_bf16_f32 v97, v102, v101
	v_cvt_pk_bf16_f32 v98, v103, v105
	v_cvt_pk_bf16_f32 v99, v106, v99
	global_store_dwordx4 v[108:109], v[96:99], off offset:256
	v_mul_f32_e32 v92, 0xbfb8aa3b, v92
	v_exp_f32_e32 v92, v92
	v_lshl_add_u64 v[96:97], s[8:9], 0, v[172:173]
	v_lshl_add_u64 v[98:99], s[10:11], 0, v[172:173]
	v_mul_f32_e32 v93, 0xbfb8aa3b, v93
	v_lshl_add_u64 v[96:97], v[96:97], 0, v[160:161]
	v_lshl_add_u64 v[100:101], v[98:99], 0, v[160:161]
	v_exp_f32_e32 v93, v93
	global_load_dwordx4 v[104:107], v[96:97], off nt
	s_nop 0
	global_load_dwordx4 v[96:99], v[96:97], off offset:256 nt
	s_nop 0
	global_load_dwordx4 v[108:111], v[100:101], off nt
	s_nop 0
	global_load_dwordx4 v[100:103], v[100:101], off offset:256 nt
	v_add_f32_e32 v92, 1.0, v92
	v_rcp_f32_e32 v92, v92
	v_add_f32_e32 v93, 1.0, v93
	v_rcp_f32_e32 v93, v93
	v_pk_mul_f32 v[130:131], v[174:175], v[78:79] op_sel_hi:[0,1]
	s_waitcnt vmcnt(9)
	v_lshlrev_b32_e32 v128, 16, v120
	s_waitcnt vmcnt(7)
	v_lshlrev_b32_e32 v129, 16, v124
	v_pk_mul_f32 v[94:95], v[130:131], v[94:95]
	v_fmac_f32_e32 v128, v92, v129
	v_and_b32_e32 v92, 0xffff0000, v120
	v_and_b32_e32 v120, 0xffff0000, v124
	v_pk_mul_f32 v[132:133], v[174:175], v[72:73] op_sel_hi:[0,1]
	v_fmac_f32_e32 v92, v93, v120
	v_mul_f32_e32 v93, 0xbfb8aa3b, v94
	v_pk_mul_f32 v[88:89], v[132:133], v[88:89]
	v_exp_f32_e32 v93, v93
	v_mul_f32_e32 v95, 0xbfb8aa3b, v95
	v_exp_f32_e32 v95, v95
	v_mul_f32_e32 v88, 0xbfb8aa3b, v88
	v_exp_f32_e32 v88, v88
	v_mul_f32_e32 v89, 0xbfb8aa3b, v89
	v_exp_f32_e32 v89, v89
	v_add_f32_e32 v93, 1.0, v93
	v_rcp_f32_e32 v93, v93
	v_add_f32_e32 v95, 1.0, v95
	v_rcp_f32_e32 v95, v95
	v_add_f32_e32 v88, 1.0, v88
	v_rcp_f32_e32 v88, v88
	v_add_f32_e32 v89, 1.0, v89
	v_lshlrev_b32_e32 v94, 16, v121
	v_lshlrev_b32_e32 v120, 16, v125
	v_rcp_f32_e32 v89, v89
	v_fmac_f32_e32 v94, v93, v120
	v_and_b32_e32 v93, 0xffff0000, v121
	v_and_b32_e32 v120, 0xffff0000, v125
	v_pk_mul_f32 v[134:135], v[174:175], v[74:75] op_sel_hi:[0,1]
	v_fmac_f32_e32 v93, v95, v120
	v_lshlrev_b32_e32 v95, 16, v122
	v_lshlrev_b32_e32 v120, 16, v126
	v_pk_mul_f32 v[90:91], v[134:135], v[90:91]
	v_fmac_f32_e32 v95, v88, v120
	v_and_b32_e32 v120, 0xffff0000, v122
	v_and_b32_e32 v88, 0xffff0000, v126
	v_fmac_f32_e32 v120, v89, v88
	v_mul_f32_e32 v88, 0xbfb8aa3b, v90
	v_exp_f32_e32 v88, v88
	v_mul_f32_e32 v89, 0xbfb8aa3b, v91
	v_exp_f32_e32 v89, v89
	v_lshlrev_b32_e32 v121, 16, v123
	v_add_f32_e32 v88, 1.0, v88
	v_rcp_f32_e32 v88, v88
	v_add_f32_e32 v89, 1.0, v89
	v_rcp_f32_e32 v89, v89
	v_lshlrev_b32_e32 v90, 16, v127
	v_fmac_f32_e32 v121, v88, v90
	v_and_b32_e32 v91, 0xffff0000, v123
	v_and_b32_e32 v88, 0xffff0000, v127
	v_cvt_f32_i32_e32 v84, v84
	v_fmac_f32_e32 v91, v89, v88
	v_cvt_pk_bf16_f32 v88, v128, v92
	v_cvt_pk_bf16_f32 v89, v94, v93
	v_lshl_add_u64 v[92:93], s[30:31], 0, v[136:137]
	v_lshl_add_u64 v[92:93], v[92:93], 0, v[160:161]
	v_cvt_pk_bf16_f32 v90, v95, v120
	v_cvt_pk_bf16_f32 v91, v121, v91
	global_store_dwordx4 v[92:93], v[88:91], off
	v_cvt_f32_i32_e32 v87, v87
	v_cvt_f32_i32_e32 v86, v86
	v_pk_mul_f32 v[88:89], v[174:175], v[60:61] op_sel_hi:[0,1]
	v_pk_mul_f32 v[84:85], v[88:89], v[84:85]
	v_cvt_f32_i32_e32 v81, v81
	v_mul_f32_e32 v84, 0xbfb8aa3b, v84
	v_exp_f32_e32 v84, v84
	v_mul_f32_e32 v85, 0xbfb8aa3b, v85
	v_exp_f32_e32 v85, v85
	v_cvt_f32_i32_e32 v80, v80
	v_add_f32_e32 v84, 1.0, v84
	v_rcp_f32_e32 v84, v84
	v_add_f32_e32 v85, 1.0, v85
	v_rcp_f32_e32 v85, v85
	v_pk_mul_f32 v[90:91], v[174:175], v[62:63] op_sel_hi:[0,1]
	v_lshlrev_b32_e32 v88, 16, v112
	s_waitcnt vmcnt(7)
;     __device__ __forceinline__ void operator()(const f32x4 (&acc)[2][2][4][2], const Unit& u, int wr, int wc, int fr, int fq) const {
;     ...
;         EPB_LOAD(0);
; #pragma unroll
;         for (int kb = 0; kb < 8; ++kb) { const int ai = kb >> 2, m = kb & 3;
;             if (kb < 7) EPB_LOAD(kb + 1);
;             { const int row = row0 + ai * HALF + m * 16; float rmx = 0.f;
; #pragma unroll
;                 for (int bj = 0; bj < 2; ++bj) { const int col = col0 + bj * HALF; f32x4 v0 = acc[ai][bj][m][0], v1 = acc[ai][bj][m][1];
;                     if (QI8) { const f32x4 c0 = cb[bj][0] * ra[ai][m], c1 = cb[bj][1] * ra[ai][m]; const i32x4 i0 = __builtin_bit_cast(i32x4, v0), i1 = __builtin_bit_cast(i32x4, v1);
;                         v0 = (f32x4){(float)i0[0], (float)i0[1], (float)i0[2], (float)i0[3]} * c0; v1 = (f32x4){(float)i1[0], (float)i1[1], (float)i1[2], (float)i1[3]} * c1; }
;                     else if (MODE == 0) { v0 = v0 * tsc; v1 = v1 * tsc; }
;                     if (!QI8 && MODE == 1) { v0 = v0 * cb[bj][0]; v1 = v1 * cb[bj][1]; }
;                     if (MODE == 2 || MODE == 3) { const u32x4 g = gq[kb & 1][bj];
;                         f32x4 g0 = {sigmoidf_(bflo(g.x)), sigmoidf_(bfhi(g.x)), sigmoidf_(bflo(g.y)), sigmoidf_(bfhi(g.y))};
;                         f32x4 g1 = {sigmoidf_(bflo(g.z)), sigmoidf_(bfhi(g.z)), sigmoidf_(bflo(g.w)), sigmoidf_(bfhi(g.w))};
;                         v0 = v0 * g0; v1 = v1 * g1;
;                         if (MODE == 3) { const u32x4 q = aq[kb & 1][bj];
;                             v0 = v0 + (f32x4){bflo(q.x), bfhi(q.x), bflo(q.y), bfhi(q.y)}; v1 = v1 + (f32x4){bflo(q.z), bfhi(q.z), bflo(q.w), bfhi(q.w)}; } }
;                     if (MODE == 4) { v0 = v0 + rs[kb & 1][bj][0]; v1 = v1 + rs[kb & 1][bj][1]; }
;                     if (MODE == 5) { const u32x4 c = gq[kb & 1][bj], q = aq[kb & 1][bj];
;                         v0 = (f32x4){bflo(c.x) + sigmoidf_(v0[0]) * bflo(q.x), bfhi(c.x) + sigmoidf_(v0[1]) * bfhi(q.x), bflo(c.y) + sigmoidf_(v0[2]) * bflo(q.y), bfhi(c.y) + sigmoidf_(v0[3]) * bfhi(q.y)};
;                         v1 = (f32x4){bflo(c.z) + sigmoidf_(v1[0]) * bflo(q.z), bfhi(c.z) + sigmoidf_(v1[1]) * bfhi(q.z), bflo(c.w) + sigmoidf_(v1[2]) * bflo(q.w), bfhi(c.w) + sigmoidf_(v1[3]) * bfhi(q.w)}; }
	v_lshlrev_b32_e32 v89, 16, v116
	v_pk_mul_f32 v[86:87], v[90:91], v[86:87]
	v_fmac_f32_e32 v88, v84, v89
	v_and_b32_e32 v84, 0xffff0000, v112
	v_and_b32_e32 v89, 0xffff0000, v116
	v_pk_mul_f32 v[94:95], v[174:175], v[56:57] op_sel_hi:[0,1]
	v_fmac_f32_e32 v84, v85, v89
	v_mul_f32_e32 v85, 0xbfb8aa3b, v86
	v_pk_mul_f32 v[80:81], v[94:95], v[80:81]
	v_exp_f32_e32 v85, v85
	v_mul_f32_e32 v87, 0xbfb8aa3b, v87
	v_exp_f32_e32 v87, v87
	v_mul_f32_e32 v80, 0xbfb8aa3b, v80
	v_exp_f32_e32 v80, v80
	v_mul_f32_e32 v81, 0xbfb8aa3b, v81
	v_exp_f32_e32 v81, v81
	v_add_f32_e32 v85, 1.0, v85
	v_rcp_f32_e32 v85, v85
	v_add_f32_e32 v87, 1.0, v87
	v_rcp_f32_e32 v87, v87
	v_add_f32_e32 v80, 1.0, v80
	v_cvt_f32_i32_e32 v83, v83
	v_cvt_f32_i32_e32 v82, v82
	v_rcp_f32_e32 v80, v80
	v_add_f32_e32 v81, 1.0, v81
	v_lshlrev_b32_e32 v86, 16, v113
	v_lshlrev_b32_e32 v89, 16, v117
	v_rcp_f32_e32 v81, v81
	v_fmac_f32_e32 v86, v85, v89
	v_and_b32_e32 v85, 0xffff0000, v113
	v_and_b32_e32 v89, 0xffff0000, v117
	v_pk_mul_f32 v[120:121], v[174:175], v[58:59] op_sel_hi:[0,1]
	v_fmac_f32_e32 v85, v87, v89
	v_lshlrev_b32_e32 v87, 16, v114
	v_lshlrev_b32_e32 v89, 16, v118
	v_pk_mul_f32 v[82:83], v[120:121], v[82:83]
	v_fmac_f32_e32 v87, v80, v89
	v_and_b32_e32 v89, 0xffff0000, v114
	v_and_b32_e32 v80, 0xffff0000, v118
	v_fmac_f32_e32 v89, v81, v80
	v_mul_f32_e32 v80, 0xbfb8aa3b, v82
	v_exp_f32_e32 v80, v80
	v_mul_f32_e32 v81, 0xbfb8aa3b, v83
	v_exp_f32_e32 v81, v81
	v_cvt_f32_i32_e32 v69, v69
	v_add_f32_e32 v80, 1.0, v80
	v_cvt_f32_i32_e32 v68, v68
	v_rcp_f32_e32 v80, v80
	v_add_f32_e32 v81, 1.0, v81
	v_rcp_f32_e32 v81, v81
	v_lshlrev_b32_e32 v90, 16, v115
	v_and_b32_e32 v83, 0xffff0000, v115
	v_pk_mul_f32 v[114:115], v[170:171], v[76:77] op_sel_hi:[0,1]
	v_lshlrev_b32_e32 v82, 16, v119
	v_pk_mul_f32 v[68:69], v[114:115], v[68:69]
	v_fmac_f32_e32 v90, v80, v82
	v_and_b32_e32 v80, 0xffff0000, v119
	v_mul_f32_e32 v68, 0xbfb8aa3b, v68
	v_fmac_f32_e32 v83, v81, v80
	v_cvt_pk_bf16_f32 v80, v88, v84
	v_exp_f32_e32 v68, v68
	v_mul_f32_e32 v69, 0xbfb8aa3b, v69
	v_cvt_pk_bf16_f32 v81, v86, v85
	v_cvt_pk_bf16_f32 v82, v87, v89
	v_cvt_pk_bf16_f32 v83, v90, v83
	global_store_dwordx4 v[92:93], v[80:83], off offset:256
	v_exp_f32_e32 v69, v69
	v_add_f32_e32 v68, 1.0, v68
	v_add_u32_e32 v80, 0x90, v166
	v_ashrrev_i32_e32 v81, 31, v80
	v_lshlrev_b64 v[112:113], 13, v[80:81]
	v_lshl_add_u64 v[80:81], s[8:9], 0, v[112:113]
	v_lshl_add_u64 v[82:83], s[10:11], 0, v[112:113]
	v_lshl_add_u64 v[80:81], v[80:81], 0, v[160:161]
	v_lshl_add_u64 v[84:85], v[82:83], 0, v[160:161]
	v_cvt_f32_i32_e32 v71, v71
	v_cvt_f32_i32_e32 v70, v70
	v_rcp_f32_e32 v68, v68
	v_add_f32_e32 v69, 1.0, v69
	global_load_dwordx4 v[88:91], v[80:81], off nt
	s_nop 0
	global_load_dwordx4 v[80:83], v[80:81], off offset:256 nt
	s_nop 0
	global_load_dwordx4 v[92:95], v[84:85], off nt
	s_nop 0
	global_load_dwordx4 v[84:87], v[84:85], off offset:256 nt
	v_rcp_f32_e32 v69, v69
	v_cvt_f32_i32_e32 v65, v65
	v_cvt_f32_i32_e32 v64, v64
	v_pk_mul_f32 v[116:117], v[170:171], v[78:79] op_sel_hi:[0,1]
	s_waitcnt vmcnt(9)
	v_lshlrev_b32_e32 v114, 16, v104
	s_waitcnt vmcnt(7)
	v_lshlrev_b32_e32 v115, 16, v108
	v_pk_mul_f32 v[70:71], v[116:117], v[70:71]
	v_fmac_f32_e32 v114, v68, v115
	v_and_b32_e32 v68, 0xffff0000, v104
	v_and_b32_e32 v104, 0xffff0000, v108
	v_pk_mul_f32 v[118:119], v[170:171], v[72:73] op_sel_hi:[0,1]
	v_fmac_f32_e32 v68, v69, v104
	v_mul_f32_e32 v69, 0xbfb8aa3b, v70
	v_pk_mul_f32 v[64:65], v[118:119], v[64:65]
	v_exp_f32_e32 v69, v69
	v_mul_f32_e32 v71, 0xbfb8aa3b, v71
	v_exp_f32_e32 v71, v71
	v_mul_f32_e32 v64, 0xbfb8aa3b, v64
	v_exp_f32_e32 v64, v64
	v_mul_f32_e32 v65, 0xbfb8aa3b, v65
	v_exp_f32_e32 v65, v65
	v_add_f32_e32 v69, 1.0, v69
	v_rcp_f32_e32 v69, v69
	v_add_f32_e32 v71, 1.0, v71
	v_rcp_f32_e32 v71, v71
	v_add_f32_e32 v64, 1.0, v64
	v_cvt_f32_i32_e32 v67, v67
	v_cvt_f32_i32_e32 v66, v66
	v_rcp_f32_e32 v64, v64
	v_add_f32_e32 v65, 1.0, v65
	v_lshlrev_b32_e32 v70, 16, v105
	v_lshlrev_b32_e32 v104, 16, v109
	v_rcp_f32_e32 v65, v65
	v_fmac_f32_e32 v70, v69, v104
	v_and_b32_e32 v69, 0xffff0000, v105
	v_and_b32_e32 v104, 0xffff0000, v109
	v_pk_mul_f32 v[120:121], v[170:171], v[74:75] op_sel_hi:[0,1]
	v_fmac_f32_e32 v69, v71, v104
	v_lshlrev_b32_e32 v71, 16, v106
	v_lshlrev_b32_e32 v104, 16, v110
	v_pk_mul_f32 v[66:67], v[120:121], v[66:67]
	v_fmac_f32_e32 v71, v64, v104
	v_and_b32_e32 v104, 0xffff0000, v106
	v_and_b32_e32 v64, 0xffff0000, v110
	v_fmac_f32_e32 v104, v65, v64
	v_mul_f32_e32 v64, 0xbfb8aa3b, v66
	v_exp_f32_e32 v64, v64
	v_mul_f32_e32 v65, 0xbfb8aa3b, v67
	v_exp_f32_e32 v65, v65
	v_lshlrev_b32_e32 v105, 16, v107
	v_add_f32_e32 v64, 1.0, v64
	v_rcp_f32_e32 v64, v64
	v_add_f32_e32 v65, 1.0, v65
	v_rcp_f32_e32 v65, v65
	v_lshlrev_b32_e32 v66, 16, v111
	v_fmac_f32_e32 v105, v64, v66
	v_and_b32_e32 v67, 0xffff0000, v107
	v_and_b32_e32 v64, 0xffff0000, v111
	v_cvt_f32_i32_e32 v53, v53
	v_cvt_f32_i32_e32 v52, v52
	v_fmac_f32_e32 v67, v65, v64
	v_cvt_pk_bf16_f32 v64, v114, v68
	v_cvt_pk_bf16_f32 v65, v70, v69
	v_lshl_add_u64 v[68:69], s[30:31], 0, v[172:173]
	v_lshl_add_u64 v[68:69], v[68:69], 0, v[160:161]
	v_cvt_pk_bf16_f32 v66, v71, v104
	v_cvt_pk_bf16_f32 v67, v105, v67
	global_store_dwordx4 v[68:69], v[64:67], off
	v_cvt_f32_i32_e32 v55, v55
	v_cvt_f32_i32_e32 v54, v54
	v_pk_mul_f32 v[64:65], v[170:171], v[60:61] op_sel_hi:[0,1]
	v_pk_mul_f32 v[52:53], v[64:65], v[52:53]
	v_cvt_f32_i32_e32 v49, v49
	v_mul_f32_e32 v52, 0xbfb8aa3b, v52
	v_exp_f32_e32 v52, v52
	v_mul_f32_e32 v53, 0xbfb8aa3b, v53
	v_exp_f32_e32 v53, v53
	v_cvt_f32_i32_e32 v48, v48
	v_add_f32_e32 v52, 1.0, v52
	v_rcp_f32_e32 v52, v52
	v_add_f32_e32 v53, 1.0, v53
	v_rcp_f32_e32 v53, v53
	v_pk_mul_f32 v[66:67], v[170:171], v[62:63] op_sel_hi:[0,1]
	v_lshlrev_b32_e32 v64, 16, v96
	s_waitcnt vmcnt(7)
;     __device__ __forceinline__ void operator()(const f32x4 (&acc)[2][2][4][2], const Unit& u, int wr, int wc, int fr, int fq) const {
;     ...
;         EPB_LOAD(0);
; #pragma unroll
;         for (int kb = 0; kb < 8; ++kb) { const int ai = kb >> 2, m = kb & 3;
;             if (kb < 7) EPB_LOAD(kb + 1);
;             { const int row = row0 + ai * HALF + m * 16; float rmx = 0.f;
; #pragma unroll
;                 for (int bj = 0; bj < 2; ++bj) { const int col = col0 + bj * HALF; f32x4 v0 = acc[ai][bj][m][0], v1 = acc[ai][bj][m][1];
;                     if (QI8) { const f32x4 c0 = cb[bj][0] * ra[ai][m], c1 = cb[bj][1] * ra[ai][m]; const i32x4 i0 = __builtin_bit_cast(i32x4, v0), i1 = __builtin_bit_cast(i32x4, v1);
;                         v0 = (f32x4){(float)i0[0], (float)i0[1], (float)i0[2], (float)i0[3]} * c0; v1 = (f32x4){(float)i1[0], (float)i1[1], (float)i1[2], (float)i1[3]} * c1; }
;                     else if (MODE == 0) { v0 = v0 * tsc; v1 = v1 * tsc; }
;                     if (!QI8 && MODE == 1) { v0 = v0 * cb[bj][0]; v1 = v1 * cb[bj][1]; }
;                     if (MODE == 2 || MODE == 3) { const u32x4 g = gq[kb & 1][bj];
;                         f32x4 g0 = {sigmoidf_(bflo(g.x)), sigmoidf_(bfhi(g.x)), sigmoidf_(bflo(g.y)), sigmoidf_(bfhi(g.y))};
;                         f32x4 g1 = {sigmoidf_(bflo(g.z)), sigmoidf_(bfhi(g.z)), sigmoidf_(bflo(g.w)), sigmoidf_(bfhi(g.w))};
;                         v0 = v0 * g0; v1 = v1 * g1;
;                         if (MODE == 3) { const u32x4 q = aq[kb & 1][bj];
;                             v0 = v0 + (f32x4){bflo(q.x), bfhi(q.x), bflo(q.y), bfhi(q.y)}; v1 = v1 + (f32x4){bflo(q.z), bfhi(q.z), bflo(q.w), bfhi(q.w)}; } }
;                     if (MODE == 4) { v0 = v0 + rs[kb & 1][bj][0]; v1 = v1 + rs[kb & 1][bj][1]; }
;                     if (MODE == 5) { const u32x4 c = gq[kb & 1][bj], q = aq[kb & 1][bj];
;                         v0 = (f32x4){bflo(c.x) + sigmoidf_(v0[0]) * bflo(q.x), bfhi(c.x) + sigmoidf_(v0[1]) * bfhi(q.x), bflo(c.y) + sigmoidf_(v0[2]) * bflo(q.y), bfhi(c.y) + sigmoidf_(v0[3]) * bfhi(q.y)};
;                         v1 = (f32x4){bflo(c.z) + sigmoidf_(v1[0]) * bflo(q.z), bfhi(c.z) + sigmoidf_(v1[1]) * bfhi(q.z), bflo(c.w) + sigmoidf_(v1[2]) * bflo(q.w), bfhi(c.w) + sigmoidf_(v1[3]) * bfhi(q.w)}; }
	v_lshlrev_b32_e32 v65, 16, v100
	v_pk_mul_f32 v[54:55], v[66:67], v[54:55]
	v_fmac_f32_e32 v64, v52, v65
	v_and_b32_e32 v52, 0xffff0000, v96
	v_and_b32_e32 v65, 0xffff0000, v100
	v_pk_mul_f32 v[70:71], v[170:171], v[56:57] op_sel_hi:[0,1]
	v_fmac_f32_e32 v52, v53, v65
	v_mul_f32_e32 v53, 0xbfb8aa3b, v54
	v_pk_mul_f32 v[48:49], v[70:71], v[48:49]
	v_exp_f32_e32 v53, v53
	v_mul_f32_e32 v55, 0xbfb8aa3b, v55
	v_exp_f32_e32 v55, v55
	v_mul_f32_e32 v48, 0xbfb8aa3b, v48
	v_exp_f32_e32 v48, v48
	v_mul_f32_e32 v49, 0xbfb8aa3b, v49
	v_exp_f32_e32 v49, v49
	v_add_f32_e32 v53, 1.0, v53
	v_rcp_f32_e32 v53, v53
	v_add_f32_e32 v55, 1.0, v55
	v_rcp_f32_e32 v55, v55
	v_add_f32_e32 v48, 1.0, v48
	v_cvt_f32_i32_e32 v51, v51
	v_cvt_f32_i32_e32 v50, v50
	v_rcp_f32_e32 v48, v48
	v_add_f32_e32 v49, 1.0, v49
	v_lshlrev_b32_e32 v54, 16, v97
	v_lshlrev_b32_e32 v65, 16, v101
	v_rcp_f32_e32 v49, v49
	v_fmac_f32_e32 v54, v53, v65
	v_and_b32_e32 v53, 0xffff0000, v97
	v_and_b32_e32 v65, 0xffff0000, v101
	v_pk_mul_f32 v[104:105], v[170:171], v[58:59] op_sel_hi:[0,1]
	v_fmac_f32_e32 v53, v55, v65
	v_lshlrev_b32_e32 v55, 16, v98
	v_lshlrev_b32_e32 v65, 16, v102
	v_pk_mul_f32 v[50:51], v[104:105], v[50:51]
	v_fmac_f32_e32 v55, v48, v65
	v_and_b32_e32 v65, 0xffff0000, v98
	v_and_b32_e32 v48, 0xffff0000, v102
	v_fmac_f32_e32 v65, v49, v48
	v_mul_f32_e32 v48, 0xbfb8aa3b, v50
	v_exp_f32_e32 v48, v48
	v_mul_f32_e32 v49, 0xbfb8aa3b, v51
	v_exp_f32_e32 v49, v49
	v_lshlrev_b32_e32 v66, 16, v99
	v_add_f32_e32 v48, 1.0, v48
	v_rcp_f32_e32 v48, v48
	v_add_f32_e32 v49, 1.0, v49
	v_rcp_f32_e32 v49, v49
	v_lshlrev_b32_e32 v50, 16, v103
	v_cvt_f32_i32_e32 v45, v45
	v_cvt_f32_i32_e32 v44, v44
	v_fmac_f32_e32 v66, v48, v50
	v_and_b32_e32 v51, 0xffff0000, v99
	v_and_b32_e32 v48, 0xffff0000, v103
	v_fmac_f32_e32 v51, v49, v48
	v_cvt_pk_bf16_f32 v48, v64, v52
	v_cvt_pk_bf16_f32 v49, v54, v53
	v_cvt_pk_bf16_f32 v50, v55, v65
	v_cvt_pk_bf16_f32 v51, v66, v51
	global_store_dwordx4 v[68:69], v[48:51], off offset:256
	v_pk_mul_f32 v[98:99], v[168:169], v[76:77] op_sel_hi:[0,1]
	v_pk_mul_f32 v[44:45], v[98:99], v[44:45]
	v_add_u32_e32 v48, 0xa0, v166
	v_ashrrev_i32_e32 v49, 31, v48
	v_lshlrev_b64 v[96:97], 13, v[48:49]
	v_mul_f32_e32 v44, 0xbfb8aa3b, v44
	v_lshl_add_u64 v[48:49], s[8:9], 0, v[96:97]
	v_lshl_add_u64 v[50:51], s[10:11], 0, v[96:97]
	v_exp_f32_e32 v44, v44
	v_mul_f32_e32 v45, 0xbfb8aa3b, v45
	v_lshl_add_u64 v[48:49], v[48:49], 0, v[160:161]
	v_lshl_add_u64 v[52:53], v[50:51], 0, v[160:161]
	v_exp_f32_e32 v45, v45
	global_load_dwordx4 v[64:67], v[48:49], off nt
	s_nop 0
	global_load_dwordx4 v[48:51], v[48:49], off offset:256 nt
	s_nop 0
	global_load_dwordx4 v[68:71], v[52:53], off nt
	s_nop 0
	global_load_dwordx4 v[52:55], v[52:53], off offset:256 nt
	v_add_f32_e32 v44, 1.0, v44
	v_cvt_f32_i32_e32 v47, v47
	v_cvt_f32_i32_e32 v46, v46
	v_rcp_f32_e32 v44, v44
	v_add_f32_e32 v45, 1.0, v45
	v_rcp_f32_e32 v45, v45
	v_cvt_f32_i32_e32 v41, v41
	v_cvt_f32_i32_e32 v40, v40
	v_pk_mul_f32 v[100:101], v[168:169], v[78:79] op_sel_hi:[0,1]
	s_waitcnt vmcnt(9)
	v_lshlrev_b32_e32 v98, 16, v88
	s_waitcnt vmcnt(7)
	v_lshlrev_b32_e32 v99, 16, v92
	v_pk_mul_f32 v[46:47], v[100:101], v[46:47]
	v_fmac_f32_e32 v98, v44, v99
	v_and_b32_e32 v44, 0xffff0000, v88
	v_and_b32_e32 v88, 0xffff0000, v92
	v_pk_mul_f32 v[102:103], v[168:169], v[72:73] op_sel_hi:[0,1]
	v_fmac_f32_e32 v44, v45, v88
	v_mul_f32_e32 v45, 0xbfb8aa3b, v46
	v_pk_mul_f32 v[40:41], v[102:103], v[40:41]
	v_exp_f32_e32 v45, v45
	v_mul_f32_e32 v47, 0xbfb8aa3b, v47
	v_exp_f32_e32 v47, v47
	v_mul_f32_e32 v40, 0xbfb8aa3b, v40
	v_exp_f32_e32 v40, v40
	v_mul_f32_e32 v41, 0xbfb8aa3b, v41
	v_exp_f32_e32 v41, v41
	v_add_f32_e32 v45, 1.0, v45
	v_rcp_f32_e32 v45, v45
	v_add_f32_e32 v47, 1.0, v47
	v_rcp_f32_e32 v47, v47
	v_add_f32_e32 v40, 1.0, v40
	v_cvt_f32_i32_e32 v43, v43
	v_cvt_f32_i32_e32 v42, v42
	v_rcp_f32_e32 v40, v40
	v_add_f32_e32 v41, 1.0, v41
	v_lshlrev_b32_e32 v46, 16, v89
	v_lshlrev_b32_e32 v88, 16, v93
	v_rcp_f32_e32 v41, v41
	v_fmac_f32_e32 v46, v45, v88
	v_and_b32_e32 v45, 0xffff0000, v89
	v_and_b32_e32 v88, 0xffff0000, v93
	v_pk_mul_f32 v[104:105], v[168:169], v[74:75] op_sel_hi:[0,1]
	v_fmac_f32_e32 v45, v47, v88
	v_lshlrev_b32_e32 v47, 16, v90
	v_lshlrev_b32_e32 v88, 16, v94
	v_pk_mul_f32 v[42:43], v[104:105], v[42:43]
	v_fmac_f32_e32 v47, v40, v88
	v_and_b32_e32 v88, 0xffff0000, v90
	v_and_b32_e32 v40, 0xffff0000, v94
	v_fmac_f32_e32 v88, v41, v40
	v_mul_f32_e32 v40, 0xbfb8aa3b, v42
	v_exp_f32_e32 v40, v40
	v_mul_f32_e32 v41, 0xbfb8aa3b, v43
	v_exp_f32_e32 v41, v41
	v_lshlrev_b32_e32 v89, 16, v91
	v_add_f32_e32 v40, 1.0, v40
	v_rcp_f32_e32 v40, v40
	v_add_f32_e32 v41, 1.0, v41
	v_rcp_f32_e32 v41, v41
	v_lshlrev_b32_e32 v42, 16, v95
	v_fmac_f32_e32 v89, v40, v42
	v_and_b32_e32 v43, 0xffff0000, v91
	v_and_b32_e32 v40, 0xffff0000, v95
	v_cvt_f32_i32_e32 v37, v37
	v_cvt_f32_i32_e32 v36, v36
	v_fmac_f32_e32 v43, v41, v40
	v_cvt_pk_bf16_f32 v40, v98, v44
	v_cvt_pk_bf16_f32 v41, v46, v45
	v_lshl_add_u64 v[44:45], s[30:31], 0, v[112:113]
	v_lshl_add_u64 v[44:45], v[44:45], 0, v[160:161]
	v_cvt_pk_bf16_f32 v42, v47, v88
	v_cvt_pk_bf16_f32 v43, v89, v43
	global_store_dwordx4 v[44:45], v[40:43], off
	v_cvt_f32_i32_e32 v39, v39
	v_cvt_f32_i32_e32 v38, v38
	v_pk_mul_f32 v[40:41], v[168:169], v[60:61] op_sel_hi:[0,1]
	v_pk_mul_f32 v[36:37], v[40:41], v[36:37]
	v_cvt_f32_i32_e32 v33, v33
	v_mul_f32_e32 v36, 0xbfb8aa3b, v36
	v_exp_f32_e32 v36, v36
	v_mul_f32_e32 v37, 0xbfb8aa3b, v37
	v_exp_f32_e32 v37, v37
	v_cvt_f32_i32_e32 v32, v32
	v_add_f32_e32 v36, 1.0, v36
	v_rcp_f32_e32 v36, v36
	v_add_f32_e32 v37, 1.0, v37
	v_rcp_f32_e32 v37, v37
	v_pk_mul_f32 v[42:43], v[168:169], v[62:63] op_sel_hi:[0,1]
	v_lshlrev_b32_e32 v40, 16, v80
	s_waitcnt vmcnt(7)
;     __device__ __forceinline__ void operator()(const f32x4 (&acc)[2][2][4][2], const Unit& u, int wr, int wc, int fr, int fq) const {
;     ...
;         EPB_LOAD(0);
; #pragma unroll
;         for (int kb = 0; kb < 8; ++kb) { const int ai = kb >> 2, m = kb & 3;
;             if (kb < 7) EPB_LOAD(kb + 1);
;             { const int row = row0 + ai * HALF + m * 16; float rmx = 0.f;
; #pragma unroll
;                 for (int bj = 0; bj < 2; ++bj) { const int col = col0 + bj * HALF; f32x4 v0 = acc[ai][bj][m][0], v1 = acc[ai][bj][m][1];
;                     if (QI8) { const f32x4 c0 = cb[bj][0] * ra[ai][m], c1 = cb[bj][1] * ra[ai][m]; const i32x4 i0 = __builtin_bit_cast(i32x4, v0), i1 = __builtin_bit_cast(i32x4, v1);
;                         v0 = (f32x4){(float)i0[0], (float)i0[1], (float)i0[2], (float)i0[3]} * c0; v1 = (f32x4){(float)i1[0], (float)i1[1], (float)i1[2], (float)i1[3]} * c1; }
;                     else if (MODE == 0) { v0 = v0 * tsc; v1 = v1 * tsc; }
;                     if (!QI8 && MODE == 1) { v0 = v0 * cb[bj][0]; v1 = v1 * cb[bj][1]; }
;                     if (MODE == 2 || MODE == 3) { const u32x4 g = gq[kb & 1][bj];
;                         f32x4 g0 = {sigmoidf_(bflo(g.x)), sigmoidf_(bfhi(g.x)), sigmoidf_(bflo(g.y)), sigmoidf_(bfhi(g.y))};
;                         f32x4 g1 = {sigmoidf_(bflo(g.z)), sigmoidf_(bfhi(g.z)), sigmoidf_(bflo(g.w)), sigmoidf_(bfhi(g.w))};
;                         v0 = v0 * g0; v1 = v1 * g1;
;                         if (MODE == 3) { const u32x4 q = aq[kb & 1][bj];
;                             v0 = v0 + (f32x4){bflo(q.x), bfhi(q.x), bflo(q.y), bfhi(q.y)}; v1 = v1 + (f32x4){bflo(q.z), bfhi(q.z), bflo(q.w), bfhi(q.w)}; } }
;                     if (MODE == 4) { v0 = v0 + rs[kb & 1][bj][0]; v1 = v1 + rs[kb & 1][bj][1]; }
;                     if (MODE == 5) { const u32x4 c = gq[kb & 1][bj], q = aq[kb & 1][bj];
;                         v0 = (f32x4){bflo(c.x) + sigmoidf_(v0[0]) * bflo(q.x), bfhi(c.x) + sigmoidf_(v0[1]) * bfhi(q.x), bflo(c.y) + sigmoidf_(v0[2]) * bflo(q.y), bfhi(c.y) + sigmoidf_(v0[3]) * bfhi(q.y)};
;                         v1 = (f32x4){bflo(c.z) + sigmoidf_(v1[0]) * bflo(q.z), bfhi(c.z) + sigmoidf_(v1[1]) * bfhi(q.z), bflo(c.w) + sigmoidf_(v1[2]) * bflo(q.w), bfhi(c.w) + sigmoidf_(v1[3]) * bfhi(q.w)}; }
	v_lshlrev_b32_e32 v41, 16, v84
	v_pk_mul_f32 v[38:39], v[42:43], v[38:39]
	v_fmac_f32_e32 v40, v36, v41
	v_and_b32_e32 v36, 0xffff0000, v80
	v_and_b32_e32 v41, 0xffff0000, v84
	v_pk_mul_f32 v[46:47], v[168:169], v[56:57] op_sel_hi:[0,1]
	v_fmac_f32_e32 v36, v37, v41
	v_mul_f32_e32 v37, 0xbfb8aa3b, v38
	v_pk_mul_f32 v[32:33], v[46:47], v[32:33]
	v_exp_f32_e32 v37, v37
	v_mul_f32_e32 v39, 0xbfb8aa3b, v39
	v_exp_f32_e32 v39, v39
	v_mul_f32_e32 v32, 0xbfb8aa3b, v32
	v_exp_f32_e32 v32, v32
	v_mul_f32_e32 v33, 0xbfb8aa3b, v33
	v_exp_f32_e32 v33, v33
	v_add_f32_e32 v37, 1.0, v37
	v_rcp_f32_e32 v37, v37
	v_add_f32_e32 v39, 1.0, v39
	v_rcp_f32_e32 v39, v39
	v_add_f32_e32 v32, 1.0, v32
	v_cvt_f32_i32_e32 v35, v35
	v_cvt_f32_i32_e32 v34, v34
	v_rcp_f32_e32 v32, v32
	v_add_f32_e32 v33, 1.0, v33
	v_lshlrev_b32_e32 v38, 16, v81
	v_lshlrev_b32_e32 v41, 16, v85
	v_rcp_f32_e32 v33, v33
	v_fmac_f32_e32 v38, v37, v41
	v_and_b32_e32 v37, 0xffff0000, v81
	v_and_b32_e32 v41, 0xffff0000, v85
	v_pk_mul_f32 v[88:89], v[168:169], v[58:59] op_sel_hi:[0,1]
	v_fmac_f32_e32 v37, v39, v41
	v_lshlrev_b32_e32 v39, 16, v82
	v_lshlrev_b32_e32 v41, 16, v86
	v_pk_mul_f32 v[34:35], v[88:89], v[34:35]
	v_fmac_f32_e32 v39, v32, v41
	v_and_b32_e32 v41, 0xffff0000, v82
	v_and_b32_e32 v32, 0xffff0000, v86
	v_fmac_f32_e32 v41, v33, v32
	v_mul_f32_e32 v32, 0xbfb8aa3b, v34
	v_exp_f32_e32 v32, v32
	v_mul_f32_e32 v33, 0xbfb8aa3b, v35
	v_exp_f32_e32 v33, v33
	v_cvt_f32_i32_e32 v29, v29
	v_add_f32_e32 v32, 1.0, v32
	v_cvt_f32_i32_e32 v28, v28
	v_rcp_f32_e32 v32, v32
	v_add_f32_e32 v33, 1.0, v33
	v_rcp_f32_e32 v33, v33
	v_lshlrev_b32_e32 v42, 16, v83
	v_and_b32_e32 v35, 0xffff0000, v83
	v_pk_mul_f32 v[82:83], v[164:165], v[76:77] op_sel_hi:[0,1]
	v_lshlrev_b32_e32 v34, 16, v87
	v_pk_mul_f32 v[28:29], v[82:83], v[28:29]
	v_fmac_f32_e32 v42, v32, v34
	v_and_b32_e32 v32, 0xffff0000, v87
	v_mul_f32_e32 v28, 0xbfb8aa3b, v28
	v_fmac_f32_e32 v35, v33, v32
	v_cvt_pk_bf16_f32 v32, v40, v36
	v_exp_f32_e32 v28, v28
	v_mul_f32_e32 v29, 0xbfb8aa3b, v29
	v_cvt_pk_bf16_f32 v33, v38, v37
	v_cvt_pk_bf16_f32 v34, v39, v41
	v_cvt_pk_bf16_f32 v35, v42, v35
	global_store_dwordx4 v[44:45], v[32:35], off offset:256
	v_exp_f32_e32 v29, v29
	v_add_f32_e32 v28, 1.0, v28
	v_add_u32_e32 v32, 0xb0, v166
	v_ashrrev_i32_e32 v33, 31, v32
	v_lshlrev_b64 v[80:81], 13, v[32:33]
	v_lshl_add_u64 v[32:33], s[8:9], 0, v[80:81]
	v_lshl_add_u64 v[34:35], s[10:11], 0, v[80:81]
	v_lshl_add_u64 v[32:33], v[32:33], 0, v[160:161]
	v_lshl_add_u64 v[36:37], v[34:35], 0, v[160:161]
	v_cvt_f32_i32_e32 v31, v31
	v_cvt_f32_i32_e32 v30, v30
	v_rcp_f32_e32 v28, v28
	v_add_f32_e32 v29, 1.0, v29
	global_load_dwordx4 v[40:43], v[32:33], off nt
	s_nop 0
	global_load_dwordx4 v[32:35], v[32:33], off offset:256 nt
	s_nop 0
	global_load_dwordx4 v[44:47], v[36:37], off nt
	s_nop 0
	global_load_dwordx4 v[36:39], v[36:37], off offset:256 nt
	v_rcp_f32_e32 v29, v29
	v_cvt_f32_i32_e32 v25, v25
	v_cvt_f32_i32_e32 v24, v24
	v_pk_mul_f32 v[84:85], v[164:165], v[78:79] op_sel_hi:[0,1]
	s_waitcnt vmcnt(9)
	v_lshlrev_b32_e32 v82, 16, v64
	s_waitcnt vmcnt(7)
	v_lshlrev_b32_e32 v83, 16, v68
	v_pk_mul_f32 v[30:31], v[84:85], v[30:31]
	v_fmac_f32_e32 v82, v28, v83
	v_and_b32_e32 v28, 0xffff0000, v64
	v_and_b32_e32 v64, 0xffff0000, v68
	v_pk_mul_f32 v[86:87], v[164:165], v[72:73] op_sel_hi:[0,1]
	v_fmac_f32_e32 v28, v29, v64
	v_mul_f32_e32 v29, 0xbfb8aa3b, v30
	v_pk_mul_f32 v[24:25], v[86:87], v[24:25]
	v_exp_f32_e32 v29, v29
	v_mul_f32_e32 v31, 0xbfb8aa3b, v31
	v_exp_f32_e32 v31, v31
	v_mul_f32_e32 v24, 0xbfb8aa3b, v24
	v_exp_f32_e32 v24, v24
	v_mul_f32_e32 v25, 0xbfb8aa3b, v25
	v_exp_f32_e32 v25, v25
	v_add_f32_e32 v29, 1.0, v29
	v_rcp_f32_e32 v29, v29
	v_add_f32_e32 v31, 1.0, v31
	v_rcp_f32_e32 v31, v31
	v_add_f32_e32 v24, 1.0, v24
	v_cvt_f32_i32_e32 v27, v27
	v_cvt_f32_i32_e32 v26, v26
	v_rcp_f32_e32 v24, v24
	v_add_f32_e32 v25, 1.0, v25
	v_lshlrev_b32_e32 v30, 16, v65
	v_lshlrev_b32_e32 v64, 16, v69
	v_rcp_f32_e32 v25, v25
	v_fmac_f32_e32 v30, v29, v64
	v_and_b32_e32 v29, 0xffff0000, v65
	v_and_b32_e32 v64, 0xffff0000, v69
	v_pk_mul_f32 v[88:89], v[164:165], v[74:75] op_sel_hi:[0,1]
	v_fmac_f32_e32 v29, v31, v64
	v_lshlrev_b32_e32 v31, 16, v66
	v_lshlrev_b32_e32 v64, 16, v70
	v_pk_mul_f32 v[26:27], v[88:89], v[26:27]
	v_fmac_f32_e32 v31, v24, v64
	v_and_b32_e32 v64, 0xffff0000, v66
	v_and_b32_e32 v24, 0xffff0000, v70
	v_fmac_f32_e32 v64, v25, v24
	v_mul_f32_e32 v24, 0xbfb8aa3b, v26
	v_exp_f32_e32 v24, v24
	v_mul_f32_e32 v25, 0xbfb8aa3b, v27
	v_exp_f32_e32 v25, v25
	v_lshlrev_b32_e32 v65, 16, v67
	v_add_f32_e32 v24, 1.0, v24
	v_rcp_f32_e32 v24, v24
	v_add_f32_e32 v25, 1.0, v25
	v_rcp_f32_e32 v25, v25
	v_lshlrev_b32_e32 v26, 16, v71
	v_fmac_f32_e32 v65, v24, v26
	v_and_b32_e32 v27, 0xffff0000, v67
	v_and_b32_e32 v24, 0xffff0000, v71
	v_cvt_f32_i32_e32 v21, v21
	v_cvt_f32_i32_e32 v20, v20
	v_fmac_f32_e32 v27, v25, v24
	v_cvt_pk_bf16_f32 v24, v82, v28
	v_cvt_pk_bf16_f32 v25, v30, v29
	v_lshl_add_u64 v[28:29], s[30:31], 0, v[96:97]
	v_lshl_add_u64 v[28:29], v[28:29], 0, v[160:161]
	v_cvt_pk_bf16_f32 v26, v31, v64
	v_cvt_pk_bf16_f32 v27, v65, v27
	global_store_dwordx4 v[28:29], v[24:27], off
	v_cvt_f32_i32_e32 v23, v23
	v_cvt_f32_i32_e32 v22, v22
	v_pk_mul_f32 v[24:25], v[164:165], v[60:61] op_sel_hi:[0,1]
	v_pk_mul_f32 v[20:21], v[24:25], v[20:21]
	v_cvt_f32_i32_e32 v17, v17
	v_mul_f32_e32 v20, 0xbfb8aa3b, v20
	v_exp_f32_e32 v20, v20
	v_mul_f32_e32 v21, 0xbfb8aa3b, v21
	v_exp_f32_e32 v21, v21
	v_cvt_f32_i32_e32 v16, v16
	v_add_f32_e32 v20, 1.0, v20
	v_rcp_f32_e32 v20, v20
	v_add_f32_e32 v21, 1.0, v21
	v_rcp_f32_e32 v21, v21
	v_pk_mul_f32 v[26:27], v[164:165], v[62:63] op_sel_hi:[0,1]
	v_lshlrev_b32_e32 v24, 16, v48
	s_waitcnt vmcnt(7)
;     __device__ __forceinline__ void operator()(const f32x4 (&acc)[2][2][4][2], const Unit& u, int wr, int wc, int fr, int fq) const {
;     ...
;         for (int kb = 0; kb < 8; ++kb) { const int ai = kb >> 2, m = kb & 3;
;             if (kb < 7) EPB_LOAD(kb + 1);
;             { const int row = row0 + ai * HALF + m * 16; float rmx = 0.f;
; #pragma unroll
;                 for (int bj = 0; bj < 2; ++bj) { const int col = col0 + bj * HALF; f32x4 v0 = acc[ai][bj][m][0], v1 = acc[ai][bj][m][1];
;                     if (QI8) { const f32x4 c0 = cb[bj][0] * ra[ai][m], c1 = cb[bj][1] * ra[ai][m]; const i32x4 i0 = __builtin_bit_cast(i32x4, v0), i1 = __builtin_bit_cast(i32x4, v1);
;                         v0 = (f32x4){(float)i0[0], (float)i0[1], (float)i0[2], (float)i0[3]} * c0; v1 = (f32x4){(float)i1[0], (float)i1[1], (float)i1[2], (float)i1[3]} * c1; }
;                     else if (MODE == 0) { v0 = v0 * tsc; v1 = v1 * tsc; }
;                     if (!QI8 && MODE == 1) { v0 = v0 * cb[bj][0]; v1 = v1 * cb[bj][1]; }
;                     if (MODE == 2 || MODE == 3) { const u32x4 g = gq[kb & 1][bj];
;                         f32x4 g0 = {sigmoidf_(bflo(g.x)), sigmoidf_(bfhi(g.x)), sigmoidf_(bflo(g.y)), sigmoidf_(bfhi(g.y))};
;                         f32x4 g1 = {sigmoidf_(bflo(g.z)), sigmoidf_(bfhi(g.z)), sigmoidf_(bflo(g.w)), sigmoidf_(bfhi(g.w))};
;                         v0 = v0 * g0; v1 = v1 * g1;
;                         if (MODE == 3) { const u32x4 q = aq[kb & 1][bj];
;                             v0 = v0 + (f32x4){bflo(q.x), bfhi(q.x), bflo(q.y), bfhi(q.y)}; v1 = v1 + (f32x4){bflo(q.z), bfhi(q.z), bflo(q.w), bfhi(q.w)}; } }
;                     if (MODE == 4) { v0 = v0 + rs[kb & 1][bj][0]; v1 = v1 + rs[kb & 1][bj][1]; }
;                     if (MODE == 5) { const u32x4 c = gq[kb & 1][bj], q = aq[kb & 1][bj];
;                         v0 = (f32x4){bflo(c.x) + sigmoidf_(v0[0]) * bflo(q.x), bfhi(c.x) + sigmoidf_(v0[1]) * bfhi(q.x), bflo(c.y) + sigmoidf_(v0[2]) * bflo(q.y), bfhi(c.y) + sigmoidf_(v0[3]) * bfhi(q.y)};
;                         v1 = (f32x4){bflo(c.z) + sigmoidf_(v1[0]) * bflo(q.z), bfhi(c.z) + sigmoidf_(v1[1]) * bfhi(q.z), bflo(c.w) + sigmoidf_(v1[2]) * bflo(q.w), bfhi(c.w) + sigmoidf_(v1[3]) * bfhi(q.w)}; }
;                     u32x4 w; w.x = cvtpk(v0[0], v0[1]); w.y = cvtpk(v0[2], v0[3]); w.z = cvtpk(v1[0], v1[1]); w.w = cvtpk(v1[2], v1[3]);
	v_lshlrev_b32_e32 v25, 16, v52
	v_pk_mul_f32 v[22:23], v[26:27], v[22:23]
	v_fmac_f32_e32 v24, v20, v25
	v_and_b32_e32 v20, 0xffff0000, v48
	v_and_b32_e32 v25, 0xffff0000, v52
	v_pk_mul_f32 v[30:31], v[164:165], v[56:57] op_sel_hi:[0,1]
	v_fmac_f32_e32 v20, v21, v25
	v_mul_f32_e32 v21, 0xbfb8aa3b, v22
	v_pk_mul_f32 v[16:17], v[30:31], v[16:17]
	v_exp_f32_e32 v21, v21
	v_mul_f32_e32 v23, 0xbfb8aa3b, v23
	v_exp_f32_e32 v23, v23
	v_mul_f32_e32 v16, 0xbfb8aa3b, v16
	v_exp_f32_e32 v16, v16
	v_mul_f32_e32 v17, 0xbfb8aa3b, v17
	v_exp_f32_e32 v17, v17
	v_add_f32_e32 v21, 1.0, v21
	v_rcp_f32_e32 v21, v21
	v_add_f32_e32 v23, 1.0, v23
	v_rcp_f32_e32 v23, v23
	v_add_f32_e32 v16, 1.0, v16
	v_cvt_f32_i32_e32 v19, v19
	v_cvt_f32_i32_e32 v18, v18
	v_rcp_f32_e32 v16, v16
	v_add_f32_e32 v17, 1.0, v17
	v_lshlrev_b32_e32 v22, 16, v49
	v_lshlrev_b32_e32 v25, 16, v53
	v_rcp_f32_e32 v17, v17
	v_fmac_f32_e32 v22, v21, v25
	v_and_b32_e32 v21, 0xffff0000, v49
	v_and_b32_e32 v25, 0xffff0000, v53
	v_pk_mul_f32 v[64:65], v[164:165], v[58:59] op_sel_hi:[0,1]
	v_fmac_f32_e32 v21, v23, v25
	v_lshlrev_b32_e32 v23, 16, v50
	v_lshlrev_b32_e32 v25, 16, v54
	v_pk_mul_f32 v[18:19], v[64:65], v[18:19]
	v_fmac_f32_e32 v23, v16, v25
	v_and_b32_e32 v25, 0xffff0000, v50
	v_and_b32_e32 v16, 0xffff0000, v54
	v_fmac_f32_e32 v25, v17, v16
	v_mul_f32_e32 v16, 0xbfb8aa3b, v18
	v_exp_f32_e32 v16, v16
	v_mul_f32_e32 v17, 0xbfb8aa3b, v19
	v_exp_f32_e32 v17, v17
	v_lshlrev_b32_e32 v26, 16, v51
	v_add_f32_e32 v16, 1.0, v16
	v_rcp_f32_e32 v16, v16
	v_add_f32_e32 v17, 1.0, v17
	v_rcp_f32_e32 v17, v17
	v_lshlrev_b32_e32 v18, 16, v55
	v_cvt_f32_i32_e32 v13, v13
	v_cvt_f32_i32_e32 v12, v12
	v_fmac_f32_e32 v26, v16, v18
	v_and_b32_e32 v19, 0xffff0000, v51
	v_and_b32_e32 v16, 0xffff0000, v55
	v_fmac_f32_e32 v19, v17, v16
	v_cvt_pk_bf16_f32 v16, v24, v20
	v_cvt_pk_bf16_f32 v17, v22, v21
	v_cvt_pk_bf16_f32 v18, v23, v25
	v_cvt_pk_bf16_f32 v19, v26, v19
	global_store_dwordx4 v[28:29], v[16:19], off offset:256
	v_cvt_f32_i32_e32 v15, v15
	v_cvt_f32_i32_e32 v14, v14
	v_pk_mul_f32 v[16:17], v[76:77], v[162:163] op_sel_hi:[1,0]
	v_cvt_f32_i32_e32 v9, v9
	v_pk_mul_f32 v[12:13], v[16:17], v[12:13]
	v_cvt_f32_i32_e32 v8, v8
	v_mul_f32_e32 v12, 0xbfb8aa3b, v12
	v_exp_f32_e32 v12, v12
	v_mul_f32_e32 v13, 0xbfb8aa3b, v13
	v_exp_f32_e32 v13, v13
	v_pk_mul_f32 v[18:19], v[78:79], v[162:163] op_sel_hi:[1,0]
	v_add_f32_e32 v12, 1.0, v12
	v_rcp_f32_e32 v12, v12
	v_add_f32_e32 v13, 1.0, v13
	v_rcp_f32_e32 v13, v13
	s_waitcnt vmcnt(5)
	v_lshlrev_b32_e32 v16, 16, v40
	s_waitcnt vmcnt(3)
	v_lshlrev_b32_e32 v17, 16, v44
	v_pk_mul_f32 v[14:15], v[18:19], v[14:15]
	v_fmac_f32_e32 v16, v12, v17
	v_and_b32_e32 v12, 0xffff0000, v40
	v_and_b32_e32 v17, 0xffff0000, v44
	v_pk_mul_f32 v[20:21], v[162:163], v[72:73] op_sel_hi:[0,1]
	v_fmac_f32_e32 v12, v13, v17
	v_mul_f32_e32 v13, 0xbfb8aa3b, v14
	v_pk_mul_f32 v[8:9], v[20:21], v[8:9]
	v_exp_f32_e32 v13, v13
	v_mul_f32_e32 v15, 0xbfb8aa3b, v15
	v_exp_f32_e32 v15, v15
	v_mul_f32_e32 v8, 0xbfb8aa3b, v8
	v_exp_f32_e32 v8, v8
	v_mul_f32_e32 v9, 0xbfb8aa3b, v9
	v_exp_f32_e32 v9, v9
	v_add_f32_e32 v13, 1.0, v13
	v_rcp_f32_e32 v13, v13
	v_add_f32_e32 v15, 1.0, v15
	v_rcp_f32_e32 v15, v15
	v_add_f32_e32 v8, 1.0, v8
	v_cvt_f32_i32_e32 v11, v11
	v_cvt_f32_i32_e32 v10, v10
	v_rcp_f32_e32 v8, v8
	v_add_f32_e32 v9, 1.0, v9
	v_lshlrev_b32_e32 v14, 16, v41
	v_lshlrev_b32_e32 v17, 16, v45
	v_rcp_f32_e32 v9, v9
	v_fmac_f32_e32 v14, v13, v17
	v_and_b32_e32 v13, 0xffff0000, v41
	v_and_b32_e32 v17, 0xffff0000, v45
	v_pk_mul_f32 v[22:23], v[162:163], v[74:75] op_sel_hi:[0,1]
	v_fmac_f32_e32 v13, v15, v17
	v_lshlrev_b32_e32 v15, 16, v42
	v_lshlrev_b32_e32 v17, 16, v46
	v_pk_mul_f32 v[10:11], v[22:23], v[10:11]
	v_fmac_f32_e32 v15, v8, v17
	v_and_b32_e32 v17, 0xffff0000, v42
	v_and_b32_e32 v8, 0xffff0000, v46
	v_fmac_f32_e32 v17, v9, v8
	v_mul_f32_e32 v8, 0xbfb8aa3b, v10
	v_exp_f32_e32 v8, v8
	v_mul_f32_e32 v9, 0xbfb8aa3b, v11
	v_exp_f32_e32 v9, v9
	v_lshlrev_b32_e32 v18, 16, v43
	v_add_f32_e32 v8, 1.0, v8
	v_rcp_f32_e32 v8, v8
	v_add_f32_e32 v9, 1.0, v9
	v_rcp_f32_e32 v9, v9
	v_lshlrev_b32_e32 v10, 16, v47
	v_fmac_f32_e32 v18, v8, v10
	v_and_b32_e32 v11, 0xffff0000, v43
	v_and_b32_e32 v8, 0xffff0000, v47
	v_cvt_f32_i32_e32 v5, v5
	v_cvt_f32_i32_e32 v4, v4
	v_fmac_f32_e32 v11, v9, v8
	v_cvt_pk_bf16_f32 v8, v16, v12
	v_cvt_pk_bf16_f32 v9, v14, v13
	v_lshl_add_u64 v[12:13], s[30:31], 0, v[80:81]
	v_lshl_add_u64 v[12:13], v[12:13], 0, v[160:161]
	v_cvt_pk_bf16_f32 v10, v15, v17
	v_cvt_pk_bf16_f32 v11, v18, v11
	global_store_dwordx4 v[12:13], v[8:11], off
	v_cvt_f32_i32_e32 v7, v7
	v_cvt_f32_i32_e32 v6, v6
	v_pk_mul_f32 v[8:9], v[162:163], v[60:61] op_sel_hi:[0,1]
	v_pk_mul_f32 v[4:5], v[8:9], v[4:5]
	v_cvt_f32_i32_e32 v1, v1
	v_mul_f32_e32 v4, 0xbfb8aa3b, v4
	v_exp_f32_e32 v4, v4
	v_mul_f32_e32 v5, 0xbfb8aa3b, v5
	v_exp_f32_e32 v5, v5
	v_cvt_f32_i32_e32 v0, v0
	v_add_f32_e32 v4, 1.0, v4
	v_rcp_f32_e32 v4, v4
	v_add_f32_e32 v5, 1.0, v5
	v_rcp_f32_e32 v5, v5
	v_pk_mul_f32 v[10:11], v[162:163], v[62:63] op_sel_hi:[0,1]
	v_lshlrev_b32_e32 v8, 16, v32
	s_waitcnt vmcnt(3)
	v_lshlrev_b32_e32 v9, 16, v36
	v_pk_mul_f32 v[6:7], v[10:11], v[6:7]
	v_fmac_f32_e32 v8, v4, v9
	v_and_b32_e32 v4, 0xffff0000, v32
	v_and_b32_e32 v9, 0xffff0000, v36
	v_pk_mul_f32 v[14:15], v[162:163], v[56:57] op_sel_hi:[0,1]
	v_fmac_f32_e32 v4, v5, v9
	v_mul_f32_e32 v5, 0xbfb8aa3b, v6
	v_pk_mul_f32 v[0:1], v[14:15], v[0:1]
	v_exp_f32_e32 v5, v5
	v_mul_f32_e32 v7, 0xbfb8aa3b, v7
	v_exp_f32_e32 v7, v7
	v_mul_f32_e32 v0, 0xbfb8aa3b, v0
	v_exp_f32_e32 v0, v0
	v_mul_f32_e32 v1, 0xbfb8aa3b, v1
	v_exp_f32_e32 v1, v1
	v_add_f32_e32 v5, 1.0, v5
	v_rcp_f32_e32 v5, v5
	v_add_f32_e32 v7, 1.0, v7
	v_rcp_f32_e32 v7, v7
	v_add_f32_e32 v0, 1.0, v0
	v_cvt_f32_i32_e32 v3, v3
	v_cvt_f32_i32_e32 v2, v2
	v_rcp_f32_e32 v0, v0
	v_add_f32_e32 v1, 1.0, v1
	v_lshlrev_b32_e32 v6, 16, v33
	v_lshlrev_b32_e32 v9, 16, v37
	v_rcp_f32_e32 v1, v1
	v_fmac_f32_e32 v6, v5, v9
	v_and_b32_e32 v5, 0xffff0000, v33
	v_and_b32_e32 v9, 0xffff0000, v37
	v_pk_mul_f32 v[16:17], v[162:163], v[58:59] op_sel_hi:[0,1]
	v_fmac_f32_e32 v5, v7, v9
	v_lshlrev_b32_e32 v7, 16, v34
	v_lshlrev_b32_e32 v9, 16, v38
	v_pk_mul_f32 v[2:3], v[16:17], v[2:3]
	v_fmac_f32_e32 v7, v0, v9
	v_and_b32_e32 v9, 0xffff0000, v34
	v_and_b32_e32 v0, 0xffff0000, v38
	v_fmac_f32_e32 v9, v1, v0
	v_mul_f32_e32 v0, 0xbfb8aa3b, v2
	v_exp_f32_e32 v0, v0
	v_mul_f32_e32 v1, 0xbfb8aa3b, v3
	v_exp_f32_e32 v1, v1
	v_lshlrev_b32_e32 v10, 16, v35
	v_add_f32_e32 v0, 1.0, v0
	v_rcp_f32_e32 v0, v0
	v_add_f32_e32 v1, 1.0, v1
	v_rcp_f32_e32 v1, v1
	v_lshlrev_b32_e32 v2, 16, v39
	v_fmac_f32_e32 v10, v0, v2
	v_and_b32_e32 v3, 0xffff0000, v35
	v_and_b32_e32 v0, 0xffff0000, v39
	v_fmac_f32_e32 v3, v1, v0
	s_andn2_b64 vcc, exec, s[6:7]
	s_mov_b64 s[6:7], -1
	v_cvt_pk_bf16_f32 v0, v8, v4
	v_cvt_pk_bf16_f32 v1, v6, v5
	v_cvt_pk_bf16_f32 v2, v7, v9
	v_cvt_pk_bf16_f32 v3, v10, v3
	global_store_dwordx4 v[12:13], v[0:3], off offset:256
	s_cbranch_vccnz .LBB0_1722
; #define PG8_BAR __builtin_amdgcn_s_barrier()
; template <class Epi, class Sched, bool ALIGN_EPI = true, bool SP2 = true, class Side = NoSide>
; __device__ __forceinline__ void gemm_phase(LAS unsigned char* lds, const Gemm g, const Sched& S, const Epi& E, const Side side = Side()) {
;     ...
;         cur = nxt; cA = nA; cB = nB; ++ui;
;         if constexpr (ALIGN_EPI) { if (wr == 1) PG8_BAR; }
	s_andn2_b64 vcc, exec, s[0:1]
	s_cbranch_vccnz .LBB0_1721
	s_barrier
	s_branch .LBB0_1721
